# E18: E15 + adjacent s_setprio 0 / s_setprio 1 pairs removed from the middle of the 32-MFMA blocks of the five GEMM K-loops
# speedup vs baseline: 1.0010x; 1.0010x over previous
.LBB0_161:
	s_cmp_eq_u32 s56, 0
	s_cselect_b32 s22, s55, s54
	s_cselect_b32 s25, s36, s38
	s_cselect_b32 s26, s33, s37
	s_cselect_b32 s24, s54, s55
	s_cselect_b32 s30, s38, s36
	s_cselect_b32 s31, s37, s33
	s_ashr_i32 s23, s22, 31
	s_lshl_b64 s[22:23], s[22:23], 19
	s_add_u32 s22, s26, s22
	s_addc_u32 s23, s25, s23
	s_and_b64 s[26:27], s[4:5], exec
	s_cselect_b32 s28, s23, s1
	s_cselect_b32 s29, s22, s0
	s_ashr_i32 s25, s24, 31
	s_lshl_b64 s[24:25], s[24:25], 19
	s_add_u32 s24, s31, s24
	s_addc_u32 s25, s30, s25
	s_and_b64 s[26:27], s[4:5], exec
	s_cselect_b32 s30, s25, s7
	s_cselect_b32 s31, s24, s6
	s_add_u32 s0, s0, 0x40080
	s_addc_u32 s1, s1, 0
	s_add_u32 s34, s6, 0x100
	s_addc_u32 s35, s7, 0
	s_mov_b32 s59, -2
	s_nop 0
	ds_read_b128 v[130:133], v163
	ds_read_b128 v[134:137], v163 offset:1024
	ds_read_b128 v[138:141], v163 offset:2048
	ds_read_b128 v[142:145], v163 offset:3072
	ds_read_b128 v[184:187], v167
	ds_read_b128 v[188:191], v167 offset:1024
	ds_read_b128 v[192:195], v167 offset:2048
	ds_read_b128 v[196:199], v167 offset:3072
	s_add_u32 s6, s0, 0xfffc0080
	s_addc_u32 s7, s1, -1
	s_cmp_eq_u32 s59, 12
	s_cselect_b32 s27, s28, s7
	s_cselect_b32 s26, s29, s6
	s_cselect_b32 s7, s30, s35
	s_cselect_b32 s6, s31, s34
	v_lshl_add_u64 v[224:225], s[0:1], 0, v[176:177]
	s_add_i32 m0, s40, 0xc000
	ds_read_b128 v[200:203], v171
	ds_read_b128 v[204:207], v171 offset:1024
	ds_read_b128 v[208:211], v171 offset:2048
	ds_read_b128 v[212:215], v171 offset:3072
	ds_read_b128 v[216:219], v171 offset:4096
	ds_read_b128 v[220:223], v171 offset:5120
	ds_read_b128 v[228:231], v171 offset:6144
	ds_read_b128 v[232:235], v171 offset:7168
	global_load_lds_dwordx4 v[224:225], off
	v_lshl_add_u64 v[224:225], s[0:1], 0, v[178:179]
	s_add_i32 m0, s40, 0xe000
	s_nop 0
	global_load_lds_dwordx4 v[224:225], off
	s_waitcnt vmcnt(8)
	s_waitcnt lgkmcnt(0)
	s_barrier
	s_setprio 1
	s_waitcnt lgkmcnt(0)
	v_mfma_i32_16x16x64_i8 v[126:129], v[130:133], v[200:203], 0
	v_mfma_i32_16x16x64_i8 v[122:125], v[138:141], v[200:203], 0
	v_mfma_i32_16x16x64_i8 v[110:113], v[130:133], v[208:211], 0
	v_mfma_i32_16x16x64_i8 v[106:109], v[138:141], v[208:211], 0
	v_mfma_i32_16x16x64_i8 v[94:97], v[130:133], v[216:219], 0
	v_mfma_i32_16x16x64_i8 v[90:93], v[138:141], v[216:219], 0
	v_mfma_i32_16x16x64_i8 v[78:81], v[130:133], v[228:231], 0
	v_mfma_i32_16x16x64_i8 v[74:77], v[138:141], v[228:231], 0
	v_mfma_i32_16x16x64_i8 v[126:129], v[134:137], v[204:207], v[126:129]
	v_mfma_i32_16x16x64_i8 v[122:125], v[142:145], v[204:207], v[122:125]
	v_mfma_i32_16x16x64_i8 v[110:113], v[134:137], v[212:215], v[110:113]
	v_mfma_i32_16x16x64_i8 v[106:109], v[142:145], v[212:215], v[106:109]
	v_mfma_i32_16x16x64_i8 v[94:97], v[134:137], v[220:223], v[94:97]
	v_mfma_i32_16x16x64_i8 v[90:93], v[142:145], v[220:223], v[90:93]
	v_mfma_i32_16x16x64_i8 v[78:81], v[134:137], v[232:235], v[78:81]
	v_mfma_i32_16x16x64_i8 v[74:77], v[142:145], v[232:235], v[74:77]
	v_mfma_i32_16x16x64_i8 v[118:121], v[184:187], v[200:203], 0
	v_mfma_i32_16x16x64_i8 v[114:117], v[192:195], v[200:203], 0
	v_mfma_i32_16x16x64_i8 v[102:105], v[184:187], v[208:211], 0
	v_mfma_i32_16x16x64_i8 v[98:101], v[192:195], v[208:211], 0
	v_mfma_i32_16x16x64_i8 v[86:89], v[184:187], v[216:219], 0
	v_mfma_i32_16x16x64_i8 v[82:85], v[192:195], v[216:219], 0
	v_mfma_i32_16x16x64_i8 v[70:73], v[184:187], v[228:231], 0
	v_mfma_i32_16x16x64_i8 v[66:69], v[192:195], v[228:231], 0
	v_mfma_i32_16x16x64_i8 v[118:121], v[188:191], v[204:207], v[118:121]
	v_mfma_i32_16x16x64_i8 v[114:117], v[196:199], v[204:207], v[114:117]
	v_mfma_i32_16x16x64_i8 v[102:105], v[188:191], v[212:215], v[102:105]
	v_mfma_i32_16x16x64_i8 v[98:101], v[196:199], v[212:215], v[98:101]
	v_mfma_i32_16x16x64_i8 v[86:89], v[188:191], v[220:223], v[86:89]
	v_mfma_i32_16x16x64_i8 v[82:85], v[196:199], v[220:223], v[82:85]
	v_mfma_i32_16x16x64_i8 v[70:73], v[188:191], v[232:235], v[70:73]
	v_mfma_i32_16x16x64_i8 v[66:69], v[196:199], v[232:235], v[66:69]
	s_setprio 0
	s_barrier
	s_add_i32 s60, s51, s39
	v_lshl_add_u64 v[224:225], s[6:7], 0, v[148:149]
	s_mov_b32 m0, s60
	ds_read_b128 v[200:203], v171 offset:16384
	ds_read_b128 v[204:207], v171 offset:17408
	ds_read_b128 v[208:211], v171 offset:18432
	ds_read_b128 v[212:215], v171 offset:19456
	ds_read_b128 v[216:219], v171 offset:20480
	ds_read_b128 v[220:223], v171 offset:21504
	ds_read_b128 v[228:231], v171 offset:22528
	ds_read_b128 v[232:235], v171 offset:23552
	global_load_lds_dwordx4 v[224:225], off
	s_add_i32 m0, s60, 0x2000
	s_add_u32 s60, s6, 0x40000
	v_lshl_add_u64 v[236:237], s[6:7], 0, v[152:153]
	s_addc_u32 s61, s7, 0
	s_add_i32 s62, s52, s39
	global_load_lds_dwordx4 v[236:237], off
	v_lshl_add_u64 v[238:239], s[60:61], 0, v[148:149]
	s_mov_b32 m0, s62
	v_lshl_add_u64 v[240:241], s[26:27], 0, v[150:151]
	global_load_lds_dwordx4 v[238:239], off
	v_lshl_add_u64 v[238:239], s[60:61], 0, v[152:153]
	s_add_i32 m0, s62, 0x2000
	s_nop 0
	global_load_lds_dwordx4 v[238:239], off
	v_lshl_add_u64 v[238:239], s[26:27], 0, v[146:147]
	s_mov_b32 m0, s40
	s_nop 0
	global_load_lds_dwordx4 v[238:239], off
	s_mov_b32 m0, s41
	s_nop 0
	global_load_lds_dwordx4 v[240:241], off
	s_waitcnt vmcnt(8)
	s_waitcnt lgkmcnt(0)
	s_barrier
	s_setprio 1
	s_waitcnt lgkmcnt(0)
	v_mfma_i32_16x16x64_i8 v[62:65], v[130:133], v[200:203], 0
	v_mfma_i32_16x16x64_i8 v[58:61], v[138:141], v[200:203], 0
	v_mfma_i32_16x16x64_i8 v[46:49], v[130:133], v[208:211], 0
	v_mfma_i32_16x16x64_i8 v[42:45], v[138:141], v[208:211], 0
	v_mfma_i32_16x16x64_i8 v[30:33], v[130:133], v[216:219], 0
	v_mfma_i32_16x16x64_i8 v[26:29], v[138:141], v[216:219], 0
	v_mfma_i32_16x16x64_i8 v[14:17], v[130:133], v[228:231], 0
	v_mfma_i32_16x16x64_i8 v[10:13], v[138:141], v[228:231], 0
	v_mfma_i32_16x16x64_i8 v[62:65], v[134:137], v[204:207], v[62:65]
	v_mfma_i32_16x16x64_i8 v[58:61], v[142:145], v[204:207], v[58:61]
	v_mfma_i32_16x16x64_i8 v[46:49], v[134:137], v[212:215], v[46:49]
	v_mfma_i32_16x16x64_i8 v[42:45], v[142:145], v[212:215], v[42:45]
	v_mfma_i32_16x16x64_i8 v[30:33], v[134:137], v[220:223], v[30:33]
	v_mfma_i32_16x16x64_i8 v[26:29], v[142:145], v[220:223], v[26:29]
	v_mfma_i32_16x16x64_i8 v[14:17], v[134:137], v[232:235], v[14:17]
	v_mfma_i32_16x16x64_i8 v[10:13], v[142:145], v[232:235], v[10:13]
	v_mfma_i32_16x16x64_i8 v[54:57], v[184:187], v[200:203], 0
	v_mfma_i32_16x16x64_i8 v[50:53], v[192:195], v[200:203], 0
	v_mfma_i32_16x16x64_i8 v[38:41], v[184:187], v[208:211], 0
	v_mfma_i32_16x16x64_i8 v[34:37], v[192:195], v[208:211], 0
	v_mfma_i32_16x16x64_i8 v[22:25], v[184:187], v[216:219], 0
	v_mfma_i32_16x16x64_i8 v[18:21], v[192:195], v[216:219], 0
	v_mfma_i32_16x16x64_i8 v[6:9], v[184:187], v[228:231], 0
	v_mfma_i32_16x16x64_i8 v[2:5], v[192:195], v[228:231], 0
	v_mfma_i32_16x16x64_i8 v[54:57], v[188:191], v[204:207], v[54:57]
	v_mfma_i32_16x16x64_i8 v[50:53], v[196:199], v[204:207], v[50:53]
	v_mfma_i32_16x16x64_i8 v[38:41], v[188:191], v[212:215], v[38:41]
	v_mfma_i32_16x16x64_i8 v[34:37], v[196:199], v[212:215], v[34:37]
	v_mfma_i32_16x16x64_i8 v[22:25], v[188:191], v[220:223], v[22:25]
	v_mfma_i32_16x16x64_i8 v[18:21], v[196:199], v[220:223], v[18:21]
	v_mfma_i32_16x16x64_i8 v[6:9], v[188:191], v[232:235], v[6:9]
	v_mfma_i32_16x16x64_i8 v[2:5], v[196:199], v[232:235], v[2:5]
	s_setprio 0
	s_barrier
	s_add_i32 s60, 0, 0x18000
	v_add_u32_e32 v0, s60, v159
	s_add_i32 s61, 0, 0x1c000
	ds_read_b128 v[130:133], v0
	ds_read_b128 v[134:137], v0 offset:1024
	ds_read_b128 v[138:141], v0 offset:2048
	ds_read_b128 v[142:145], v0 offset:3072
	v_add_u32_e32 v0, s61, v159
	ds_read_b128 v[184:187], v0
	ds_read_b128 v[188:191], v0 offset:1024
	ds_read_b128 v[192:195], v0 offset:2048
	ds_read_b128 v[196:199], v0 offset:3072
	s_add_u32 s26, s26, 0x40000
	s_addc_u32 s27, s27, 0
	s_mov_b32 m0, s42
	v_lshl_add_u64 v[242:243], s[26:27], 0, v[146:147]
	ds_read_b128 v[200:203], v171 offset:32768
	ds_read_b128 v[204:207], v171 offset:33792
	ds_read_b128 v[208:211], v171 offset:34816
	ds_read_b128 v[212:215], v171 offset:35840
	ds_read_b128 v[216:219], v171 offset:36864
	ds_read_b128 v[220:223], v171 offset:37888
	ds_read_b128 v[228:231], v171 offset:38912
	ds_read_b128 v[232:235], v171 offset:39936
	global_load_lds_dwordx4 v[242:243], off
	v_lshl_add_u64 v[242:243], s[26:27], 0, v[150:151]
	s_mov_b32 m0, s43
	s_nop 0
	global_load_lds_dwordx4 v[242:243], off
	s_waitcnt vmcnt(8)
	s_waitcnt lgkmcnt(0)
	s_barrier
	s_setprio 1
	s_waitcnt lgkmcnt(0)
	v_mfma_i32_16x16x64_i8 v[126:129], v[130:133], v[200:203], v[126:129]
	v_mfma_i32_16x16x64_i8 v[122:125], v[138:141], v[200:203], v[122:125]
	v_mfma_i32_16x16x64_i8 v[110:113], v[130:133], v[208:211], v[110:113]
	v_mfma_i32_16x16x64_i8 v[106:109], v[138:141], v[208:211], v[106:109]
	v_mfma_i32_16x16x64_i8 v[94:97], v[130:133], v[216:219], v[94:97]
	v_mfma_i32_16x16x64_i8 v[90:93], v[138:141], v[216:219], v[90:93]
	v_mfma_i32_16x16x64_i8 v[78:81], v[130:133], v[228:231], v[78:81]
	v_mfma_i32_16x16x64_i8 v[74:77], v[138:141], v[228:231], v[74:77]
	v_mfma_i32_16x16x64_i8 v[126:129], v[134:137], v[204:207], v[126:129]
	v_mfma_i32_16x16x64_i8 v[122:125], v[142:145], v[204:207], v[122:125]
	v_mfma_i32_16x16x64_i8 v[110:113], v[134:137], v[212:215], v[110:113]
	v_mfma_i32_16x16x64_i8 v[106:109], v[142:145], v[212:215], v[106:109]
	v_mfma_i32_16x16x64_i8 v[94:97], v[134:137], v[220:223], v[94:97]
	v_mfma_i32_16x16x64_i8 v[90:93], v[142:145], v[220:223], v[90:93]
	v_mfma_i32_16x16x64_i8 v[78:81], v[134:137], v[232:235], v[78:81]
	v_mfma_i32_16x16x64_i8 v[74:77], v[142:145], v[232:235], v[74:77]
	v_mfma_i32_16x16x64_i8 v[118:121], v[184:187], v[200:203], v[118:121]
	v_mfma_i32_16x16x64_i8 v[114:117], v[192:195], v[200:203], v[114:117]
	v_mfma_i32_16x16x64_i8 v[102:105], v[184:187], v[208:211], v[102:105]
	v_mfma_i32_16x16x64_i8 v[98:101], v[192:195], v[208:211], v[98:101]
	v_mfma_i32_16x16x64_i8 v[86:89], v[184:187], v[216:219], v[86:89]
	v_mfma_i32_16x16x64_i8 v[82:85], v[192:195], v[216:219], v[82:85]
	v_mfma_i32_16x16x64_i8 v[70:73], v[184:187], v[228:231], v[70:73]
	v_mfma_i32_16x16x64_i8 v[66:69], v[192:195], v[228:231], v[66:69]
	v_mfma_i32_16x16x64_i8 v[118:121], v[188:191], v[204:207], v[118:121]
	v_mfma_i32_16x16x64_i8 v[114:117], v[196:199], v[204:207], v[114:117]
	v_mfma_i32_16x16x64_i8 v[102:105], v[188:191], v[212:215], v[102:105]
	v_mfma_i32_16x16x64_i8 v[98:101], v[196:199], v[212:215], v[98:101]
	v_mfma_i32_16x16x64_i8 v[86:89], v[188:191], v[220:223], v[86:89]
	v_mfma_i32_16x16x64_i8 v[82:85], v[196:199], v[220:223], v[82:85]
	v_mfma_i32_16x16x64_i8 v[70:73], v[188:191], v[232:235], v[70:73]
	v_mfma_i32_16x16x64_i8 v[66:69], v[196:199], v[232:235], v[66:69]
	s_setprio 0
	s_barrier
	s_add_i32 s26, s60, s39
	v_lshl_add_u64 v[224:225], v[224:225], 0, s[12:13]
	s_mov_b32 m0, s26
	ds_read_b128 v[200:203], v171 offset:49152
	ds_read_b128 v[204:207], v171 offset:50176
	ds_read_b128 v[208:211], v171 offset:51200
	ds_read_b128 v[212:215], v171 offset:52224
	ds_read_b128 v[216:219], v171 offset:53248
	ds_read_b128 v[220:223], v171 offset:54272
	ds_read_b128 v[228:231], v171 offset:55296
	ds_read_b128 v[232:235], v171 offset:56320
	global_load_lds_dwordx4 v[224:225], off
	s_add_i32 m0, s26, 0x2000
	s_add_u32 s6, s6, 0x40080
	v_lshl_add_u64 v[224:225], v[236:237], 0, s[12:13]
	s_addc_u32 s7, s7, 0
	s_add_i32 s26, s61, s39
	global_load_lds_dwordx4 v[224:225], off
	v_lshl_add_u64 v[224:225], s[6:7], 0, v[148:149]
	s_mov_b32 m0, s26
	s_nop 0
	global_load_lds_dwordx4 v[224:225], off
	v_lshl_add_u64 v[224:225], s[6:7], 0, v[152:153]
	s_add_i32 m0, s26, 0x2000
	s_nop 0
	global_load_lds_dwordx4 v[224:225], off
	v_lshl_add_u64 v[224:225], v[238:239], 0, s[12:13]
	s_mov_b32 m0, s45
	s_nop 0
	global_load_lds_dwordx4 v[224:225], off
	v_lshl_add_u64 v[224:225], v[240:241], 0, s[12:13]
	s_mov_b32 m0, s46
	s_nop 0
	global_load_lds_dwordx4 v[224:225], off
	s_waitcnt vmcnt(8)
	s_waitcnt lgkmcnt(0)
	s_barrier
	s_setprio 1
	s_waitcnt lgkmcnt(0)
	v_mfma_i32_16x16x64_i8 v[62:65], v[130:133], v[200:203], v[62:65]
	v_mfma_i32_16x16x64_i8 v[58:61], v[138:141], v[200:203], v[58:61]
	v_mfma_i32_16x16x64_i8 v[46:49], v[130:133], v[208:211], v[46:49]
	v_mfma_i32_16x16x64_i8 v[42:45], v[138:141], v[208:211], v[42:45]
	v_mfma_i32_16x16x64_i8 v[30:33], v[130:133], v[216:219], v[30:33]
	v_mfma_i32_16x16x64_i8 v[26:29], v[138:141], v[216:219], v[26:29]
	v_mfma_i32_16x16x64_i8 v[14:17], v[130:133], v[228:231], v[14:17]
	v_mfma_i32_16x16x64_i8 v[10:13], v[138:141], v[228:231], v[10:13]
	v_mfma_i32_16x16x64_i8 v[62:65], v[134:137], v[204:207], v[62:65]
	v_mfma_i32_16x16x64_i8 v[58:61], v[142:145], v[204:207], v[58:61]
	v_mfma_i32_16x16x64_i8 v[46:49], v[134:137], v[212:215], v[46:49]
	v_mfma_i32_16x16x64_i8 v[42:45], v[142:145], v[212:215], v[42:45]
	v_mfma_i32_16x16x64_i8 v[30:33], v[134:137], v[220:223], v[30:33]
	v_mfma_i32_16x16x64_i8 v[26:29], v[142:145], v[220:223], v[26:29]
	v_mfma_i32_16x16x64_i8 v[14:17], v[134:137], v[232:235], v[14:17]
	v_mfma_i32_16x16x64_i8 v[10:13], v[142:145], v[232:235], v[10:13]
	v_mfma_i32_16x16x64_i8 v[54:57], v[184:187], v[200:203], v[54:57]
	v_mfma_i32_16x16x64_i8 v[50:53], v[192:195], v[200:203], v[50:53]
	v_mfma_i32_16x16x64_i8 v[38:41], v[184:187], v[208:211], v[38:41]
	v_mfma_i32_16x16x64_i8 v[34:37], v[192:195], v[208:211], v[34:37]
	v_mfma_i32_16x16x64_i8 v[22:25], v[184:187], v[216:219], v[22:25]
	v_mfma_i32_16x16x64_i8 v[18:21], v[192:195], v[216:219], v[18:21]
	v_mfma_i32_16x16x64_i8 v[6:9], v[184:187], v[228:231], v[6:9]
	v_mfma_i32_16x16x64_i8 v[2:5], v[192:195], v[228:231], v[2:5]
	v_mfma_i32_16x16x64_i8 v[54:57], v[188:191], v[204:207], v[54:57]
	v_mfma_i32_16x16x64_i8 v[50:53], v[196:199], v[204:207], v[50:53]
	v_mfma_i32_16x16x64_i8 v[38:41], v[188:191], v[212:215], v[38:41]
	v_mfma_i32_16x16x64_i8 v[34:37], v[196:199], v[212:215], v[34:37]
	v_mfma_i32_16x16x64_i8 v[22:25], v[188:191], v[220:223], v[22:25]
	v_mfma_i32_16x16x64_i8 v[18:21], v[196:199], v[220:223], v[18:21]
	v_mfma_i32_16x16x64_i8 v[6:9], v[188:191], v[232:235], v[6:9]
	v_mfma_i32_16x16x64_i8 v[2:5], v[196:199], v[232:235], v[2:5]
	s_setprio 0
	s_barrier
	s_add_i32 s59, s59, 2
	s_add_u32 s0, s0, 0x100
	s_addc_u32 s1, s1, 0
	s_add_u32 s34, s34, 0x100
	s_addc_u32 s35, s35, 0
	s_cmp_gt_u32 s59, 13
	s_cbranch_scc0 .LBB0_162
	s_branch .Lkexit_162
	s_nop 0
	s_nop 0
	s_nop 0
	s_nop 0
	s_nop 0
	s_nop 0
	s_nop 0
	s_nop 0
	s_nop 0
	s_nop 0
	s_nop 0
	s_nop 0
	s_nop 0
	s_nop 0
	s_nop 0
	s_nop 0
.LBB0_162:
	ds_read_b128 v[130:133], v163
	ds_read_b128 v[134:137], v163 offset:1024
	ds_read_b128 v[138:141], v163 offset:2048
	ds_read_b128 v[142:145], v163 offset:3072
	ds_read_b128 v[184:187], v167
	ds_read_b128 v[188:191], v167 offset:1024
	ds_read_b128 v[192:195], v167 offset:2048
	ds_read_b128 v[196:199], v167 offset:3072
	s_add_u32 s6, s0, 0xfffc0080
	s_addc_u32 s7, s1, -1
	s_cmp_eq_u32 s59, 12
	s_cselect_b32 s27, s28, s7
	s_cselect_b32 s26, s29, s6
	s_cselect_b32 s7, s30, s35
	s_cselect_b32 s6, s31, s34
	v_lshl_add_u64 v[224:225], s[0:1], 0, v[176:177]
	s_add_i32 m0, s40, 0xc000
	ds_read_b128 v[200:203], v171
	ds_read_b128 v[204:207], v171 offset:1024
	ds_read_b128 v[208:211], v171 offset:2048
	ds_read_b128 v[212:215], v171 offset:3072
	ds_read_b128 v[216:219], v171 offset:4096
	ds_read_b128 v[220:223], v171 offset:5120
	ds_read_b128 v[228:231], v171 offset:6144
	ds_read_b128 v[232:235], v171 offset:7168
	global_load_lds_dwordx4 v[224:225], off
	v_lshl_add_u64 v[224:225], s[0:1], 0, v[178:179]
	s_add_i32 m0, s40, 0xe000
	s_nop 0
	global_load_lds_dwordx4 v[224:225], off
	s_waitcnt vmcnt(8)
	s_waitcnt lgkmcnt(0)
	s_barrier
	s_setprio 1
	s_waitcnt lgkmcnt(0)
	v_mfma_i32_16x16x64_i8 v[126:129], v[130:133], v[200:203], v[126:129]
	v_mfma_i32_16x16x64_i8 v[122:125], v[138:141], v[200:203], v[122:125]
	v_mfma_i32_16x16x64_i8 v[110:113], v[130:133], v[208:211], v[110:113]
	v_mfma_i32_16x16x64_i8 v[106:109], v[138:141], v[208:211], v[106:109]
	v_mfma_i32_16x16x64_i8 v[94:97], v[130:133], v[216:219], v[94:97]
	v_mfma_i32_16x16x64_i8 v[90:93], v[138:141], v[216:219], v[90:93]
	v_mfma_i32_16x16x64_i8 v[78:81], v[130:133], v[228:231], v[78:81]
	v_mfma_i32_16x16x64_i8 v[74:77], v[138:141], v[228:231], v[74:77]
	v_mfma_i32_16x16x64_i8 v[126:129], v[134:137], v[204:207], v[126:129]
	v_mfma_i32_16x16x64_i8 v[122:125], v[142:145], v[204:207], v[122:125]
	v_mfma_i32_16x16x64_i8 v[110:113], v[134:137], v[212:215], v[110:113]
	v_mfma_i32_16x16x64_i8 v[106:109], v[142:145], v[212:215], v[106:109]
	v_mfma_i32_16x16x64_i8 v[94:97], v[134:137], v[220:223], v[94:97]
	v_mfma_i32_16x16x64_i8 v[90:93], v[142:145], v[220:223], v[90:93]
	v_mfma_i32_16x16x64_i8 v[78:81], v[134:137], v[232:235], v[78:81]
	v_mfma_i32_16x16x64_i8 v[74:77], v[142:145], v[232:235], v[74:77]
	v_mfma_i32_16x16x64_i8 v[118:121], v[184:187], v[200:203], v[118:121]
	v_mfma_i32_16x16x64_i8 v[114:117], v[192:195], v[200:203], v[114:117]
	v_mfma_i32_16x16x64_i8 v[102:105], v[184:187], v[208:211], v[102:105]
	v_mfma_i32_16x16x64_i8 v[98:101], v[192:195], v[208:211], v[98:101]
	v_mfma_i32_16x16x64_i8 v[86:89], v[184:187], v[216:219], v[86:89]
	v_mfma_i32_16x16x64_i8 v[82:85], v[192:195], v[216:219], v[82:85]
	v_mfma_i32_16x16x64_i8 v[70:73], v[184:187], v[228:231], v[70:73]
	v_mfma_i32_16x16x64_i8 v[66:69], v[192:195], v[228:231], v[66:69]
	v_mfma_i32_16x16x64_i8 v[118:121], v[188:191], v[204:207], v[118:121]
	v_mfma_i32_16x16x64_i8 v[114:117], v[196:199], v[204:207], v[114:117]
	v_mfma_i32_16x16x64_i8 v[102:105], v[188:191], v[212:215], v[102:105]
	v_mfma_i32_16x16x64_i8 v[98:101], v[196:199], v[212:215], v[98:101]
	v_mfma_i32_16x16x64_i8 v[86:89], v[188:191], v[220:223], v[86:89]
	v_mfma_i32_16x16x64_i8 v[82:85], v[196:199], v[220:223], v[82:85]
	v_mfma_i32_16x16x64_i8 v[70:73], v[188:191], v[232:235], v[70:73]
	v_mfma_i32_16x16x64_i8 v[66:69], v[196:199], v[232:235], v[66:69]
	s_setprio 0
	s_barrier
	s_add_i32 s60, s51, s39
	v_lshl_add_u64 v[224:225], s[6:7], 0, v[148:149]
	s_mov_b32 m0, s60
	ds_read_b128 v[200:203], v171 offset:16384
	ds_read_b128 v[204:207], v171 offset:17408
	ds_read_b128 v[208:211], v171 offset:18432
	ds_read_b128 v[212:215], v171 offset:19456
	ds_read_b128 v[216:219], v171 offset:20480
	ds_read_b128 v[220:223], v171 offset:21504
	ds_read_b128 v[228:231], v171 offset:22528
	ds_read_b128 v[232:235], v171 offset:23552
	global_load_lds_dwordx4 v[224:225], off
	s_add_i32 m0, s60, 0x2000
	s_add_u32 s60, s6, 0x40000
	v_lshl_add_u64 v[236:237], s[6:7], 0, v[152:153]
	s_addc_u32 s61, s7, 0
	s_add_i32 s62, s52, s39
	global_load_lds_dwordx4 v[236:237], off
	v_lshl_add_u64 v[238:239], s[60:61], 0, v[148:149]
	s_mov_b32 m0, s62
	v_lshl_add_u64 v[240:241], s[26:27], 0, v[150:151]
	global_load_lds_dwordx4 v[238:239], off
	v_lshl_add_u64 v[238:239], s[60:61], 0, v[152:153]
	s_add_i32 m0, s62, 0x2000
	s_nop 0
	global_load_lds_dwordx4 v[238:239], off
	v_lshl_add_u64 v[238:239], s[26:27], 0, v[146:147]
	s_mov_b32 m0, s40
	s_nop 0
	global_load_lds_dwordx4 v[238:239], off
	s_mov_b32 m0, s41
	s_nop 0
	global_load_lds_dwordx4 v[240:241], off
	s_waitcnt vmcnt(8)
	s_waitcnt lgkmcnt(0)
	s_barrier
	s_setprio 1
	s_waitcnt lgkmcnt(0)
	v_mfma_i32_16x16x64_i8 v[62:65], v[130:133], v[200:203], v[62:65]
	v_mfma_i32_16x16x64_i8 v[58:61], v[138:141], v[200:203], v[58:61]
	v_mfma_i32_16x16x64_i8 v[46:49], v[130:133], v[208:211], v[46:49]
	v_mfma_i32_16x16x64_i8 v[42:45], v[138:141], v[208:211], v[42:45]
	v_mfma_i32_16x16x64_i8 v[30:33], v[130:133], v[216:219], v[30:33]
	v_mfma_i32_16x16x64_i8 v[26:29], v[138:141], v[216:219], v[26:29]
	v_mfma_i32_16x16x64_i8 v[14:17], v[130:133], v[228:231], v[14:17]
	v_mfma_i32_16x16x64_i8 v[10:13], v[138:141], v[228:231], v[10:13]
	v_mfma_i32_16x16x64_i8 v[62:65], v[134:137], v[204:207], v[62:65]
	v_mfma_i32_16x16x64_i8 v[58:61], v[142:145], v[204:207], v[58:61]
	v_mfma_i32_16x16x64_i8 v[46:49], v[134:137], v[212:215], v[46:49]
	v_mfma_i32_16x16x64_i8 v[42:45], v[142:145], v[212:215], v[42:45]
	v_mfma_i32_16x16x64_i8 v[30:33], v[134:137], v[220:223], v[30:33]
	v_mfma_i32_16x16x64_i8 v[26:29], v[142:145], v[220:223], v[26:29]
	v_mfma_i32_16x16x64_i8 v[14:17], v[134:137], v[232:235], v[14:17]
	v_mfma_i32_16x16x64_i8 v[10:13], v[142:145], v[232:235], v[10:13]
	v_mfma_i32_16x16x64_i8 v[54:57], v[184:187], v[200:203], v[54:57]
	v_mfma_i32_16x16x64_i8 v[50:53], v[192:195], v[200:203], v[50:53]
	v_mfma_i32_16x16x64_i8 v[38:41], v[184:187], v[208:211], v[38:41]
	v_mfma_i32_16x16x64_i8 v[34:37], v[192:195], v[208:211], v[34:37]
	v_mfma_i32_16x16x64_i8 v[22:25], v[184:187], v[216:219], v[22:25]
	v_mfma_i32_16x16x64_i8 v[18:21], v[192:195], v[216:219], v[18:21]
	v_mfma_i32_16x16x64_i8 v[6:9], v[184:187], v[228:231], v[6:9]
	v_mfma_i32_16x16x64_i8 v[2:5], v[192:195], v[228:231], v[2:5]
	v_mfma_i32_16x16x64_i8 v[54:57], v[188:191], v[204:207], v[54:57]
	v_mfma_i32_16x16x64_i8 v[50:53], v[196:199], v[204:207], v[50:53]
	v_mfma_i32_16x16x64_i8 v[38:41], v[188:191], v[212:215], v[38:41]
	v_mfma_i32_16x16x64_i8 v[34:37], v[196:199], v[212:215], v[34:37]
	v_mfma_i32_16x16x64_i8 v[22:25], v[188:191], v[220:223], v[22:25]
	v_mfma_i32_16x16x64_i8 v[18:21], v[196:199], v[220:223], v[18:21]
	v_mfma_i32_16x16x64_i8 v[6:9], v[188:191], v[232:235], v[6:9]
	v_mfma_i32_16x16x64_i8 v[2:5], v[196:199], v[232:235], v[2:5]
	s_setprio 0
	s_barrier
	s_add_i32 s60, 0, 0x18000
	v_add_u32_e32 v0, s60, v159
	s_add_i32 s61, 0, 0x1c000
	ds_read_b128 v[130:133], v0
	ds_read_b128 v[134:137], v0 offset:1024
	ds_read_b128 v[138:141], v0 offset:2048
	ds_read_b128 v[142:145], v0 offset:3072
	v_add_u32_e32 v0, s61, v159
	ds_read_b128 v[184:187], v0
	ds_read_b128 v[188:191], v0 offset:1024
	ds_read_b128 v[192:195], v0 offset:2048
	ds_read_b128 v[196:199], v0 offset:3072
	s_add_u32 s26, s26, 0x40000
	s_addc_u32 s27, s27, 0
	s_mov_b32 m0, s42
	v_lshl_add_u64 v[242:243], s[26:27], 0, v[146:147]
	ds_read_b128 v[200:203], v171 offset:32768
	ds_read_b128 v[204:207], v171 offset:33792
	ds_read_b128 v[208:211], v171 offset:34816
	ds_read_b128 v[212:215], v171 offset:35840
	ds_read_b128 v[216:219], v171 offset:36864
	ds_read_b128 v[220:223], v171 offset:37888
	ds_read_b128 v[228:231], v171 offset:38912
	ds_read_b128 v[232:235], v171 offset:39936
	global_load_lds_dwordx4 v[242:243], off
	v_lshl_add_u64 v[242:243], s[26:27], 0, v[150:151]
	s_mov_b32 m0, s43
	s_nop 0
	global_load_lds_dwordx4 v[242:243], off
	s_waitcnt vmcnt(8)
	s_waitcnt lgkmcnt(0)
	s_barrier
	s_setprio 1
	s_waitcnt lgkmcnt(0)
	v_mfma_i32_16x16x64_i8 v[126:129], v[130:133], v[200:203], v[126:129]
	v_mfma_i32_16x16x64_i8 v[122:125], v[138:141], v[200:203], v[122:125]
	v_mfma_i32_16x16x64_i8 v[110:113], v[130:133], v[208:211], v[110:113]
	v_mfma_i32_16x16x64_i8 v[106:109], v[138:141], v[208:211], v[106:109]
	v_mfma_i32_16x16x64_i8 v[94:97], v[130:133], v[216:219], v[94:97]
	v_mfma_i32_16x16x64_i8 v[90:93], v[138:141], v[216:219], v[90:93]
	v_mfma_i32_16x16x64_i8 v[78:81], v[130:133], v[228:231], v[78:81]
	v_mfma_i32_16x16x64_i8 v[74:77], v[138:141], v[228:231], v[74:77]
	v_mfma_i32_16x16x64_i8 v[126:129], v[134:137], v[204:207], v[126:129]
	v_mfma_i32_16x16x64_i8 v[122:125], v[142:145], v[204:207], v[122:125]
	v_mfma_i32_16x16x64_i8 v[110:113], v[134:137], v[212:215], v[110:113]
	v_mfma_i32_16x16x64_i8 v[106:109], v[142:145], v[212:215], v[106:109]
	v_mfma_i32_16x16x64_i8 v[94:97], v[134:137], v[220:223], v[94:97]
	v_mfma_i32_16x16x64_i8 v[90:93], v[142:145], v[220:223], v[90:93]
	v_mfma_i32_16x16x64_i8 v[78:81], v[134:137], v[232:235], v[78:81]
	v_mfma_i32_16x16x64_i8 v[74:77], v[142:145], v[232:235], v[74:77]
	v_mfma_i32_16x16x64_i8 v[118:121], v[184:187], v[200:203], v[118:121]
	v_mfma_i32_16x16x64_i8 v[114:117], v[192:195], v[200:203], v[114:117]
	v_mfma_i32_16x16x64_i8 v[102:105], v[184:187], v[208:211], v[102:105]
	v_mfma_i32_16x16x64_i8 v[98:101], v[192:195], v[208:211], v[98:101]
	v_mfma_i32_16x16x64_i8 v[86:89], v[184:187], v[216:219], v[86:89]
	v_mfma_i32_16x16x64_i8 v[82:85], v[192:195], v[216:219], v[82:85]
	v_mfma_i32_16x16x64_i8 v[70:73], v[184:187], v[228:231], v[70:73]
	v_mfma_i32_16x16x64_i8 v[66:69], v[192:195], v[228:231], v[66:69]
	v_mfma_i32_16x16x64_i8 v[118:121], v[188:191], v[204:207], v[118:121]
	v_mfma_i32_16x16x64_i8 v[114:117], v[196:199], v[204:207], v[114:117]
	v_mfma_i32_16x16x64_i8 v[102:105], v[188:191], v[212:215], v[102:105]
	v_mfma_i32_16x16x64_i8 v[98:101], v[196:199], v[212:215], v[98:101]
	v_mfma_i32_16x16x64_i8 v[86:89], v[188:191], v[220:223], v[86:89]
	v_mfma_i32_16x16x64_i8 v[82:85], v[196:199], v[220:223], v[82:85]
	v_mfma_i32_16x16x64_i8 v[70:73], v[188:191], v[232:235], v[70:73]
	v_mfma_i32_16x16x64_i8 v[66:69], v[196:199], v[232:235], v[66:69]
	s_setprio 0
	s_barrier
	s_add_i32 s26, s60, s39
	v_lshl_add_u64 v[224:225], v[224:225], 0, s[12:13]
	s_mov_b32 m0, s26
	ds_read_b128 v[200:203], v171 offset:49152
	ds_read_b128 v[204:207], v171 offset:50176
	ds_read_b128 v[208:211], v171 offset:51200
	ds_read_b128 v[212:215], v171 offset:52224
	ds_read_b128 v[216:219], v171 offset:53248
	ds_read_b128 v[220:223], v171 offset:54272
	ds_read_b128 v[228:231], v171 offset:55296
	ds_read_b128 v[232:235], v171 offset:56320
	global_load_lds_dwordx4 v[224:225], off
	s_add_i32 m0, s26, 0x2000
	s_add_u32 s6, s6, 0x40080
	v_lshl_add_u64 v[224:225], v[236:237], 0, s[12:13]
	s_addc_u32 s7, s7, 0
	s_add_i32 s26, s61, s39
	global_load_lds_dwordx4 v[224:225], off
	v_lshl_add_u64 v[224:225], s[6:7], 0, v[148:149]
	s_mov_b32 m0, s26
	s_nop 0
	global_load_lds_dwordx4 v[224:225], off
	v_lshl_add_u64 v[224:225], s[6:7], 0, v[152:153]
	s_add_i32 m0, s26, 0x2000
	s_nop 0
	global_load_lds_dwordx4 v[224:225], off
	v_lshl_add_u64 v[224:225], v[238:239], 0, s[12:13]
	s_mov_b32 m0, s45
	s_nop 0
	global_load_lds_dwordx4 v[224:225], off
	v_lshl_add_u64 v[224:225], v[240:241], 0, s[12:13]
	s_mov_b32 m0, s46
	s_nop 0
	global_load_lds_dwordx4 v[224:225], off
	s_waitcnt vmcnt(8)
	s_waitcnt lgkmcnt(0)
	s_barrier
	s_setprio 1
	s_waitcnt lgkmcnt(0)
	v_mfma_i32_16x16x64_i8 v[62:65], v[130:133], v[200:203], v[62:65]
	v_mfma_i32_16x16x64_i8 v[58:61], v[138:141], v[200:203], v[58:61]
	v_mfma_i32_16x16x64_i8 v[46:49], v[130:133], v[208:211], v[46:49]
	v_mfma_i32_16x16x64_i8 v[42:45], v[138:141], v[208:211], v[42:45]
	v_mfma_i32_16x16x64_i8 v[30:33], v[130:133], v[216:219], v[30:33]
	v_mfma_i32_16x16x64_i8 v[26:29], v[138:141], v[216:219], v[26:29]
	v_mfma_i32_16x16x64_i8 v[14:17], v[130:133], v[228:231], v[14:17]
	v_mfma_i32_16x16x64_i8 v[10:13], v[138:141], v[228:231], v[10:13]
	v_mfma_i32_16x16x64_i8 v[62:65], v[134:137], v[204:207], v[62:65]
	v_mfma_i32_16x16x64_i8 v[58:61], v[142:145], v[204:207], v[58:61]
	v_mfma_i32_16x16x64_i8 v[46:49], v[134:137], v[212:215], v[46:49]
	v_mfma_i32_16x16x64_i8 v[42:45], v[142:145], v[212:215], v[42:45]
	v_mfma_i32_16x16x64_i8 v[30:33], v[134:137], v[220:223], v[30:33]
	v_mfma_i32_16x16x64_i8 v[26:29], v[142:145], v[220:223], v[26:29]
	v_mfma_i32_16x16x64_i8 v[14:17], v[134:137], v[232:235], v[14:17]
	v_mfma_i32_16x16x64_i8 v[10:13], v[142:145], v[232:235], v[10:13]
	v_mfma_i32_16x16x64_i8 v[54:57], v[184:187], v[200:203], v[54:57]
	v_mfma_i32_16x16x64_i8 v[50:53], v[192:195], v[200:203], v[50:53]
	v_mfma_i32_16x16x64_i8 v[38:41], v[184:187], v[208:211], v[38:41]
	v_mfma_i32_16x16x64_i8 v[34:37], v[192:195], v[208:211], v[34:37]
	v_mfma_i32_16x16x64_i8 v[22:25], v[184:187], v[216:219], v[22:25]
	v_mfma_i32_16x16x64_i8 v[18:21], v[192:195], v[216:219], v[18:21]
	v_mfma_i32_16x16x64_i8 v[6:9], v[184:187], v[228:231], v[6:9]
	v_mfma_i32_16x16x64_i8 v[2:5], v[192:195], v[228:231], v[2:5]
	v_mfma_i32_16x16x64_i8 v[54:57], v[188:191], v[204:207], v[54:57]
	v_mfma_i32_16x16x64_i8 v[50:53], v[196:199], v[204:207], v[50:53]
	v_mfma_i32_16x16x64_i8 v[38:41], v[188:191], v[212:215], v[38:41]
	v_mfma_i32_16x16x64_i8 v[34:37], v[196:199], v[212:215], v[34:37]
	v_mfma_i32_16x16x64_i8 v[22:25], v[188:191], v[220:223], v[22:25]
	v_mfma_i32_16x16x64_i8 v[18:21], v[196:199], v[220:223], v[18:21]
	v_mfma_i32_16x16x64_i8 v[6:9], v[188:191], v[232:235], v[6:9]
	v_mfma_i32_16x16x64_i8 v[2:5], v[196:199], v[232:235], v[2:5]
	s_setprio 0
	s_barrier
	s_add_i32 s59, s59, 2
	s_add_u32 s0, s0, 0x100
	s_addc_u32 s1, s1, 0
	s_add_u32 s34, s34, 0x100
	s_addc_u32 s35, s35, 0
	s_cmp_gt_u32 s59, 13
	s_cbranch_scc0 .LBB0_162

.LBB0_165:
	s_cmp_lg_u32 s8, 0
	s_cbranch_scc0 .LBB0_167
	s_cmp_eq_u32 s58, 21
	s_mov_b32 s0, 0x4e490a00
	s_cselect_b32 s0, s0, 0x4f490a00
	s_lshl_b32 s1, s57, 8
	v_or_b32_e32 v130, s1, v158
	v_lshl_add_u32 v184, s58, 8, v156
	v_ashrrev_i32_e32 v131, 31, v130
	v_ashrrev_i32_e32 v185, 31, v184
	v_lshl_add_u64 v[130:131], v[130:131], 2, s[16:17]
	v_lshl_add_u64 v[186:187], v[184:185], 2, s[2:3]
	global_load_dword v192, v[186:187], off
	global_load_dwordx4 v[142:145], v[130:131], off
	global_load_dwordx4 v[138:141], v[130:131], off offset:16
	global_load_dwordx4 v[134:137], v[130:131], off offset:512
	s_nop 0
	global_load_dwordx4 v[130:133], v[130:131], off offset:528
	s_nop 0
	global_load_dword v194, v[186:187], off offset:64
	v_add_u32_e32 v184, 0x80, v184
	v_ashrrev_i32_e32 v185, 31, v184
	v_lshl_add_u64 v[184:185], v[184:185], 2, s[2:3]
	global_load_dword v222, v[186:187], off offset:128
	global_load_dword v200, v[186:187], off offset:192
	global_load_dword v196, v[184:185], off
	global_load_dword v188, v[184:185], off offset:64
	s_nop 0
	global_load_dword v186, v[184:185], off offset:128
	s_nop 0
	global_load_dword v184, v[184:185], off offset:192
	v_readlane_b32 s6, v252, 2
	v_readlane_b32 s7, v252, 3
	s_add_u32 s6, s6, s0
	v_cvt_f32_i32_e32 v203, v127
	v_cvt_f32_i32_e32 v202, v126
	v_cvt_f32_i32_e32 v205, v123
	v_cvt_f32_i32_e32 v204, v122
	v_cvt_f32_i32_e32 v207, v129
	v_cvt_f32_i32_e32 v206, v128
	v_cvt_f32_i32_e32 v209, v125
	v_cvt_f32_i32_e32 v208, v124
	v_cvt_f32_i32_e32 v217, v117
	v_cvt_f32_i32_e32 v216, v116
	s_addc_u32 s7, s7, 0
	s_ashr_i32 s8, s57, 3
	v_cvt_f32_i32_e32 v211, v119
	v_cvt_f32_i32_e32 v210, v118
	v_cvt_f32_i32_e32 v213, v115
	v_cvt_f32_i32_e32 v212, v114
	v_cvt_f32_i32_e32 v215, v121
	v_cvt_f32_i32_e32 v214, v120
	s_and_b32 s1, s1, 0xf00
	s_and_b32 s0, s8, -2
	v_or_b32_e32 v0, s1, v157
	s_ashr_i32 s1, s0, 31
	v_lshl_add_u64 v[198:199], s[6:7], 0, v[160:161]
	s_lshl_b64 s[0:1], s[0:1], 20
	v_lshlrev_b32_e32 v154, 1, v0
	v_lshl_add_u64 v[224:225], v[198:199], 0, s[0:1]
	v_lshl_add_u64 v[224:225], v[224:225], 0, v[154:155]
	v_cvt_f32_i32_e32 v219, v111
	v_cvt_f32_i32_e32 v218, v110
	v_cvt_f32_i32_e32 v221, v107
	v_cvt_f32_i32_e32 v220, v106
	v_lshl_add_u64 v[190:191], s[6:7], 0, v[164:165]
	s_waitcnt vmcnt(0)
	v_pk_mul_f32 v[228:229], v[142:143], v[192:193] op_sel_hi:[1,0]
	v_pk_mul_f32 v[230:231], v[138:139], v[192:193] op_sel_hi:[1,0]
	v_pk_mul_f32 v[232:233], v[144:145], v[192:193] op_sel_hi:[1,0]
	v_pk_mul_f32 v[234:235], v[140:141], v[192:193] op_sel_hi:[1,0]
	v_pk_mul_f32 v[236:237], v[134:135], v[192:193] op_sel_hi:[1,0]
	v_pk_mul_f32 v[238:239], v[192:193], v[130:131] op_sel_hi:[0,1]
	v_pk_mul_f32 v[240:241], v[136:137], v[192:193] op_sel_hi:[1,0]
	v_pk_mul_f32 v[192:193], v[192:193], v[132:133] op_sel_hi:[0,1]
	v_pk_mul_f32 v[202:203], v[228:229], v[202:203]
	v_pk_mul_f32 v[204:205], v[230:231], v[204:205]
	v_pk_mul_f32 v[206:207], v[232:233], v[206:207]
	v_pk_mul_f32 v[208:209], v[234:235], v[208:209]
	v_pk_mul_f32 v[192:193], v[192:193], v[216:217]
	v_pk_mul_f32 v[210:211], v[236:237], v[210:211]
	v_pk_mul_f32 v[212:213], v[238:239], v[212:213]
	v_pk_mul_f32 v[214:215], v[240:241], v[214:215]
	v_cvt_pk_bf16_f32 v202, v202, v203
	v_cvt_pk_bf16_f32 v203, v206, v207
	v_cvt_pk_bf16_f32 v204, v204, v205
	v_cvt_pk_bf16_f32 v205, v208, v209
	v_cvt_pk_bf16_f32 v209, v192, v193
	v_cvt_f32_i32_e32 v193, v113
	v_cvt_f32_i32_e32 v192, v112
	v_cvt_pk_bf16_f32 v206, v210, v211
	v_cvt_pk_bf16_f32 v207, v214, v215
	v_cvt_pk_bf16_f32 v208, v212, v213
	global_store_dwordx2 v[224:225], v[202:203], off
	global_store_dwordx2 v[224:225], v[204:205], off offset:16
	global_store_dwordx2 v[224:225], v[206:207], off offset:256
	global_store_dwordx2 v[224:225], v[208:209], off offset:272
	v_cvt_f32_i32_e32 v203, v109
	v_cvt_f32_i32_e32 v202, v108
	v_pk_mul_f32 v[204:205], v[144:145], v[194:195] op_sel_hi:[1,0]
	v_pk_mul_f32 v[242:243], v[142:143], v[194:195] op_sel_hi:[1,0]
	v_pk_mul_f32 v[192:193], v[204:205], v[192:193]
	v_pk_mul_f32 v[204:205], v[140:141], v[194:195] op_sel_hi:[1,0]
	v_pk_mul_f32 v[244:245], v[138:139], v[194:195] op_sel_hi:[1,0]
	v_pk_mul_f32 v[202:203], v[204:205], v[202:203]
	v_pk_mul_f32 v[216:217], v[242:243], v[218:219]
	v_pk_mul_f32 v[218:219], v[244:245], v[220:221]
	v_cvt_pk_bf16_f32 v205, v192, v193
	v_cvt_pk_bf16_f32 v193, v202, v203
	v_lshl_add_u64 v[202:203], v[190:191], 0, s[0:1]
	v_cvt_pk_bf16_f32 v204, v216, v217
	v_cvt_pk_bf16_f32 v192, v218, v219
	v_lshl_add_u64 v[202:203], v[202:203], 0, v[154:155]
	global_store_dwordx2 v[202:203], v[204:205], off
	global_store_dwordx2 v[202:203], v[192:193], off offset:16
	v_cvt_f32_i32_e32 v193, v103
	v_cvt_f32_i32_e32 v192, v102
	v_cvt_f32_i32_e32 v205, v99
	v_cvt_f32_i32_e32 v204, v98
	v_pk_mul_f32 v[206:207], v[134:135], v[194:195] op_sel_hi:[1,0]
	v_cvt_f32_i32_e32 v209, v101
	v_pk_mul_f32 v[192:193], v[206:207], v[192:193]
	v_pk_mul_f32 v[206:207], v[130:131], v[194:195] op_sel_hi:[1,0]
	v_cvt_f32_i32_e32 v208, v100
	v_pk_mul_f32 v[204:205], v[206:207], v[204:205]
	v_cvt_f32_i32_e32 v207, v105
	v_cvt_f32_i32_e32 v206, v104
	v_pk_mul_f32 v[210:211], v[136:137], v[194:195] op_sel_hi:[1,0]
	v_pk_mul_f32 v[194:195], v[132:133], v[194:195] op_sel_hi:[1,0]
	v_cvt_pk_bf16_f32 v192, v192, v193
	v_pk_mul_f32 v[206:207], v[210:211], v[206:207]
	v_pk_mul_f32 v[194:195], v[194:195], v[208:209]
	v_cvt_pk_bf16_f32 v193, v206, v207
	v_cvt_pk_bf16_f32 v204, v204, v205
	v_cvt_pk_bf16_f32 v205, v194, v195
	v_cvt_f32_i32_e32 v195, v95
	v_cvt_f32_i32_e32 v194, v94
	global_store_dwordx2 v[202:203], v[192:193], off offset:256
	global_store_dwordx2 v[202:203], v[204:205], off offset:272
	v_cvt_f32_i32_e32 v203, v91
	v_cvt_f32_i32_e32 v202, v90
	v_pk_mul_f32 v[204:205], v[142:143], v[222:223] op_sel_hi:[1,0]
	v_cvt_f32_i32_e32 v207, v93
	v_pk_mul_f32 v[194:195], v[204:205], v[194:195]
	v_pk_mul_f32 v[204:205], v[138:139], v[222:223] op_sel_hi:[1,0]
	v_cvt_f32_i32_e32 v206, v92
	v_pk_mul_f32 v[202:203], v[204:205], v[202:203]
	v_cvt_f32_i32_e32 v205, v97
	v_cvt_f32_i32_e32 v204, v96
	v_pk_mul_f32 v[208:209], v[144:145], v[222:223] op_sel_hi:[1,0]
	v_lshl_add_u64 v[192:193], s[6:7], 0, v[168:169]
	v_cvt_pk_bf16_f32 v194, v194, v195
	v_pk_mul_f32 v[204:205], v[208:209], v[204:205]
	v_pk_mul_f32 v[208:209], v[140:141], v[222:223] op_sel_hi:[1,0]
	v_cvt_pk_bf16_f32 v195, v204, v205
	v_lshl_add_u64 v[204:205], v[192:193], 0, s[0:1]
	v_pk_mul_f32 v[206:207], v[208:209], v[206:207]
	v_lshl_add_u64 v[204:205], v[204:205], 0, v[154:155]
	v_cvt_pk_bf16_f32 v202, v202, v203
	v_cvt_pk_bf16_f32 v203, v206, v207
	global_store_dwordx2 v[204:205], v[194:195], off
	global_store_dwordx2 v[204:205], v[202:203], off offset:16
	v_cvt_f32_i32_e32 v195, v87
	v_cvt_f32_i32_e32 v194, v86
	v_cvt_f32_i32_e32 v203, v83
	v_cvt_f32_i32_e32 v202, v82
	v_pk_mul_f32 v[206:207], v[134:135], v[222:223] op_sel_hi:[1,0]
	v_cvt_f32_i32_e32 v209, v85
	v_pk_mul_f32 v[194:195], v[206:207], v[194:195]
	v_pk_mul_f32 v[206:207], v[130:131], v[222:223] op_sel_hi:[1,0]
	v_cvt_f32_i32_e32 v208, v84
	v_pk_mul_f32 v[202:203], v[206:207], v[202:203]
	v_cvt_f32_i32_e32 v207, v89
	v_cvt_f32_i32_e32 v206, v88
	v_pk_mul_f32 v[210:211], v[136:137], v[222:223] op_sel_hi:[1,0]
	v_cvt_pk_bf16_f32 v194, v194, v195
	v_cvt_pk_bf16_f32 v202, v202, v203
	v_pk_mul_f32 v[206:207], v[210:211], v[206:207]
	v_pk_mul_f32 v[210:211], v[132:133], v[222:223] op_sel_hi:[1,0]
	v_cvt_pk_bf16_f32 v195, v206, v207
	v_pk_mul_f32 v[208:209], v[210:211], v[208:209]
	v_pk_mul_f32 v[206:207], v[142:143], v[200:201] op_sel_hi:[1,0]
	v_cvt_pk_bf16_f32 v203, v208, v209
	global_store_dwordx2 v[204:205], v[194:195], off offset:256
	global_store_dwordx2 v[204:205], v[202:203], off offset:272
	v_cvt_f32_i32_e32 v203, v79
	v_cvt_f32_i32_e32 v202, v78
	v_cvt_f32_i32_e32 v205, v75
	v_cvt_f32_i32_e32 v204, v74
	v_cvt_f32_i32_e32 v209, v77
	v_pk_mul_f32 v[202:203], v[206:207], v[202:203]
	v_pk_mul_f32 v[206:207], v[138:139], v[200:201] op_sel_hi:[1,0]
	v_cvt_f32_i32_e32 v208, v76
	v_pk_mul_f32 v[204:205], v[206:207], v[204:205]
	v_cvt_f32_i32_e32 v207, v81
	v_cvt_f32_i32_e32 v206, v80
	v_pk_mul_f32 v[210:211], v[144:145], v[200:201] op_sel_hi:[1,0]
	v_lshl_add_u64 v[194:195], s[6:7], 0, v[172:173]
	v_cvt_pk_bf16_f32 v202, v202, v203
	v_pk_mul_f32 v[206:207], v[210:211], v[206:207]
	v_pk_mul_f32 v[210:211], v[140:141], v[200:201] op_sel_hi:[1,0]
	v_cvt_pk_bf16_f32 v203, v206, v207
	v_lshl_add_u64 v[206:207], v[194:195], 0, s[0:1]
	v_pk_mul_f32 v[208:209], v[210:211], v[208:209]
	v_lshl_add_u64 v[206:207], v[206:207], 0, v[154:155]
	v_cvt_pk_bf16_f32 v204, v204, v205
	v_cvt_pk_bf16_f32 v205, v208, v209
	global_store_dwordx2 v[206:207], v[202:203], off
	global_store_dwordx2 v[206:207], v[204:205], off offset:16
	v_cvt_f32_i32_e32 v203, v71
	v_cvt_f32_i32_e32 v202, v70
	v_cvt_f32_i32_e32 v205, v67
	v_cvt_f32_i32_e32 v204, v66
	v_pk_mul_f32 v[208:209], v[134:135], v[200:201] op_sel_hi:[1,0]
	v_cvt_f32_i32_e32 v211, v69
	v_pk_mul_f32 v[202:203], v[208:209], v[202:203]
	v_pk_mul_f32 v[208:209], v[130:131], v[200:201] op_sel_hi:[1,0]
	v_cvt_f32_i32_e32 v210, v68
	v_pk_mul_f32 v[204:205], v[208:209], v[204:205]
	v_cvt_f32_i32_e32 v209, v73
	v_cvt_f32_i32_e32 v208, v72
	v_pk_mul_f32 v[212:213], v[136:137], v[200:201] op_sel_hi:[1,0]
	v_pk_mul_f32 v[200:201], v[132:133], v[200:201] op_sel_hi:[1,0]
	v_cvt_pk_bf16_f32 v202, v202, v203
	v_pk_mul_f32 v[208:209], v[212:213], v[208:209]
	v_pk_mul_f32 v[200:201], v[200:201], v[210:211]
	v_cvt_pk_bf16_f32 v203, v208, v209
	v_cvt_pk_bf16_f32 v204, v204, v205
	v_cvt_pk_bf16_f32 v205, v200, v201
	v_cvt_f32_i32_e32 v201, v63
	v_cvt_f32_i32_e32 v200, v62
	global_store_dwordx2 v[206:207], v[202:203], off offset:256
	global_store_dwordx2 v[206:207], v[204:205], off offset:272
	v_cvt_f32_i32_e32 v203, v59
	v_cvt_f32_i32_e32 v202, v58
	v_pk_mul_f32 v[204:205], v[142:143], v[196:197] op_sel_hi:[1,0]
	v_cvt_f32_i32_e32 v207, v61
	v_pk_mul_f32 v[200:201], v[204:205], v[200:201]
	v_pk_mul_f32 v[204:205], v[138:139], v[196:197] op_sel_hi:[1,0]
	v_cvt_f32_i32_e32 v206, v60
	v_pk_mul_f32 v[202:203], v[204:205], v[202:203]
	v_cvt_f32_i32_e32 v205, v65
	v_cvt_f32_i32_e32 v204, v64
	s_or_b32 s0, s8, 1
	s_ashr_i32 s1, s0, 31
	v_pk_mul_f32 v[208:209], v[144:145], v[196:197] op_sel_hi:[1,0]
	s_lshl_b64 s[0:1], s[0:1], 20
	v_pk_mul_f32 v[204:205], v[208:209], v[204:205]
	v_pk_mul_f32 v[208:209], v[140:141], v[196:197] op_sel_hi:[1,0]
	v_lshl_add_u64 v[198:199], v[198:199], 0, s[0:1]
	v_pk_mul_f32 v[206:207], v[208:209], v[206:207]
	v_cvt_pk_bf16_f32 v200, v200, v201
	v_cvt_pk_bf16_f32 v201, v204, v205
	v_lshl_add_u64 v[198:199], v[198:199], 0, v[154:155]
	v_cvt_pk_bf16_f32 v202, v202, v203
	v_cvt_pk_bf16_f32 v203, v206, v207
	global_store_dwordx2 v[198:199], v[200:201], off
	global_store_dwordx2 v[198:199], v[202:203], off offset:16
	v_cvt_f32_i32_e32 v201, v55
	v_cvt_f32_i32_e32 v200, v54
	v_cvt_f32_i32_e32 v203, v51
	v_cvt_f32_i32_e32 v202, v50
	v_pk_mul_f32 v[204:205], v[134:135], v[196:197] op_sel_hi:[1,0]
	v_cvt_f32_i32_e32 v207, v53
	v_pk_mul_f32 v[200:201], v[204:205], v[200:201]
	v_pk_mul_f32 v[204:205], v[130:131], v[196:197] op_sel_hi:[1,0]
	v_cvt_f32_i32_e32 v206, v52
	v_pk_mul_f32 v[202:203], v[204:205], v[202:203]
	v_cvt_f32_i32_e32 v205, v57
	v_cvt_f32_i32_e32 v204, v56
	v_pk_mul_f32 v[208:209], v[136:137], v[196:197] op_sel_hi:[1,0]
	v_pk_mul_f32 v[196:197], v[132:133], v[196:197] op_sel_hi:[1,0]
	v_cvt_pk_bf16_f32 v200, v200, v201
	v_pk_mul_f32 v[204:205], v[208:209], v[204:205]
	v_pk_mul_f32 v[196:197], v[196:197], v[206:207]
	v_cvt_pk_bf16_f32 v201, v204, v205
	v_cvt_pk_bf16_f32 v202, v202, v203
	v_cvt_pk_bf16_f32 v203, v196, v197
	v_cvt_f32_i32_e32 v197, v47
	v_cvt_f32_i32_e32 v196, v46
	global_store_dwordx2 v[198:199], v[200:201], off offset:256
	global_store_dwordx2 v[198:199], v[202:203], off offset:272
	v_cvt_f32_i32_e32 v199, v43
	v_cvt_f32_i32_e32 v198, v42
	v_pk_mul_f32 v[200:201], v[142:143], v[188:189] op_sel_hi:[1,0]
	v_cvt_f32_i32_e32 v203, v45
	v_pk_mul_f32 v[196:197], v[200:201], v[196:197]
	v_pk_mul_f32 v[200:201], v[138:139], v[188:189] op_sel_hi:[1,0]
	v_cvt_f32_i32_e32 v202, v44
	v_pk_mul_f32 v[198:199], v[200:201], v[198:199]
	v_cvt_f32_i32_e32 v201, v49
	v_cvt_f32_i32_e32 v200, v48
	v_pk_mul_f32 v[204:205], v[144:145], v[188:189] op_sel_hi:[1,0]
	v_lshl_add_u64 v[190:191], v[190:191], 0, s[0:1]
	v_cvt_pk_bf16_f32 v196, v196, v197
	v_pk_mul_f32 v[200:201], v[204:205], v[200:201]
	v_pk_mul_f32 v[204:205], v[140:141], v[188:189] op_sel_hi:[1,0]
	v_cvt_pk_bf16_f32 v197, v200, v201
	v_pk_mul_f32 v[202:203], v[204:205], v[202:203]
	v_lshl_add_u64 v[190:191], v[190:191], 0, v[154:155]
	v_cvt_pk_bf16_f32 v198, v198, v199
	v_cvt_pk_bf16_f32 v199, v202, v203
	global_store_dwordx2 v[190:191], v[196:197], off
	global_store_dwordx2 v[190:191], v[198:199], off offset:16
	v_cvt_f32_i32_e32 v197, v39
	v_cvt_f32_i32_e32 v196, v38
	v_cvt_f32_i32_e32 v199, v35
	v_cvt_f32_i32_e32 v198, v34
	v_pk_mul_f32 v[200:201], v[134:135], v[188:189] op_sel_hi:[1,0]
	v_cvt_f32_i32_e32 v203, v37
	v_pk_mul_f32 v[196:197], v[200:201], v[196:197]
	v_pk_mul_f32 v[200:201], v[130:131], v[188:189] op_sel_hi:[1,0]
	v_cvt_f32_i32_e32 v202, v36
	v_pk_mul_f32 v[198:199], v[200:201], v[198:199]
	v_cvt_f32_i32_e32 v201, v41
	v_cvt_f32_i32_e32 v200, v40
	v_pk_mul_f32 v[204:205], v[136:137], v[188:189] op_sel_hi:[1,0]
	v_pk_mul_f32 v[188:189], v[132:133], v[188:189] op_sel_hi:[1,0]
	v_cvt_pk_bf16_f32 v196, v196, v197
	v_pk_mul_f32 v[200:201], v[204:205], v[200:201]
	v_pk_mul_f32 v[188:189], v[188:189], v[202:203]
	v_cvt_pk_bf16_f32 v197, v200, v201
	v_cvt_pk_bf16_f32 v198, v198, v199
	v_cvt_pk_bf16_f32 v199, v188, v189
	v_cvt_f32_i32_e32 v189, v31
	v_cvt_f32_i32_e32 v188, v30
	global_store_dwordx2 v[190:191], v[196:197], off offset:256
	global_store_dwordx2 v[190:191], v[198:199], off offset:272
	v_cvt_f32_i32_e32 v191, v27
	v_cvt_f32_i32_e32 v190, v26
	v_pk_mul_f32 v[196:197], v[142:143], v[186:187] op_sel_hi:[1,0]
	v_cvt_f32_i32_e32 v199, v29
	v_pk_mul_f32 v[188:189], v[196:197], v[188:189]
	v_pk_mul_f32 v[196:197], v[138:139], v[186:187] op_sel_hi:[1,0]
	v_cvt_f32_i32_e32 v198, v28
	v_pk_mul_f32 v[190:191], v[196:197], v[190:191]
	v_cvt_f32_i32_e32 v197, v33
	v_cvt_f32_i32_e32 v196, v32
	v_pk_mul_f32 v[200:201], v[144:145], v[186:187] op_sel_hi:[1,0]
	v_lshl_add_u64 v[192:193], v[192:193], 0, s[0:1]
	v_cvt_pk_bf16_f32 v188, v188, v189
	v_pk_mul_f32 v[196:197], v[200:201], v[196:197]
	v_pk_mul_f32 v[200:201], v[140:141], v[186:187] op_sel_hi:[1,0]
	v_cvt_pk_bf16_f32 v189, v196, v197
	v_pk_mul_f32 v[198:199], v[200:201], v[198:199]
	v_lshl_add_u64 v[192:193], v[192:193], 0, v[154:155]
	v_cvt_pk_bf16_f32 v190, v190, v191
	v_cvt_pk_bf16_f32 v191, v198, v199
	global_store_dwordx2 v[192:193], v[188:189], off
	global_store_dwordx2 v[192:193], v[190:191], off offset:16
	v_cvt_f32_i32_e32 v189, v23
	v_cvt_f32_i32_e32 v188, v22
	v_cvt_f32_i32_e32 v191, v19
	v_cvt_f32_i32_e32 v190, v18
	v_pk_mul_f32 v[196:197], v[134:135], v[186:187] op_sel_hi:[1,0]
	v_cvt_f32_i32_e32 v199, v21
	v_pk_mul_f32 v[188:189], v[196:197], v[188:189]
	v_pk_mul_f32 v[196:197], v[130:131], v[186:187] op_sel_hi:[1,0]
	v_cvt_f32_i32_e32 v198, v20
	v_pk_mul_f32 v[190:191], v[196:197], v[190:191]
	v_cvt_f32_i32_e32 v197, v25
	v_cvt_f32_i32_e32 v196, v24
	v_pk_mul_f32 v[200:201], v[136:137], v[186:187] op_sel_hi:[1,0]
	v_pk_mul_f32 v[186:187], v[132:133], v[186:187] op_sel_hi:[1,0]
	v_cvt_pk_bf16_f32 v188, v188, v189
	v_pk_mul_f32 v[196:197], v[200:201], v[196:197]
	v_pk_mul_f32 v[186:187], v[186:187], v[198:199]
	v_cvt_pk_bf16_f32 v189, v196, v197
	v_cvt_pk_bf16_f32 v190, v190, v191
	v_cvt_pk_bf16_f32 v191, v186, v187
	global_store_dwordx2 v[192:193], v[188:189], off offset:256
	global_store_dwordx2 v[192:193], v[190:191], off offset:272
	v_cvt_f32_i32_e32 v189, v11
	v_cvt_f32_i32_e32 v188, v10
	v_cvt_f32_i32_e32 v187, v15
	v_cvt_f32_i32_e32 v186, v14
	v_pk_mul_f32 v[138:139], v[138:139], v[184:185] op_sel_hi:[1,0]
	v_pk_mul_f32 v[142:143], v[142:143], v[184:185] op_sel_hi:[1,0]
	v_pk_mul_f32 v[138:139], v[138:139], v[188:189]
	v_cvt_f32_i32_e32 v189, v13
	v_cvt_f32_i32_e32 v188, v12
	v_pk_mul_f32 v[142:143], v[142:143], v[186:187]
	v_cvt_f32_i32_e32 v187, v17
	v_cvt_f32_i32_e32 v186, v16
	v_pk_mul_f32 v[140:141], v[140:141], v[184:185] op_sel_hi:[1,0]
	v_pk_mul_f32 v[144:145], v[144:145], v[184:185] op_sel_hi:[1,0]
	v_pk_mul_f32 v[140:141], v[140:141], v[188:189]
	v_pk_mul_f32 v[144:145], v[144:145], v[186:187]
	v_cvt_pk_bf16_f32 v138, v138, v139
	v_cvt_pk_bf16_f32 v139, v140, v141
	v_lshl_add_u64 v[140:141], v[194:195], 0, s[0:1]
	v_cvt_pk_bf16_f32 v142, v142, v143
	v_cvt_pk_bf16_f32 v143, v144, v145
	v_lshl_add_u64 v[140:141], v[140:141], 0, v[154:155]
	global_store_dwordx2 v[140:141], v[142:143], off
	global_store_dwordx2 v[140:141], v[138:139], off offset:16
	v_cvt_f32_i32_e32 v139, v7
	v_cvt_f32_i32_e32 v138, v6
	v_cvt_f32_i32_e32 v143, v3
	v_cvt_f32_i32_e32 v142, v2
	v_pk_mul_f32 v[134:135], v[134:135], v[184:185] op_sel_hi:[1,0]
	v_pk_mul_f32 v[130:131], v[130:131], v[184:185] op_sel_hi:[1,0]
	v_pk_mul_f32 v[134:135], v[134:135], v[138:139]
	v_cvt_f32_i32_e32 v139, v9
	v_cvt_f32_i32_e32 v138, v8
	v_pk_mul_f32 v[130:131], v[130:131], v[142:143]
	v_cvt_f32_i32_e32 v143, v5
	v_cvt_f32_i32_e32 v142, v4
	v_pk_mul_f32 v[136:137], v[136:137], v[184:185] op_sel_hi:[1,0]
	v_pk_mul_f32 v[132:133], v[132:133], v[184:185] op_sel_hi:[1,0]
	v_pk_mul_f32 v[136:137], v[136:137], v[138:139]
	v_pk_mul_f32 v[132:133], v[132:133], v[142:143]
	v_cvt_pk_bf16_f32 v134, v134, v135
	v_cvt_pk_bf16_f32 v135, v136, v137
	v_cvt_pk_bf16_f32 v130, v130, v131
	v_cvt_pk_bf16_f32 v131, v132, v133
	global_store_dwordx2 v[140:141], v[134:135], off offset:256
	global_store_dwordx2 v[140:141], v[130:131], off offset:272
	s_cbranch_execz .LBB0_168
	s_branch .LBB0_243
	s_nop 0
	s_nop 0
	s_nop 0
	s_nop 0
	s_nop 0
	s_nop 0
	s_nop 0
	s_nop 0

.LBB0_368:
	ds_read_b128 v[144:147], v139
	ds_read_b128 v[148:151], v139 offset:1024
	ds_read_b128 v[152:155], v139 offset:2048
	ds_read_b128 v[156:159], v139 offset:3072
	ds_read_b128 v[160:163], v140
	ds_read_b128 v[164:167], v140 offset:1024
	ds_read_b128 v[168:171], v140 offset:2048
	ds_read_b128 v[172:175], v140 offset:3072
	s_add_u32 s8, s6, 0x100
	s_addc_u32 s9, s7, 0
	s_cmp_lg_u32 s22, 28
	s_cselect_b32 s10, s8, 0
	s_add_u32 s12, s2, s10
	s_addc_u32 s13, s3, 0
	s_add_u32 s10, s0, s10
	s_addc_u32 s11, s1, 0
	s_mov_b32 m0, s23
	v_lshl_add_u64 v[208:209], v[134:135], 0, s[6:7]
	ds_read_b128 v[176:179], v141
	ds_read_b128 v[180:183], v141 offset:1024
	ds_read_b128 v[184:187], v141 offset:2048
	ds_read_b128 v[188:191], v141 offset:3072
	ds_read_b128 v[192:195], v141 offset:4096
	ds_read_b128 v[196:199], v141 offset:5120
	ds_read_b128 v[200:203], v141 offset:6144
	ds_read_b128 v[204:207], v141 offset:7168
	global_load_lds_dwordx4 v[208:209], off
	v_lshl_add_u64 v[208:209], v[136:137], 0, s[6:7]
	s_mov_b32 m0, s24
	s_nop 0
	global_load_lds_dwordx4 v[208:209], off
	s_waitcnt vmcnt(8)
	s_waitcnt lgkmcnt(0)
	s_barrier
	s_setprio 1
	s_waitcnt lgkmcnt(0)
	v_mfma_f32_16x16x32_bf16 v[126:129], v[144:147], v[176:179], v[126:129]
	v_mfma_f32_16x16x32_bf16 v[122:125], v[152:155], v[176:179], v[122:125]
	v_mfma_f32_16x16x32_bf16 v[118:121], v[144:147], v[184:187], v[118:121]
	v_mfma_f32_16x16x32_bf16 v[114:117], v[152:155], v[184:187], v[114:117]
	v_mfma_f32_16x16x32_bf16 v[106:109], v[144:147], v[192:195], v[106:109]
	v_mfma_f32_16x16x32_bf16 v[98:101], v[152:155], v[192:195], v[98:101]
	v_mfma_f32_16x16x32_bf16 v[90:93], v[144:147], v[200:203], v[90:93]
	v_mfma_f32_16x16x32_bf16 v[82:85], v[152:155], v[200:203], v[82:85]
	v_mfma_f32_16x16x32_bf16 v[126:129], v[148:151], v[180:183], v[126:129]
	v_mfma_f32_16x16x32_bf16 v[122:125], v[156:159], v[180:183], v[122:125]
	v_mfma_f32_16x16x32_bf16 v[118:121], v[148:151], v[188:191], v[118:121]
	v_mfma_f32_16x16x32_bf16 v[114:117], v[156:159], v[188:191], v[114:117]
	v_mfma_f32_16x16x32_bf16 v[106:109], v[148:151], v[196:199], v[106:109]
	v_mfma_f32_16x16x32_bf16 v[98:101], v[156:159], v[196:199], v[98:101]
	v_mfma_f32_16x16x32_bf16 v[90:93], v[148:151], v[204:207], v[90:93]
	v_mfma_f32_16x16x32_bf16 v[82:85], v[156:159], v[204:207], v[82:85]
	v_mfma_f32_16x16x32_bf16 v[110:113], v[160:163], v[176:179], v[110:113]
	v_mfma_f32_16x16x32_bf16 v[102:105], v[168:171], v[176:179], v[102:105]
	v_mfma_f32_16x16x32_bf16 v[94:97], v[160:163], v[184:187], v[94:97]
	v_mfma_f32_16x16x32_bf16 v[86:89], v[168:171], v[184:187], v[86:89]
	v_mfma_f32_16x16x32_bf16 v[78:81], v[160:163], v[192:195], v[78:81]
	v_mfma_f32_16x16x32_bf16 v[74:77], v[168:171], v[192:195], v[74:77]
	v_mfma_f32_16x16x32_bf16 v[70:73], v[160:163], v[200:203], v[70:73]
	v_mfma_f32_16x16x32_bf16 v[66:69], v[168:171], v[200:203], v[66:69]
	v_mfma_f32_16x16x32_bf16 v[110:113], v[164:167], v[180:183], v[110:113]
	v_mfma_f32_16x16x32_bf16 v[102:105], v[172:175], v[180:183], v[102:105]
	v_mfma_f32_16x16x32_bf16 v[94:97], v[164:167], v[188:191], v[94:97]
	v_mfma_f32_16x16x32_bf16 v[86:89], v[172:175], v[188:191], v[86:89]
	v_mfma_f32_16x16x32_bf16 v[78:81], v[164:167], v[196:199], v[78:81]
	v_mfma_f32_16x16x32_bf16 v[74:77], v[172:175], v[196:199], v[74:77]
	v_mfma_f32_16x16x32_bf16 v[70:73], v[164:167], v[204:207], v[70:73]
	v_mfma_f32_16x16x32_bf16 v[66:69], v[172:175], v[204:207], v[66:69]
	s_setprio 0
	s_barrier
	s_mov_b32 m0, s25
	v_lshl_add_u64 v[208:209], s[10:11], 0, v[132:133]
	s_add_u32 s6, s10, 0x80000
	ds_read_b128 v[176:179], v141 offset:16384
	ds_read_b128 v[180:183], v141 offset:17408
	ds_read_b128 v[184:187], v141 offset:18432
	ds_read_b128 v[188:191], v141 offset:19456
	ds_read_b128 v[192:195], v141 offset:20480
	ds_read_b128 v[196:199], v141 offset:21504
	ds_read_b128 v[200:203], v141 offset:22528
	ds_read_b128 v[204:207], v141 offset:23552
	global_load_lds_dwordx4 v[208:209], off
	v_lshl_add_u64 v[210:211], s[10:11], 0, v[130:131]
	s_mov_b32 m0, s26
	s_addc_u32 s7, s11, 0
	global_load_lds_dwordx4 v[210:211], off
	v_lshl_add_u64 v[212:213], s[6:7], 0, v[132:133]
	s_mov_b32 m0, s27
	v_lshl_add_u64 v[214:215], s[12:13], 0, v[130:131]
	global_load_lds_dwordx4 v[212:213], off
	v_lshl_add_u64 v[212:213], s[6:7], 0, v[130:131]
	s_mov_b32 m0, s28
	s_nop 0
	global_load_lds_dwordx4 v[212:213], off
	v_lshl_add_u64 v[212:213], s[12:13], 0, v[132:133]
	s_mov_b32 m0, s15
	s_nop 0
	global_load_lds_dwordx4 v[212:213], off
	s_mov_b32 m0, s16
	s_nop 0
	global_load_lds_dwordx4 v[214:215], off
	s_waitcnt vmcnt(8)
	s_waitcnt lgkmcnt(0)
	s_barrier
	s_setprio 1
	s_waitcnt lgkmcnt(0)
	v_mfma_f32_16x16x32_bf16 v[62:65], v[144:147], v[176:179], v[62:65]
	v_mfma_f32_16x16x32_bf16 v[58:61], v[152:155], v[176:179], v[58:61]
	v_mfma_f32_16x16x32_bf16 v[54:57], v[144:147], v[184:187], v[54:57]
	v_mfma_f32_16x16x32_bf16 v[50:53], v[152:155], v[184:187], v[50:53]
	v_mfma_f32_16x16x32_bf16 v[42:45], v[144:147], v[192:195], v[42:45]
	v_mfma_f32_16x16x32_bf16 v[34:37], v[152:155], v[192:195], v[34:37]
	v_mfma_f32_16x16x32_bf16 v[26:29], v[144:147], v[200:203], v[26:29]
	v_mfma_f32_16x16x32_bf16 v[18:21], v[152:155], v[200:203], v[18:21]
	v_mfma_f32_16x16x32_bf16 v[62:65], v[148:151], v[180:183], v[62:65]
	v_mfma_f32_16x16x32_bf16 v[58:61], v[156:159], v[180:183], v[58:61]
	v_mfma_f32_16x16x32_bf16 v[54:57], v[148:151], v[188:191], v[54:57]
	v_mfma_f32_16x16x32_bf16 v[50:53], v[156:159], v[188:191], v[50:53]
	v_mfma_f32_16x16x32_bf16 v[42:45], v[148:151], v[196:199], v[42:45]
	v_mfma_f32_16x16x32_bf16 v[34:37], v[156:159], v[196:199], v[34:37]
	v_mfma_f32_16x16x32_bf16 v[26:29], v[148:151], v[204:207], v[26:29]
	v_mfma_f32_16x16x32_bf16 v[18:21], v[156:159], v[204:207], v[18:21]
	v_mfma_f32_16x16x32_bf16 v[46:49], v[160:163], v[176:179], v[46:49]
	v_mfma_f32_16x16x32_bf16 v[38:41], v[168:171], v[176:179], v[38:41]
	v_mfma_f32_16x16x32_bf16 v[30:33], v[160:163], v[184:187], v[30:33]
	v_mfma_f32_16x16x32_bf16 v[22:25], v[168:171], v[184:187], v[22:25]
	v_mfma_f32_16x16x32_bf16 v[14:17], v[160:163], v[192:195], v[14:17]
	v_mfma_f32_16x16x32_bf16 v[10:13], v[168:171], v[192:195], v[10:13]
	v_mfma_f32_16x16x32_bf16 v[6:9], v[160:163], v[200:203], v[6:9]
	v_mfma_f32_16x16x32_bf16 v[2:5], v[168:171], v[200:203], v[2:5]
	v_mfma_f32_16x16x32_bf16 v[46:49], v[164:167], v[180:183], v[46:49]
	v_mfma_f32_16x16x32_bf16 v[38:41], v[172:175], v[180:183], v[38:41]
	v_mfma_f32_16x16x32_bf16 v[30:33], v[164:167], v[188:191], v[30:33]
	v_mfma_f32_16x16x32_bf16 v[22:25], v[172:175], v[188:191], v[22:25]
	v_mfma_f32_16x16x32_bf16 v[14:17], v[164:167], v[196:199], v[14:17]
	v_mfma_f32_16x16x32_bf16 v[10:13], v[172:175], v[196:199], v[10:13]
	v_mfma_f32_16x16x32_bf16 v[6:9], v[164:167], v[204:207], v[6:9]
	v_mfma_f32_16x16x32_bf16 v[2:5], v[172:175], v[204:207], v[2:5]
	s_setprio 0
	s_barrier
	ds_read_b128 v[144:147], v142
	ds_read_b128 v[148:151], v142 offset:1024
	ds_read_b128 v[152:155], v142 offset:2048
	ds_read_b128 v[156:159], v142 offset:3072
	ds_read_b128 v[160:163], v143
	ds_read_b128 v[164:167], v143 offset:1024
	ds_read_b128 v[168:171], v143 offset:2048
	ds_read_b128 v[172:175], v143 offset:3072
	s_add_u32 s6, s12, 0x80000
	s_addc_u32 s7, s13, 0
	s_mov_b32 m0, s17
	v_lshl_add_u64 v[216:217], s[6:7], 0, v[132:133]
	ds_read_b128 v[176:179], v141 offset:32768
	ds_read_b128 v[180:183], v141 offset:33792
	ds_read_b128 v[184:187], v141 offset:34816
	ds_read_b128 v[188:191], v141 offset:35840
	ds_read_b128 v[192:195], v141 offset:36864
	ds_read_b128 v[196:199], v141 offset:37888
	ds_read_b128 v[200:203], v141 offset:38912
	ds_read_b128 v[204:207], v141 offset:39936
	global_load_lds_dwordx4 v[216:217], off
	v_lshl_add_u64 v[216:217], s[6:7], 0, v[130:131]
	s_mov_b32 m0, s18
	s_nop 0
	global_load_lds_dwordx4 v[216:217], off
	s_waitcnt vmcnt(8)
	s_waitcnt lgkmcnt(0)
	s_barrier
	s_setprio 1
	s_waitcnt lgkmcnt(0)
	v_mfma_f32_16x16x32_bf16 v[126:129], v[144:147], v[176:179], v[126:129]
	v_mfma_f32_16x16x32_bf16 v[122:125], v[152:155], v[176:179], v[122:125]
	v_mfma_f32_16x16x32_bf16 v[118:121], v[144:147], v[184:187], v[118:121]
	v_mfma_f32_16x16x32_bf16 v[114:117], v[152:155], v[184:187], v[114:117]
	v_mfma_f32_16x16x32_bf16 v[106:109], v[144:147], v[192:195], v[106:109]
	v_mfma_f32_16x16x32_bf16 v[98:101], v[152:155], v[192:195], v[98:101]
	v_mfma_f32_16x16x32_bf16 v[90:93], v[144:147], v[200:203], v[90:93]
	v_mfma_f32_16x16x32_bf16 v[82:85], v[152:155], v[200:203], v[82:85]
	v_mfma_f32_16x16x32_bf16 v[126:129], v[148:151], v[180:183], v[126:129]
	v_mfma_f32_16x16x32_bf16 v[122:125], v[156:159], v[180:183], v[122:125]
	v_mfma_f32_16x16x32_bf16 v[118:121], v[148:151], v[188:191], v[118:121]
	v_mfma_f32_16x16x32_bf16 v[114:117], v[156:159], v[188:191], v[114:117]
	v_mfma_f32_16x16x32_bf16 v[106:109], v[148:151], v[196:199], v[106:109]
	v_mfma_f32_16x16x32_bf16 v[98:101], v[156:159], v[196:199], v[98:101]
	v_mfma_f32_16x16x32_bf16 v[90:93], v[148:151], v[204:207], v[90:93]
	v_mfma_f32_16x16x32_bf16 v[82:85], v[156:159], v[204:207], v[82:85]
	v_mfma_f32_16x16x32_bf16 v[110:113], v[160:163], v[176:179], v[110:113]
	v_mfma_f32_16x16x32_bf16 v[102:105], v[168:171], v[176:179], v[102:105]
	v_mfma_f32_16x16x32_bf16 v[94:97], v[160:163], v[184:187], v[94:97]
	v_mfma_f32_16x16x32_bf16 v[86:89], v[168:171], v[184:187], v[86:89]
	v_mfma_f32_16x16x32_bf16 v[78:81], v[160:163], v[192:195], v[78:81]
	v_mfma_f32_16x16x32_bf16 v[74:77], v[168:171], v[192:195], v[74:77]
	v_mfma_f32_16x16x32_bf16 v[70:73], v[160:163], v[200:203], v[70:73]
	v_mfma_f32_16x16x32_bf16 v[66:69], v[168:171], v[200:203], v[66:69]
	v_mfma_f32_16x16x32_bf16 v[110:113], v[164:167], v[180:183], v[110:113]
	v_mfma_f32_16x16x32_bf16 v[102:105], v[172:175], v[180:183], v[102:105]
	v_mfma_f32_16x16x32_bf16 v[94:97], v[164:167], v[188:191], v[94:97]
	v_mfma_f32_16x16x32_bf16 v[86:89], v[172:175], v[188:191], v[86:89]
	v_mfma_f32_16x16x32_bf16 v[78:81], v[164:167], v[196:199], v[78:81]
	v_mfma_f32_16x16x32_bf16 v[74:77], v[172:175], v[196:199], v[74:77]
	v_mfma_f32_16x16x32_bf16 v[70:73], v[164:167], v[204:207], v[70:73]
	v_mfma_f32_16x16x32_bf16 v[66:69], v[172:175], v[204:207], v[66:69]
	s_setprio 0
	s_barrier
	s_mov_b32 m0, s29
	v_lshl_add_u64 v[208:209], v[208:209], 0, s[4:5]
	s_add_u32 s6, s10, 0x80080
	ds_read_b128 v[176:179], v141 offset:49152
	ds_read_b128 v[180:183], v141 offset:50176
	ds_read_b128 v[184:187], v141 offset:51200
	ds_read_b128 v[188:191], v141 offset:52224
	ds_read_b128 v[192:195], v141 offset:53248
	ds_read_b128 v[196:199], v141 offset:54272
	ds_read_b128 v[200:203], v141 offset:55296
	ds_read_b128 v[204:207], v141 offset:56320
	global_load_lds_dwordx4 v[208:209], off
	v_lshl_add_u64 v[208:209], v[210:211], 0, s[4:5]
	s_mov_b32 m0, s30
	s_addc_u32 s7, s11, 0
	global_load_lds_dwordx4 v[208:209], off
	v_lshl_add_u64 v[208:209], s[6:7], 0, v[132:133]
	s_mov_b32 m0, s31
	s_nop 0
	global_load_lds_dwordx4 v[208:209], off
	v_lshl_add_u64 v[208:209], s[6:7], 0, v[130:131]
	s_mov_b32 m0, s33
	s_nop 0
	global_load_lds_dwordx4 v[208:209], off
	v_lshl_add_u64 v[208:209], v[212:213], 0, s[4:5]
	s_mov_b32 m0, s20
	s_nop 0
	global_load_lds_dwordx4 v[208:209], off
	v_lshl_add_u64 v[208:209], v[214:215], 0, s[4:5]
	s_mov_b32 m0, s21
	s_nop 0
	global_load_lds_dwordx4 v[208:209], off
	s_waitcnt vmcnt(8)
	s_waitcnt lgkmcnt(0)
	s_barrier
	s_setprio 1
	s_waitcnt lgkmcnt(0)
	v_mfma_f32_16x16x32_bf16 v[62:65], v[144:147], v[176:179], v[62:65]
	v_mfma_f32_16x16x32_bf16 v[58:61], v[152:155], v[176:179], v[58:61]
	v_mfma_f32_16x16x32_bf16 v[54:57], v[144:147], v[184:187], v[54:57]
	v_mfma_f32_16x16x32_bf16 v[50:53], v[152:155], v[184:187], v[50:53]
	v_mfma_f32_16x16x32_bf16 v[42:45], v[144:147], v[192:195], v[42:45]
	v_mfma_f32_16x16x32_bf16 v[34:37], v[152:155], v[192:195], v[34:37]
	v_mfma_f32_16x16x32_bf16 v[26:29], v[144:147], v[200:203], v[26:29]
	v_mfma_f32_16x16x32_bf16 v[18:21], v[152:155], v[200:203], v[18:21]
	v_mfma_f32_16x16x32_bf16 v[62:65], v[148:151], v[180:183], v[62:65]
	v_mfma_f32_16x16x32_bf16 v[58:61], v[156:159], v[180:183], v[58:61]
	v_mfma_f32_16x16x32_bf16 v[54:57], v[148:151], v[188:191], v[54:57]
	v_mfma_f32_16x16x32_bf16 v[50:53], v[156:159], v[188:191], v[50:53]
	v_mfma_f32_16x16x32_bf16 v[42:45], v[148:151], v[196:199], v[42:45]
	v_mfma_f32_16x16x32_bf16 v[34:37], v[156:159], v[196:199], v[34:37]
	v_mfma_f32_16x16x32_bf16 v[26:29], v[148:151], v[204:207], v[26:29]
	v_mfma_f32_16x16x32_bf16 v[18:21], v[156:159], v[204:207], v[18:21]
	v_mfma_f32_16x16x32_bf16 v[46:49], v[160:163], v[176:179], v[46:49]
	v_mfma_f32_16x16x32_bf16 v[38:41], v[168:171], v[176:179], v[38:41]
	v_mfma_f32_16x16x32_bf16 v[30:33], v[160:163], v[184:187], v[30:33]
	v_mfma_f32_16x16x32_bf16 v[22:25], v[168:171], v[184:187], v[22:25]
	v_mfma_f32_16x16x32_bf16 v[14:17], v[160:163], v[192:195], v[14:17]
	v_mfma_f32_16x16x32_bf16 v[10:13], v[168:171], v[192:195], v[10:13]
	v_mfma_f32_16x16x32_bf16 v[6:9], v[160:163], v[200:203], v[6:9]
	v_mfma_f32_16x16x32_bf16 v[2:5], v[168:171], v[200:203], v[2:5]
	v_mfma_f32_16x16x32_bf16 v[46:49], v[164:167], v[180:183], v[46:49]
	v_mfma_f32_16x16x32_bf16 v[38:41], v[172:175], v[180:183], v[38:41]
	v_mfma_f32_16x16x32_bf16 v[30:33], v[164:167], v[188:191], v[30:33]
	v_mfma_f32_16x16x32_bf16 v[22:25], v[172:175], v[188:191], v[22:25]
	v_mfma_f32_16x16x32_bf16 v[14:17], v[164:167], v[196:199], v[14:17]
	v_mfma_f32_16x16x32_bf16 v[10:13], v[172:175], v[196:199], v[10:13]
	v_mfma_f32_16x16x32_bf16 v[6:9], v[164:167], v[204:207], v[6:9]
	v_mfma_f32_16x16x32_bf16 v[2:5], v[172:175], v[204:207], v[2:5]
	s_setprio 0
	s_barrier
	s_add_i32 s22, s22, 2
	s_cmp_gt_u32 s22, 29
	s_mov_b64 s[6:7], s[8:9]
	s_cbranch_scc0 .LBB0_368
	s_cmpk_lt_u32 s14, 0x100
	s_cbranch_scc0 .LBB0_371
	s_barrier

.LBB0_372:
	s_waitcnt vmcnt(0)
	s_waitcnt vmcnt(0)
	s_barrier
	s_mov_b64 s[0:1], exec
	v_readlane_b32 s2, v252, 11
	v_readlane_b32 s3, v252, 12
	s_and_b64 s[2:3], s[0:1], s[2:3]
	s_mov_b64 exec, s[2:3]
	s_cbranch_execz .LBB0_424
	s_add_i32 s2, 0, 0x26f20
	v_mov_b32_e32 v0, s2
	s_waitcnt vmcnt(0) expcnt(0) lgkmcnt(0)
	ds_read_b32 v3, v0
	s_add_i32 s2, 0, 0x26f24
	v_mov_b32_e32 v0, s2
	ds_read_b32 v1, v0
	s_waitcnt lgkmcnt(1)
	v_cmp_ne_u32_e32 vcc, 0, v3
	s_cbranch_vccnz .LBB0_388
	v_readlane_b32 s2, v252, 4
	v_readlane_b32 s3, v252, 5
	s_load_dwordx2 s[6:7], s[2:3], 0x4
	v_readlane_b32 s36, v252, 2
	v_readlane_b32 s37, v252, 3
	s_add_u32 s2, s36, 0x4200
	s_addc_u32 s3, s37, 0
	s_add_u32 s4, s36, 0x4400
	s_addc_u32 s5, s37, 0
	v_readlane_b32 s8, v252, 6
	s_waitcnt lgkmcnt(0)
	s_mul_i32 s33, s6, s8
	s_add_u32 s6, s36, 0x4500
	s_mul_i32 s33, s33, s7
	s_addc_u32 s7, s37, 0
	v_readlane_b32 s9, v252, 7
	s_add_u32 s8, s36, 0x4600
	s_addc_u32 s9, s37, 0
	s_add_u32 s10, s36, 0x4700
	s_addc_u32 s11, s37, 0
	s_add_u32 s12, s36, 0x4800
	s_addc_u32 s13, s37, 0
	s_add_u32 s14, s36, 0x4900
	s_addc_u32 s15, s37, 0
	s_add_u32 s16, s36, 0x4a00
	s_addc_u32 s17, s37, 0
	s_add_u32 s18, s36, 0x4b00
	s_addc_u32 s19, s37, 0
	s_add_u32 s20, s36, 0x4c00
	s_addc_u32 s21, s37, 0
	s_add_u32 s22, s36, 0x4d00
	s_addc_u32 s23, s37, 0
	s_add_u32 s24, s36, 0x4e00
	s_addc_u32 s25, s37, 0
	s_add_u32 s26, s36, 0x4f00
	s_addc_u32 s27, s37, 0
	s_add_u32 s28, s36, 0x5000
	s_addc_u32 s29, s37, 0
	s_add_u32 s30, s36, 0x5100
	s_addc_u32 s31, s37, 0
	s_add_u32 s34, s36, 0x5200
	s_addc_u32 s35, s37, 0
	s_add_u32 s38, s36, 0x5300
	s_addc_u32 s39, s37, 0
	s_mov_b32 s36, 1
	v_mov_b32_e32 v17, 0
	s_branch .LBB0_376
	s_nop 0
	s_nop 0
	s_nop 0
	s_nop 0
	s_nop 0
	s_nop 0
	s_nop 0
	s_nop 0

.LBB0_981:
	s_ashr_i32 s11, s10, 31
	s_lshl_b64 s[12:13], s[10:11], 20
	s_add_u32 s12, s24, s12
	s_addc_u32 s13, s25, s13
	s_and_b64 s[14:15], s[4:5], exec
	s_cselect_b32 s11, s13, s19
	s_cselect_b32 s41, s12, s18
	s_ashr_i32 s9, s8, 31
	s_lshl_b64 s[14:15], s[8:9], 20
	s_add_u32 s14, s27, s14
	s_addc_u32 s15, s28, s15
	s_and_b64 s[22:23], s[4:5], exec
	s_cselect_b32 s9, s15, s21
	s_cselect_b32 s42, s14, s20
	s_add_u32 s18, s18, 0x80080
	s_addc_u32 s19, s19, 0
	s_add_u32 s43, s20, 0x100
	s_addc_u32 s44, s21, 0
	s_mov_b32 s45, -2
	ds_read_b128 v[146:149], v154
	ds_read_b128 v[158:161], v154 offset:1024
	ds_read_b128 v[162:165], v154 offset:2048
	ds_read_b128 v[166:169], v154 offset:3072
	ds_read_b128 v[170:173], v155
	ds_read_b128 v[174:177], v155 offset:1024
	ds_read_b128 v[178:181], v155 offset:2048
	ds_read_b128 v[182:185], v155 offset:3072
	s_add_u32 s20, s18, 0xfff80080
	s_addc_u32 s21, s19, -1
	s_cmp_eq_u32 s45, 28
	s_cselect_b32 s23, s11, s21
	s_cselect_b32 s22, s41, s20
	s_cselect_b32 s21, s9, s44
	s_cselect_b32 s20, s42, s43
	v_lshl_add_u64 v[150:151], s[18:19], 0, v[138:139]
	s_add_i32 m0, s17, 0xc000
	ds_read_b128 v[186:189], v156
	ds_read_b128 v[190:193], v156 offset:1024
	ds_read_b128 v[194:197], v156 offset:2048
	ds_read_b128 v[198:201], v156 offset:3072
	ds_read_b128 v[202:205], v156 offset:4096
	ds_read_b128 v[206:209], v156 offset:5120
	ds_read_b128 v[210:213], v156 offset:6144
	ds_read_b128 v[214:217], v156 offset:7168
	global_load_lds_dwordx4 v[150:151], off
	v_lshl_add_u64 v[150:151], s[18:19], 0, v[140:141]
	s_add_i32 m0, s17, 0xe000
	s_nop 0
	global_load_lds_dwordx4 v[150:151], off
	s_waitcnt vmcnt(40)
	s_waitcnt lgkmcnt(0)
	s_barrier
	s_setprio 1
	s_waitcnt lgkmcnt(0)
	v_mfma_f32_16x16x32_bf16 v[126:129], v[146:149], v[186:189], 0
	v_mfma_f32_16x16x32_bf16 v[122:125], v[162:165], v[186:189], 0
	v_mfma_f32_16x16x32_bf16 v[118:121], v[146:149], v[194:197], 0
	v_mfma_f32_16x16x32_bf16 v[114:117], v[162:165], v[194:197], 0
	v_mfma_f32_16x16x32_bf16 v[106:109], v[146:149], v[202:205], 0
	v_mfma_f32_16x16x32_bf16 v[98:101], v[162:165], v[202:205], 0
	v_mfma_f32_16x16x32_bf16 v[86:89], v[146:149], v[210:213], 0
	v_mfma_f32_16x16x32_bf16 v[78:81], v[162:165], v[210:213], 0
	v_mfma_f32_16x16x32_bf16 v[126:129], v[158:161], v[190:193], v[126:129]
	v_mfma_f32_16x16x32_bf16 v[122:125], v[166:169], v[190:193], v[122:125]
	v_mfma_f32_16x16x32_bf16 v[118:121], v[158:161], v[198:201], v[118:121]
	v_mfma_f32_16x16x32_bf16 v[114:117], v[166:169], v[198:201], v[114:117]
	v_mfma_f32_16x16x32_bf16 v[106:109], v[158:161], v[206:209], v[106:109]
	v_mfma_f32_16x16x32_bf16 v[98:101], v[166:169], v[206:209], v[98:101]
	v_mfma_f32_16x16x32_bf16 v[86:89], v[158:161], v[214:217], v[86:89]
	v_mfma_f32_16x16x32_bf16 v[78:81], v[166:169], v[214:217], v[78:81]
	v_mfma_f32_16x16x32_bf16 v[110:113], v[170:173], v[186:189], 0
	v_mfma_f32_16x16x32_bf16 v[102:105], v[178:181], v[186:189], 0
	v_mfma_f32_16x16x32_bf16 v[94:97], v[170:173], v[194:197], 0
	v_mfma_f32_16x16x32_bf16 v[90:93], v[178:181], v[194:197], 0
	v_mfma_f32_16x16x32_bf16 v[82:85], v[170:173], v[202:205], 0
	v_mfma_f32_16x16x32_bf16 v[74:77], v[178:181], v[202:205], 0
	v_mfma_f32_16x16x32_bf16 v[70:73], v[170:173], v[210:213], 0
	v_mfma_f32_16x16x32_bf16 v[66:69], v[178:181], v[210:213], 0
	v_mfma_f32_16x16x32_bf16 v[110:113], v[174:177], v[190:193], v[110:113]
	v_mfma_f32_16x16x32_bf16 v[102:105], v[182:185], v[190:193], v[102:105]
	v_mfma_f32_16x16x32_bf16 v[94:97], v[174:177], v[198:201], v[94:97]
	v_mfma_f32_16x16x32_bf16 v[90:93], v[182:185], v[198:201], v[90:93]
	v_mfma_f32_16x16x32_bf16 v[82:85], v[174:177], v[206:209], v[82:85]
	v_mfma_f32_16x16x32_bf16 v[74:77], v[182:185], v[206:209], v[74:77]
	v_mfma_f32_16x16x32_bf16 v[70:73], v[174:177], v[214:217], v[70:73]
	v_mfma_f32_16x16x32_bf16 v[66:69], v[182:185], v[214:217], v[66:69]
	s_setprio 0
	s_barrier
	s_add_i32 s46, s38, s29
	v_lshl_add_u64 v[150:151], s[20:21], 0, v[132:133]
	s_mov_b32 m0, s46
	ds_read_b128 v[186:189], v156 offset:16384
	ds_read_b128 v[190:193], v156 offset:17408
	ds_read_b128 v[194:197], v156 offset:18432
	ds_read_b128 v[198:201], v156 offset:19456
	ds_read_b128 v[202:205], v156 offset:20480
	ds_read_b128 v[206:209], v156 offset:21504
	ds_read_b128 v[210:213], v156 offset:22528
	ds_read_b128 v[214:217], v156 offset:23552
	global_load_lds_dwordx4 v[150:151], off
	s_add_i32 m0, s46, 0x2000
	s_add_u32 s46, s20, 0x80000
	v_lshl_add_u64 v[218:219], s[20:21], 0, v[136:137]
	s_addc_u32 s47, s21, 0
	s_add_i32 s48, s39, s29
	global_load_lds_dwordx4 v[218:219], off
	v_lshl_add_u64 v[220:221], s[46:47], 0, v[132:133]
	s_mov_b32 m0, s48
	v_lshl_add_u64 v[222:223], s[22:23], 0, v[134:135]
	global_load_lds_dwordx4 v[220:221], off
	v_lshl_add_u64 v[220:221], s[46:47], 0, v[136:137]
	s_add_i32 m0, s48, 0x2000
	s_nop 0
	global_load_lds_dwordx4 v[220:221], off
	v_lshl_add_u64 v[220:221], s[22:23], 0, v[130:131]
	s_mov_b32 m0, s17
	s_nop 0
	global_load_lds_dwordx4 v[220:221], off
	s_mov_b32 m0, s30
	s_nop 0
	global_load_lds_dwordx4 v[222:223], off
	s_waitcnt vmcnt(8)
	s_waitcnt lgkmcnt(0)
	s_barrier
	s_setprio 1
	s_waitcnt lgkmcnt(0)
	v_mfma_f32_16x16x32_bf16 v[62:65], v[146:149], v[186:189], 0
	v_mfma_f32_16x16x32_bf16 v[58:61], v[162:165], v[186:189], 0
	v_mfma_f32_16x16x32_bf16 v[50:53], v[146:149], v[194:197], 0
	v_mfma_f32_16x16x32_bf16 v[42:45], v[162:165], v[194:197], 0
	v_mfma_f32_16x16x32_bf16 v[38:41], v[146:149], v[202:205], 0
	v_mfma_f32_16x16x32_bf16 v[30:33], v[162:165], v[202:205], 0
	v_mfma_f32_16x16x32_bf16 v[22:25], v[146:149], v[210:213], 0
	v_mfma_f32_16x16x32_bf16 v[14:17], v[162:165], v[210:213], 0
	v_mfma_f32_16x16x32_bf16 v[62:65], v[158:161], v[190:193], v[62:65]
	v_mfma_f32_16x16x32_bf16 v[58:61], v[166:169], v[190:193], v[58:61]
	v_mfma_f32_16x16x32_bf16 v[50:53], v[158:161], v[198:201], v[50:53]
	v_mfma_f32_16x16x32_bf16 v[42:45], v[166:169], v[198:201], v[42:45]
	v_mfma_f32_16x16x32_bf16 v[38:41], v[158:161], v[206:209], v[38:41]
	v_mfma_f32_16x16x32_bf16 v[30:33], v[166:169], v[206:209], v[30:33]
	v_mfma_f32_16x16x32_bf16 v[22:25], v[158:161], v[214:217], v[22:25]
	v_mfma_f32_16x16x32_bf16 v[14:17], v[166:169], v[214:217], v[14:17]
	v_mfma_f32_16x16x32_bf16 v[54:57], v[170:173], v[186:189], 0
	v_mfma_f32_16x16x32_bf16 v[46:49], v[178:181], v[186:189], 0
	v_mfma_f32_16x16x32_bf16 v[34:37], v[170:173], v[194:197], 0
	v_mfma_f32_16x16x32_bf16 v[26:29], v[178:181], v[194:197], 0
	v_mfma_f32_16x16x32_bf16 v[18:21], v[170:173], v[202:205], 0
	v_mfma_f32_16x16x32_bf16 v[10:13], v[178:181], v[202:205], 0
	v_mfma_f32_16x16x32_bf16 v[6:9], v[170:173], v[210:213], 0
	v_mfma_f32_16x16x32_bf16 v[2:5], v[178:181], v[210:213], 0
	v_mfma_f32_16x16x32_bf16 v[54:57], v[174:177], v[190:193], v[54:57]
	v_mfma_f32_16x16x32_bf16 v[46:49], v[182:185], v[190:193], v[46:49]
	v_mfma_f32_16x16x32_bf16 v[34:37], v[174:177], v[198:201], v[34:37]
	v_mfma_f32_16x16x32_bf16 v[26:29], v[182:185], v[198:201], v[26:29]
	v_mfma_f32_16x16x32_bf16 v[18:21], v[174:177], v[206:209], v[18:21]
	v_mfma_f32_16x16x32_bf16 v[10:13], v[182:185], v[206:209], v[10:13]
	v_mfma_f32_16x16x32_bf16 v[6:9], v[174:177], v[214:217], v[6:9]
	v_mfma_f32_16x16x32_bf16 v[2:5], v[182:185], v[214:217], v[2:5]
	s_setprio 0
	s_barrier
	s_add_i32 s46, 0, 0x18000
	v_add_u32_e32 v0, s46, v152
	s_add_i32 s47, 0, 0x1c000
	ds_read_b128 v[146:149], v0
	ds_read_b128 v[158:161], v0 offset:1024
	ds_read_b128 v[162:165], v0 offset:2048
	ds_read_b128 v[166:169], v0 offset:3072
	v_add_u32_e32 v0, s47, v152
	ds_read_b128 v[170:173], v0
	ds_read_b128 v[174:177], v0 offset:1024
	ds_read_b128 v[178:181], v0 offset:2048
	ds_read_b128 v[182:185], v0 offset:3072
	s_add_u32 s22, s22, 0x80000
	s_addc_u32 s23, s23, 0
	s_mov_b32 m0, s31
	v_lshl_add_u64 v[224:225], s[22:23], 0, v[130:131]
	ds_read_b128 v[186:189], v156 offset:32768
	ds_read_b128 v[190:193], v156 offset:33792
	ds_read_b128 v[194:197], v156 offset:34816
	ds_read_b128 v[198:201], v156 offset:35840
	ds_read_b128 v[202:205], v156 offset:36864
	ds_read_b128 v[206:209], v156 offset:37888
	ds_read_b128 v[210:213], v156 offset:38912
	ds_read_b128 v[214:217], v156 offset:39936
	global_load_lds_dwordx4 v[224:225], off
	v_lshl_add_u64 v[224:225], s[22:23], 0, v[134:135]
	s_mov_b32 m0, s33
	s_nop 0
	global_load_lds_dwordx4 v[224:225], off
	s_waitcnt vmcnt(8)
	s_waitcnt lgkmcnt(0)
	s_barrier
	s_setprio 1
	s_waitcnt lgkmcnt(0)
	v_mfma_f32_16x16x32_bf16 v[126:129], v[146:149], v[186:189], v[126:129]
	v_mfma_f32_16x16x32_bf16 v[122:125], v[162:165], v[186:189], v[122:125]
	v_mfma_f32_16x16x32_bf16 v[118:121], v[146:149], v[194:197], v[118:121]
	v_mfma_f32_16x16x32_bf16 v[114:117], v[162:165], v[194:197], v[114:117]
	v_mfma_f32_16x16x32_bf16 v[106:109], v[146:149], v[202:205], v[106:109]
	v_mfma_f32_16x16x32_bf16 v[98:101], v[162:165], v[202:205], v[98:101]
	v_mfma_f32_16x16x32_bf16 v[86:89], v[146:149], v[210:213], v[86:89]
	v_mfma_f32_16x16x32_bf16 v[78:81], v[162:165], v[210:213], v[78:81]
	v_mfma_f32_16x16x32_bf16 v[126:129], v[158:161], v[190:193], v[126:129]
	v_mfma_f32_16x16x32_bf16 v[122:125], v[166:169], v[190:193], v[122:125]
	v_mfma_f32_16x16x32_bf16 v[118:121], v[158:161], v[198:201], v[118:121]
	v_mfma_f32_16x16x32_bf16 v[114:117], v[166:169], v[198:201], v[114:117]
	v_mfma_f32_16x16x32_bf16 v[106:109], v[158:161], v[206:209], v[106:109]
	v_mfma_f32_16x16x32_bf16 v[98:101], v[166:169], v[206:209], v[98:101]
	v_mfma_f32_16x16x32_bf16 v[86:89], v[158:161], v[214:217], v[86:89]
	v_mfma_f32_16x16x32_bf16 v[78:81], v[166:169], v[214:217], v[78:81]
	v_mfma_f32_16x16x32_bf16 v[110:113], v[170:173], v[186:189], v[110:113]
	v_mfma_f32_16x16x32_bf16 v[102:105], v[178:181], v[186:189], v[102:105]
	v_mfma_f32_16x16x32_bf16 v[94:97], v[170:173], v[194:197], v[94:97]
	v_mfma_f32_16x16x32_bf16 v[90:93], v[178:181], v[194:197], v[90:93]
	v_mfma_f32_16x16x32_bf16 v[82:85], v[170:173], v[202:205], v[82:85]
	v_mfma_f32_16x16x32_bf16 v[74:77], v[178:181], v[202:205], v[74:77]
	v_mfma_f32_16x16x32_bf16 v[70:73], v[170:173], v[210:213], v[70:73]
	v_mfma_f32_16x16x32_bf16 v[66:69], v[178:181], v[210:213], v[66:69]
	v_mfma_f32_16x16x32_bf16 v[110:113], v[174:177], v[190:193], v[110:113]
	v_mfma_f32_16x16x32_bf16 v[102:105], v[182:185], v[190:193], v[102:105]
	v_mfma_f32_16x16x32_bf16 v[94:97], v[174:177], v[198:201], v[94:97]
	v_mfma_f32_16x16x32_bf16 v[90:93], v[182:185], v[198:201], v[90:93]
	v_mfma_f32_16x16x32_bf16 v[82:85], v[174:177], v[206:209], v[82:85]
	v_mfma_f32_16x16x32_bf16 v[74:77], v[182:185], v[206:209], v[74:77]
	v_mfma_f32_16x16x32_bf16 v[70:73], v[174:177], v[214:217], v[70:73]
	v_mfma_f32_16x16x32_bf16 v[66:69], v[182:185], v[214:217], v[66:69]
	s_setprio 0
	s_barrier
	s_add_i32 s22, s46, s29
	v_lshl_add_u64 v[150:151], v[150:151], 0, s[2:3]
	s_mov_b32 m0, s22
	ds_read_b128 v[186:189], v156 offset:49152
	ds_read_b128 v[190:193], v156 offset:50176
	ds_read_b128 v[194:197], v156 offset:51200
	ds_read_b128 v[198:201], v156 offset:52224
	ds_read_b128 v[202:205], v156 offset:53248
	ds_read_b128 v[206:209], v156 offset:54272
	ds_read_b128 v[210:213], v156 offset:55296
	ds_read_b128 v[214:217], v156 offset:56320
	global_load_lds_dwordx4 v[150:151], off
	s_add_i32 m0, s22, 0x2000
	s_add_u32 s20, s20, 0x80080
	v_lshl_add_u64 v[150:151], v[218:219], 0, s[2:3]
	s_addc_u32 s21, s21, 0
	s_add_i32 s22, s47, s29
	global_load_lds_dwordx4 v[150:151], off
	v_lshl_add_u64 v[150:151], s[20:21], 0, v[132:133]
	s_mov_b32 m0, s22
	s_nop 0
	global_load_lds_dwordx4 v[150:151], off
	v_lshl_add_u64 v[150:151], s[20:21], 0, v[136:137]
	s_add_i32 m0, s22, 0x2000
	s_nop 0
	global_load_lds_dwordx4 v[150:151], off
	v_lshl_add_u64 v[150:151], v[220:221], 0, s[2:3]
	s_mov_b32 m0, s35
	s_nop 0
	global_load_lds_dwordx4 v[150:151], off
	v_lshl_add_u64 v[150:151], v[222:223], 0, s[2:3]
	s_mov_b32 m0, s36
	s_nop 0
	global_load_lds_dwordx4 v[150:151], off
	s_waitcnt vmcnt(8)
	s_waitcnt lgkmcnt(0)
	s_barrier
	s_setprio 1
	s_waitcnt lgkmcnt(0)
	v_mfma_f32_16x16x32_bf16 v[62:65], v[146:149], v[186:189], v[62:65]
	v_mfma_f32_16x16x32_bf16 v[58:61], v[162:165], v[186:189], v[58:61]
	v_mfma_f32_16x16x32_bf16 v[50:53], v[146:149], v[194:197], v[50:53]
	v_mfma_f32_16x16x32_bf16 v[42:45], v[162:165], v[194:197], v[42:45]
	v_mfma_f32_16x16x32_bf16 v[38:41], v[146:149], v[202:205], v[38:41]
	v_mfma_f32_16x16x32_bf16 v[30:33], v[162:165], v[202:205], v[30:33]
	v_mfma_f32_16x16x32_bf16 v[22:25], v[146:149], v[210:213], v[22:25]
	v_mfma_f32_16x16x32_bf16 v[14:17], v[162:165], v[210:213], v[14:17]
	v_mfma_f32_16x16x32_bf16 v[62:65], v[158:161], v[190:193], v[62:65]
	v_mfma_f32_16x16x32_bf16 v[58:61], v[166:169], v[190:193], v[58:61]
	v_mfma_f32_16x16x32_bf16 v[50:53], v[158:161], v[198:201], v[50:53]
	v_mfma_f32_16x16x32_bf16 v[42:45], v[166:169], v[198:201], v[42:45]
	v_mfma_f32_16x16x32_bf16 v[38:41], v[158:161], v[206:209], v[38:41]
	v_mfma_f32_16x16x32_bf16 v[30:33], v[166:169], v[206:209], v[30:33]
	v_mfma_f32_16x16x32_bf16 v[22:25], v[158:161], v[214:217], v[22:25]
	v_mfma_f32_16x16x32_bf16 v[14:17], v[166:169], v[214:217], v[14:17]
	v_mfma_f32_16x16x32_bf16 v[54:57], v[170:173], v[186:189], v[54:57]
	v_mfma_f32_16x16x32_bf16 v[46:49], v[178:181], v[186:189], v[46:49]
	v_mfma_f32_16x16x32_bf16 v[34:37], v[170:173], v[194:197], v[34:37]
	v_mfma_f32_16x16x32_bf16 v[26:29], v[178:181], v[194:197], v[26:29]
	v_mfma_f32_16x16x32_bf16 v[18:21], v[170:173], v[202:205], v[18:21]
	v_mfma_f32_16x16x32_bf16 v[10:13], v[178:181], v[202:205], v[10:13]
	v_mfma_f32_16x16x32_bf16 v[6:9], v[170:173], v[210:213], v[6:9]
	v_mfma_f32_16x16x32_bf16 v[2:5], v[178:181], v[210:213], v[2:5]
	v_mfma_f32_16x16x32_bf16 v[54:57], v[174:177], v[190:193], v[54:57]
	v_mfma_f32_16x16x32_bf16 v[46:49], v[182:185], v[190:193], v[46:49]
	v_mfma_f32_16x16x32_bf16 v[34:37], v[174:177], v[198:201], v[34:37]
	v_mfma_f32_16x16x32_bf16 v[26:29], v[182:185], v[198:201], v[26:29]
	v_mfma_f32_16x16x32_bf16 v[18:21], v[174:177], v[206:209], v[18:21]
	v_mfma_f32_16x16x32_bf16 v[10:13], v[182:185], v[206:209], v[10:13]
	v_mfma_f32_16x16x32_bf16 v[6:9], v[174:177], v[214:217], v[6:9]
	v_mfma_f32_16x16x32_bf16 v[2:5], v[182:185], v[214:217], v[2:5]
	s_setprio 0
	s_barrier
	s_add_i32 s45, s45, 2
	s_add_u32 s18, s18, 0x100
	s_addc_u32 s19, s19, 0
	s_add_u32 s43, s43, 0x100
	s_addc_u32 s44, s44, 0
	s_cmp_gt_u32 s45, 29
	s_cbranch_scc0 .LBB0_982
	s_branch .Lkexit_982
	s_nop 0
	s_nop 0
	s_nop 0
	s_nop 0
	s_nop 0
	s_nop 0
	s_nop 0
	s_nop 0
	s_nop 0
	s_nop 0
	s_nop 0
	s_nop 0
	s_nop 0
	s_nop 0
	s_nop 0
	s_nop 0
.LBB0_982:
	ds_read_b128 v[146:149], v154
	ds_read_b128 v[158:161], v154 offset:1024
	ds_read_b128 v[162:165], v154 offset:2048
	ds_read_b128 v[166:169], v154 offset:3072
	ds_read_b128 v[170:173], v155
	ds_read_b128 v[174:177], v155 offset:1024
	ds_read_b128 v[178:181], v155 offset:2048
	ds_read_b128 v[182:185], v155 offset:3072
	s_add_u32 s20, s18, 0xfff80080
	s_addc_u32 s21, s19, -1
	s_cmp_eq_u32 s45, 28
	s_cselect_b32 s23, s11, s21
	s_cselect_b32 s22, s41, s20
	s_cselect_b32 s21, s9, s44
	s_cselect_b32 s20, s42, s43
	v_lshl_add_u64 v[150:151], s[18:19], 0, v[138:139]
	s_add_i32 m0, s17, 0xc000
	ds_read_b128 v[186:189], v156
	ds_read_b128 v[190:193], v156 offset:1024
	ds_read_b128 v[194:197], v156 offset:2048
	ds_read_b128 v[198:201], v156 offset:3072
	ds_read_b128 v[202:205], v156 offset:4096
	ds_read_b128 v[206:209], v156 offset:5120
	ds_read_b128 v[210:213], v156 offset:6144
	ds_read_b128 v[214:217], v156 offset:7168
	global_load_lds_dwordx4 v[150:151], off
	v_lshl_add_u64 v[150:151], s[18:19], 0, v[140:141]
	s_add_i32 m0, s17, 0xe000
	s_nop 0
	global_load_lds_dwordx4 v[150:151], off
	s_waitcnt vmcnt(8)
	s_waitcnt lgkmcnt(0)
	s_barrier
	s_setprio 1
	s_waitcnt lgkmcnt(0)
	v_mfma_f32_16x16x32_bf16 v[126:129], v[146:149], v[186:189], v[126:129]
	v_mfma_f32_16x16x32_bf16 v[122:125], v[162:165], v[186:189], v[122:125]
	v_mfma_f32_16x16x32_bf16 v[118:121], v[146:149], v[194:197], v[118:121]
	v_mfma_f32_16x16x32_bf16 v[114:117], v[162:165], v[194:197], v[114:117]
	v_mfma_f32_16x16x32_bf16 v[106:109], v[146:149], v[202:205], v[106:109]
	v_mfma_f32_16x16x32_bf16 v[98:101], v[162:165], v[202:205], v[98:101]
	v_mfma_f32_16x16x32_bf16 v[86:89], v[146:149], v[210:213], v[86:89]
	v_mfma_f32_16x16x32_bf16 v[78:81], v[162:165], v[210:213], v[78:81]
	v_mfma_f32_16x16x32_bf16 v[126:129], v[158:161], v[190:193], v[126:129]
	v_mfma_f32_16x16x32_bf16 v[122:125], v[166:169], v[190:193], v[122:125]
	v_mfma_f32_16x16x32_bf16 v[118:121], v[158:161], v[198:201], v[118:121]
	v_mfma_f32_16x16x32_bf16 v[114:117], v[166:169], v[198:201], v[114:117]
	v_mfma_f32_16x16x32_bf16 v[106:109], v[158:161], v[206:209], v[106:109]
	v_mfma_f32_16x16x32_bf16 v[98:101], v[166:169], v[206:209], v[98:101]
	v_mfma_f32_16x16x32_bf16 v[86:89], v[158:161], v[214:217], v[86:89]
	v_mfma_f32_16x16x32_bf16 v[78:81], v[166:169], v[214:217], v[78:81]
	v_mfma_f32_16x16x32_bf16 v[110:113], v[170:173], v[186:189], v[110:113]
	v_mfma_f32_16x16x32_bf16 v[102:105], v[178:181], v[186:189], v[102:105]
	v_mfma_f32_16x16x32_bf16 v[94:97], v[170:173], v[194:197], v[94:97]
	v_mfma_f32_16x16x32_bf16 v[90:93], v[178:181], v[194:197], v[90:93]
	v_mfma_f32_16x16x32_bf16 v[82:85], v[170:173], v[202:205], v[82:85]
	v_mfma_f32_16x16x32_bf16 v[74:77], v[178:181], v[202:205], v[74:77]
	v_mfma_f32_16x16x32_bf16 v[70:73], v[170:173], v[210:213], v[70:73]
	v_mfma_f32_16x16x32_bf16 v[66:69], v[178:181], v[210:213], v[66:69]
	v_mfma_f32_16x16x32_bf16 v[110:113], v[174:177], v[190:193], v[110:113]
	v_mfma_f32_16x16x32_bf16 v[102:105], v[182:185], v[190:193], v[102:105]
	v_mfma_f32_16x16x32_bf16 v[94:97], v[174:177], v[198:201], v[94:97]
	v_mfma_f32_16x16x32_bf16 v[90:93], v[182:185], v[198:201], v[90:93]
	v_mfma_f32_16x16x32_bf16 v[82:85], v[174:177], v[206:209], v[82:85]
	v_mfma_f32_16x16x32_bf16 v[74:77], v[182:185], v[206:209], v[74:77]
	v_mfma_f32_16x16x32_bf16 v[70:73], v[174:177], v[214:217], v[70:73]
	v_mfma_f32_16x16x32_bf16 v[66:69], v[182:185], v[214:217], v[66:69]
	s_setprio 0
	s_barrier
	s_add_i32 s46, s38, s29
	v_lshl_add_u64 v[150:151], s[20:21], 0, v[132:133]
	s_mov_b32 m0, s46
	ds_read_b128 v[186:189], v156 offset:16384
	ds_read_b128 v[190:193], v156 offset:17408
	ds_read_b128 v[194:197], v156 offset:18432
	ds_read_b128 v[198:201], v156 offset:19456
	ds_read_b128 v[202:205], v156 offset:20480
	ds_read_b128 v[206:209], v156 offset:21504
	ds_read_b128 v[210:213], v156 offset:22528
	ds_read_b128 v[214:217], v156 offset:23552
	global_load_lds_dwordx4 v[150:151], off
	s_add_i32 m0, s46, 0x2000
	s_add_u32 s46, s20, 0x80000
	v_lshl_add_u64 v[218:219], s[20:21], 0, v[136:137]
	s_addc_u32 s47, s21, 0
	s_add_i32 s48, s39, s29
	global_load_lds_dwordx4 v[218:219], off
	v_lshl_add_u64 v[220:221], s[46:47], 0, v[132:133]
	s_mov_b32 m0, s48
	v_lshl_add_u64 v[222:223], s[22:23], 0, v[134:135]
	global_load_lds_dwordx4 v[220:221], off
	v_lshl_add_u64 v[220:221], s[46:47], 0, v[136:137]
	s_add_i32 m0, s48, 0x2000
	s_nop 0
	global_load_lds_dwordx4 v[220:221], off
	v_lshl_add_u64 v[220:221], s[22:23], 0, v[130:131]
	s_mov_b32 m0, s17
	s_nop 0
	global_load_lds_dwordx4 v[220:221], off
	s_mov_b32 m0, s30
	s_nop 0
	global_load_lds_dwordx4 v[222:223], off
	s_waitcnt vmcnt(8)
	s_waitcnt lgkmcnt(0)
	s_barrier
	s_setprio 1
	s_waitcnt lgkmcnt(0)
	v_mfma_f32_16x16x32_bf16 v[62:65], v[146:149], v[186:189], v[62:65]
	v_mfma_f32_16x16x32_bf16 v[58:61], v[162:165], v[186:189], v[58:61]
	v_mfma_f32_16x16x32_bf16 v[50:53], v[146:149], v[194:197], v[50:53]
	v_mfma_f32_16x16x32_bf16 v[42:45], v[162:165], v[194:197], v[42:45]
	v_mfma_f32_16x16x32_bf16 v[38:41], v[146:149], v[202:205], v[38:41]
	v_mfma_f32_16x16x32_bf16 v[30:33], v[162:165], v[202:205], v[30:33]
	v_mfma_f32_16x16x32_bf16 v[22:25], v[146:149], v[210:213], v[22:25]
	v_mfma_f32_16x16x32_bf16 v[14:17], v[162:165], v[210:213], v[14:17]
	v_mfma_f32_16x16x32_bf16 v[62:65], v[158:161], v[190:193], v[62:65]
	v_mfma_f32_16x16x32_bf16 v[58:61], v[166:169], v[190:193], v[58:61]
	v_mfma_f32_16x16x32_bf16 v[50:53], v[158:161], v[198:201], v[50:53]
	v_mfma_f32_16x16x32_bf16 v[42:45], v[166:169], v[198:201], v[42:45]
	v_mfma_f32_16x16x32_bf16 v[38:41], v[158:161], v[206:209], v[38:41]
	v_mfma_f32_16x16x32_bf16 v[30:33], v[166:169], v[206:209], v[30:33]
	v_mfma_f32_16x16x32_bf16 v[22:25], v[158:161], v[214:217], v[22:25]
	v_mfma_f32_16x16x32_bf16 v[14:17], v[166:169], v[214:217], v[14:17]
	v_mfma_f32_16x16x32_bf16 v[54:57], v[170:173], v[186:189], v[54:57]
	v_mfma_f32_16x16x32_bf16 v[46:49], v[178:181], v[186:189], v[46:49]
	v_mfma_f32_16x16x32_bf16 v[34:37], v[170:173], v[194:197], v[34:37]
	v_mfma_f32_16x16x32_bf16 v[26:29], v[178:181], v[194:197], v[26:29]
	v_mfma_f32_16x16x32_bf16 v[18:21], v[170:173], v[202:205], v[18:21]
	v_mfma_f32_16x16x32_bf16 v[10:13], v[178:181], v[202:205], v[10:13]
	v_mfma_f32_16x16x32_bf16 v[6:9], v[170:173], v[210:213], v[6:9]
	v_mfma_f32_16x16x32_bf16 v[2:5], v[178:181], v[210:213], v[2:5]
	v_mfma_f32_16x16x32_bf16 v[54:57], v[174:177], v[190:193], v[54:57]
	v_mfma_f32_16x16x32_bf16 v[46:49], v[182:185], v[190:193], v[46:49]
	v_mfma_f32_16x16x32_bf16 v[34:37], v[174:177], v[198:201], v[34:37]
	v_mfma_f32_16x16x32_bf16 v[26:29], v[182:185], v[198:201], v[26:29]
	v_mfma_f32_16x16x32_bf16 v[18:21], v[174:177], v[206:209], v[18:21]
	v_mfma_f32_16x16x32_bf16 v[10:13], v[182:185], v[206:209], v[10:13]
	v_mfma_f32_16x16x32_bf16 v[6:9], v[174:177], v[214:217], v[6:9]
	v_mfma_f32_16x16x32_bf16 v[2:5], v[182:185], v[214:217], v[2:5]
	s_setprio 0
	s_barrier
	s_add_i32 s46, 0, 0x18000
	v_add_u32_e32 v0, s46, v152
	s_add_i32 s47, 0, 0x1c000
	ds_read_b128 v[146:149], v0
	ds_read_b128 v[158:161], v0 offset:1024
	ds_read_b128 v[162:165], v0 offset:2048
	ds_read_b128 v[166:169], v0 offset:3072
	v_add_u32_e32 v0, s47, v152
	ds_read_b128 v[170:173], v0
	ds_read_b128 v[174:177], v0 offset:1024
	ds_read_b128 v[178:181], v0 offset:2048
	ds_read_b128 v[182:185], v0 offset:3072
	s_add_u32 s22, s22, 0x80000
	s_addc_u32 s23, s23, 0
	s_mov_b32 m0, s31
	v_lshl_add_u64 v[224:225], s[22:23], 0, v[130:131]
	ds_read_b128 v[186:189], v156 offset:32768
	ds_read_b128 v[190:193], v156 offset:33792
	ds_read_b128 v[194:197], v156 offset:34816
	ds_read_b128 v[198:201], v156 offset:35840
	ds_read_b128 v[202:205], v156 offset:36864
	ds_read_b128 v[206:209], v156 offset:37888
	ds_read_b128 v[210:213], v156 offset:38912
	ds_read_b128 v[214:217], v156 offset:39936
	global_load_lds_dwordx4 v[224:225], off
	v_lshl_add_u64 v[224:225], s[22:23], 0, v[134:135]
	s_mov_b32 m0, s33
	s_nop 0
	global_load_lds_dwordx4 v[224:225], off
	s_waitcnt vmcnt(8)
	s_waitcnt lgkmcnt(0)
	s_barrier
	s_setprio 1
	s_waitcnt lgkmcnt(0)
	v_mfma_f32_16x16x32_bf16 v[126:129], v[146:149], v[186:189], v[126:129]
	v_mfma_f32_16x16x32_bf16 v[122:125], v[162:165], v[186:189], v[122:125]
	v_mfma_f32_16x16x32_bf16 v[118:121], v[146:149], v[194:197], v[118:121]
	v_mfma_f32_16x16x32_bf16 v[114:117], v[162:165], v[194:197], v[114:117]
	v_mfma_f32_16x16x32_bf16 v[106:109], v[146:149], v[202:205], v[106:109]
	v_mfma_f32_16x16x32_bf16 v[98:101], v[162:165], v[202:205], v[98:101]
	v_mfma_f32_16x16x32_bf16 v[86:89], v[146:149], v[210:213], v[86:89]
	v_mfma_f32_16x16x32_bf16 v[78:81], v[162:165], v[210:213], v[78:81]
	v_mfma_f32_16x16x32_bf16 v[126:129], v[158:161], v[190:193], v[126:129]
	v_mfma_f32_16x16x32_bf16 v[122:125], v[166:169], v[190:193], v[122:125]
	v_mfma_f32_16x16x32_bf16 v[118:121], v[158:161], v[198:201], v[118:121]
	v_mfma_f32_16x16x32_bf16 v[114:117], v[166:169], v[198:201], v[114:117]
	v_mfma_f32_16x16x32_bf16 v[106:109], v[158:161], v[206:209], v[106:109]
	v_mfma_f32_16x16x32_bf16 v[98:101], v[166:169], v[206:209], v[98:101]
	v_mfma_f32_16x16x32_bf16 v[86:89], v[158:161], v[214:217], v[86:89]
	v_mfma_f32_16x16x32_bf16 v[78:81], v[166:169], v[214:217], v[78:81]
	v_mfma_f32_16x16x32_bf16 v[110:113], v[170:173], v[186:189], v[110:113]
	v_mfma_f32_16x16x32_bf16 v[102:105], v[178:181], v[186:189], v[102:105]
	v_mfma_f32_16x16x32_bf16 v[94:97], v[170:173], v[194:197], v[94:97]
	v_mfma_f32_16x16x32_bf16 v[90:93], v[178:181], v[194:197], v[90:93]
	v_mfma_f32_16x16x32_bf16 v[82:85], v[170:173], v[202:205], v[82:85]
	v_mfma_f32_16x16x32_bf16 v[74:77], v[178:181], v[202:205], v[74:77]
	v_mfma_f32_16x16x32_bf16 v[70:73], v[170:173], v[210:213], v[70:73]
	v_mfma_f32_16x16x32_bf16 v[66:69], v[178:181], v[210:213], v[66:69]
	v_mfma_f32_16x16x32_bf16 v[110:113], v[174:177], v[190:193], v[110:113]
	v_mfma_f32_16x16x32_bf16 v[102:105], v[182:185], v[190:193], v[102:105]
	v_mfma_f32_16x16x32_bf16 v[94:97], v[174:177], v[198:201], v[94:97]
	v_mfma_f32_16x16x32_bf16 v[90:93], v[182:185], v[198:201], v[90:93]
	v_mfma_f32_16x16x32_bf16 v[82:85], v[174:177], v[206:209], v[82:85]
	v_mfma_f32_16x16x32_bf16 v[74:77], v[182:185], v[206:209], v[74:77]
	v_mfma_f32_16x16x32_bf16 v[70:73], v[174:177], v[214:217], v[70:73]
	v_mfma_f32_16x16x32_bf16 v[66:69], v[182:185], v[214:217], v[66:69]
	s_setprio 0
	s_barrier
	s_add_i32 s22, s46, s29
	v_lshl_add_u64 v[150:151], v[150:151], 0, s[2:3]
	s_mov_b32 m0, s22
	ds_read_b128 v[186:189], v156 offset:49152
	ds_read_b128 v[190:193], v156 offset:50176
	ds_read_b128 v[194:197], v156 offset:51200
	ds_read_b128 v[198:201], v156 offset:52224
	ds_read_b128 v[202:205], v156 offset:53248
	ds_read_b128 v[206:209], v156 offset:54272
	ds_read_b128 v[210:213], v156 offset:55296
	ds_read_b128 v[214:217], v156 offset:56320
	global_load_lds_dwordx4 v[150:151], off
	s_add_i32 m0, s22, 0x2000
	s_add_u32 s20, s20, 0x80080
	v_lshl_add_u64 v[150:151], v[218:219], 0, s[2:3]
	s_addc_u32 s21, s21, 0
	s_add_i32 s22, s47, s29
	global_load_lds_dwordx4 v[150:151], off
	v_lshl_add_u64 v[150:151], s[20:21], 0, v[132:133]
	s_mov_b32 m0, s22
	s_nop 0
	global_load_lds_dwordx4 v[150:151], off
	v_lshl_add_u64 v[150:151], s[20:21], 0, v[136:137]
	s_add_i32 m0, s22, 0x2000
	s_nop 0
	global_load_lds_dwordx4 v[150:151], off
	v_lshl_add_u64 v[150:151], v[220:221], 0, s[2:3]
	s_mov_b32 m0, s35
	s_nop 0
	global_load_lds_dwordx4 v[150:151], off
	v_lshl_add_u64 v[150:151], v[222:223], 0, s[2:3]
	s_mov_b32 m0, s36
	s_nop 0
	global_load_lds_dwordx4 v[150:151], off
	s_waitcnt vmcnt(8)
	s_waitcnt lgkmcnt(0)
	s_barrier
	s_setprio 1
	s_waitcnt lgkmcnt(0)
	v_mfma_f32_16x16x32_bf16 v[62:65], v[146:149], v[186:189], v[62:65]
	v_mfma_f32_16x16x32_bf16 v[58:61], v[162:165], v[186:189], v[58:61]
	v_mfma_f32_16x16x32_bf16 v[50:53], v[146:149], v[194:197], v[50:53]
	v_mfma_f32_16x16x32_bf16 v[42:45], v[162:165], v[194:197], v[42:45]
	v_mfma_f32_16x16x32_bf16 v[38:41], v[146:149], v[202:205], v[38:41]
	v_mfma_f32_16x16x32_bf16 v[30:33], v[162:165], v[202:205], v[30:33]
	v_mfma_f32_16x16x32_bf16 v[22:25], v[146:149], v[210:213], v[22:25]
	v_mfma_f32_16x16x32_bf16 v[14:17], v[162:165], v[210:213], v[14:17]
	v_mfma_f32_16x16x32_bf16 v[62:65], v[158:161], v[190:193], v[62:65]
	v_mfma_f32_16x16x32_bf16 v[58:61], v[166:169], v[190:193], v[58:61]
	v_mfma_f32_16x16x32_bf16 v[50:53], v[158:161], v[198:201], v[50:53]
	v_mfma_f32_16x16x32_bf16 v[42:45], v[166:169], v[198:201], v[42:45]
	v_mfma_f32_16x16x32_bf16 v[38:41], v[158:161], v[206:209], v[38:41]
	v_mfma_f32_16x16x32_bf16 v[30:33], v[166:169], v[206:209], v[30:33]
	v_mfma_f32_16x16x32_bf16 v[22:25], v[158:161], v[214:217], v[22:25]
	v_mfma_f32_16x16x32_bf16 v[14:17], v[166:169], v[214:217], v[14:17]
	v_mfma_f32_16x16x32_bf16 v[54:57], v[170:173], v[186:189], v[54:57]
	v_mfma_f32_16x16x32_bf16 v[46:49], v[178:181], v[186:189], v[46:49]
	v_mfma_f32_16x16x32_bf16 v[34:37], v[170:173], v[194:197], v[34:37]
	v_mfma_f32_16x16x32_bf16 v[26:29], v[178:181], v[194:197], v[26:29]
	v_mfma_f32_16x16x32_bf16 v[18:21], v[170:173], v[202:205], v[18:21]
	v_mfma_f32_16x16x32_bf16 v[10:13], v[178:181], v[202:205], v[10:13]
	v_mfma_f32_16x16x32_bf16 v[6:9], v[170:173], v[210:213], v[6:9]
	v_mfma_f32_16x16x32_bf16 v[2:5], v[178:181], v[210:213], v[2:5]
	v_mfma_f32_16x16x32_bf16 v[54:57], v[174:177], v[190:193], v[54:57]
	v_mfma_f32_16x16x32_bf16 v[46:49], v[182:185], v[190:193], v[46:49]
	v_mfma_f32_16x16x32_bf16 v[34:37], v[174:177], v[198:201], v[34:37]
	v_mfma_f32_16x16x32_bf16 v[26:29], v[182:185], v[198:201], v[26:29]
	v_mfma_f32_16x16x32_bf16 v[18:21], v[174:177], v[206:209], v[18:21]
	v_mfma_f32_16x16x32_bf16 v[10:13], v[182:185], v[206:209], v[10:13]
	v_mfma_f32_16x16x32_bf16 v[6:9], v[174:177], v[214:217], v[6:9]
	v_mfma_f32_16x16x32_bf16 v[2:5], v[182:185], v[214:217], v[2:5]
	s_setprio 0
	s_barrier
	s_add_i32 s45, s45, 2
	s_add_u32 s18, s18, 0x100
	s_addc_u32 s19, s19, 0
	s_add_u32 s43, s43, 0x100
	s_addc_u32 s44, s44, 0
	s_cmp_gt_u32 s45, 29
	s_cbranch_scc0 .LBB0_982

.LBB0_989:
	s_waitcnt vmcnt(0)
	s_barrier
	s_mov_b64 s[0:1], exec
	v_readlane_b32 s2, v252, 11
	v_readlane_b32 s3, v252, 12
	s_and_b64 s[2:3], s[0:1], s[2:3]
	s_mov_b64 exec, s[2:3]
	s_cbranch_execz .LBB0_1041
	s_add_i32 s2, 0, 0x26f20
	v_mov_b32_e32 v0, s2
	s_waitcnt vmcnt(0) expcnt(0) lgkmcnt(0)
	ds_read_b32 v3, v0
	s_add_i32 s2, 0, 0x26f24
	v_mov_b32_e32 v0, s2
	ds_read_b32 v1, v0
	s_waitcnt lgkmcnt(1)
	v_cmp_ne_u32_e32 vcc, 0, v3
	s_cbranch_vccnz .LBB0_1005
	v_readlane_b32 s2, v252, 4
	v_readlane_b32 s3, v252, 5
	s_load_dwordx2 s[6:7], s[2:3], 0x4
	v_readlane_b32 s36, v252, 2
	v_readlane_b32 s37, v252, 3
	s_add_u32 s2, s36, 0x4200
	s_addc_u32 s3, s37, 0
	s_add_u32 s4, s36, 0x4400
	s_addc_u32 s5, s37, 0
	v_readlane_b32 s8, v252, 6
	s_waitcnt lgkmcnt(0)
	s_mul_i32 s33, s6, s8
	s_add_u32 s6, s36, 0x4500
	s_mul_i32 s33, s33, s7
	s_addc_u32 s7, s37, 0
	v_readlane_b32 s9, v252, 7
	s_add_u32 s8, s36, 0x4600
	s_addc_u32 s9, s37, 0
	s_add_u32 s10, s36, 0x4700
	s_addc_u32 s11, s37, 0
	s_add_u32 s12, s36, 0x4800
	s_addc_u32 s13, s37, 0
	s_add_u32 s14, s36, 0x4900
	s_addc_u32 s15, s37, 0
	s_add_u32 s16, s36, 0x4a00
	s_addc_u32 s17, s37, 0
	s_add_u32 s18, s36, 0x4b00
	s_addc_u32 s19, s37, 0
	s_add_u32 s20, s36, 0x4c00
	s_addc_u32 s21, s37, 0
	s_add_u32 s22, s36, 0x4d00
	s_addc_u32 s23, s37, 0
	s_add_u32 s24, s36, 0x4e00
	s_addc_u32 s25, s37, 0
	s_add_u32 s26, s36, 0x4f00
	s_addc_u32 s27, s37, 0
	s_add_u32 s28, s36, 0x5000
	s_addc_u32 s29, s37, 0
	s_add_u32 s30, s36, 0x5100
	s_addc_u32 s31, s37, 0
	s_add_u32 s34, s36, 0x5200
	s_addc_u32 s35, s37, 0
	s_add_u32 s36, s36, 0x5300
	s_addc_u32 s37, s37, 0
	s_mov_b32 s44, 1
	v_mov_b32_e32 v17, 0
	s_branch .LBB0_993
	s_nop 0
	s_nop 0
	s_nop 0
	s_nop 0
	s_nop 0
	s_nop 0
	s_nop 0
	s_nop 0

.LBB0_1213:
	s_add_u32 s35, s42, 0x100
	s_addc_u32 s37, s43, 0
	s_mov_b32 s39, -2
	s_mov_b64 s[42:43], 0
	ds_read_b128 v[70:73], v190
	ds_read_b128 v[74:77], v190 offset:1024
	ds_read_b128 v[78:81], v190 offset:2048
	ds_read_b128 v[82:85], v190 offset:3072
	ds_read_b128 v[94:97], v191
	ds_read_b128 v[98:101], v191 offset:1024
	ds_read_b128 v[102:105], v191 offset:2048
	ds_read_b128 v[106:109], v191 offset:3072
	s_add_u32 s44, s42, 0x100
	s_addc_u32 s45, s43, 0
	s_add_u32 s48, s35, s42
	s_addc_u32 s49, s37, s43
	s_cmp_eq_u32 s39, 12
	s_cselect_b64 vcc, -1, 0
	s_and_b64 s[46:47], vcc, exec
	s_cselect_b32 s73, 0, s44
	s_cselect_b32 s72, 0, s45
	s_cselect_b32 s46, s0, s48
	s_cselect_b32 s47, s1, s49
	s_add_u32 s48, s14, s73
	s_addc_u32 s49, s15, s72
	s_add_i32 m0, s11, 0xc000
	s_add_u32 s42, s24, s42
	s_addc_u32 s43, s25, s43
	ds_read_b128 v[176:179], v192
	ds_read_b128 v[180:183], v192 offset:1024
	ds_read_b128 v[194:197], v192 offset:2048
	ds_read_b128 v[198:201], v192 offset:3072
	ds_read_b128 v[202:205], v192 offset:4096
	ds_read_b128 v[206:209], v192 offset:5120
	ds_read_b128 v[210:213], v192 offset:6144
	ds_read_b128 v[214:217], v192 offset:7168
	global_load_lds_dwordx4 v187, s[42:43]
	s_add_i32 m0, s11, 0xe000
	v_mov_b32_e32 v0, v172
	global_load_lds_dwordx4 v186, s[42:43]
	v_mov_b32_e32 v169, v173
	v_lshlrev_b32_e32 v184, 11, v0
	v_lshlrev_b32_e32 v185, 11, v169
	v_bfe_u32 v0, v0, 16, 16
	v_bfe_u32 v169, v169, 16, 16
	v_and_b32_e32 v184, 0x7fff800, v184
	v_and_b32_e32 v185, 0x7fff800, v185
	v_lshl_add_u32 v0, v0, 11, v175
	v_lshl_add_u32 v169, v169, 11, v175
	v_add_u32_e32 v184, v184, v175
	v_add_u32_e32 v185, v185, v175
	v_cndmask_b32_e32 v168, v168, v0, vcc
	v_cndmask_b32_e32 v186, v186, v169, vcc
	v_cndmask_b32_e32 v170, v170, v184, vcc
	v_cndmask_b32_e32 v187, v187, v185, vcc
	s_waitcnt vmcnt(24)
	s_waitcnt lgkmcnt(0)
	s_barrier
	s_setprio 1
	s_waitcnt lgkmcnt(0)
	v_mfma_i32_16x16x64_i8 v[158:161], v[70:73], v[176:179], 0
	v_mfma_i32_16x16x64_i8 v[150:153], v[78:81], v[176:179], 0
	v_mfma_i32_16x16x64_i8 v[142:145], v[70:73], v[194:197], 0
	v_mfma_i32_16x16x64_i8 v[134:137], v[78:81], v[194:197], 0
	v_mfma_i32_16x16x64_i8 v[126:129], v[70:73], v[202:205], 0
	v_mfma_i32_16x16x64_i8 v[118:121], v[78:81], v[202:205], 0
	v_mfma_i32_16x16x64_i8 v[110:113], v[70:73], v[210:213], 0
	v_mfma_i32_16x16x64_i8 v[86:89], v[78:81], v[210:213], 0
	v_mfma_i32_16x16x64_i8 v[158:161], v[74:77], v[180:183], v[158:161]
	v_mfma_i32_16x16x64_i8 v[150:153], v[82:85], v[180:183], v[150:153]
	v_mfma_i32_16x16x64_i8 v[142:145], v[74:77], v[198:201], v[142:145]
	v_mfma_i32_16x16x64_i8 v[134:137], v[82:85], v[198:201], v[134:137]
	v_mfma_i32_16x16x64_i8 v[126:129], v[74:77], v[206:209], v[126:129]
	v_mfma_i32_16x16x64_i8 v[118:121], v[82:85], v[206:209], v[118:121]
	v_mfma_i32_16x16x64_i8 v[110:113], v[74:77], v[214:217], v[110:113]
	v_mfma_i32_16x16x64_i8 v[86:89], v[82:85], v[214:217], v[86:89]
	v_mfma_i32_16x16x64_i8 v[154:157], v[94:97], v[176:179], 0
	v_mfma_i32_16x16x64_i8 v[146:149], v[102:105], v[176:179], 0
	v_mfma_i32_16x16x64_i8 v[138:141], v[94:97], v[194:197], 0
	v_mfma_i32_16x16x64_i8 v[130:133], v[102:105], v[194:197], 0
	v_mfma_i32_16x16x64_i8 v[122:125], v[94:97], v[202:205], 0
	v_mfma_i32_16x16x64_i8 v[114:117], v[102:105], v[202:205], 0
	v_mfma_i32_16x16x64_i8 v[90:93], v[94:97], v[210:213], 0
	v_mfma_i32_16x16x64_i8 v[66:69], v[102:105], v[210:213], 0
	v_mfma_i32_16x16x64_i8 v[154:157], v[98:101], v[180:183], v[154:157]
	v_mfma_i32_16x16x64_i8 v[146:149], v[106:109], v[180:183], v[146:149]
	v_mfma_i32_16x16x64_i8 v[138:141], v[98:101], v[198:201], v[138:141]
	v_mfma_i32_16x16x64_i8 v[130:133], v[106:109], v[198:201], v[130:133]
	v_mfma_i32_16x16x64_i8 v[122:125], v[98:101], v[206:209], v[122:125]
	v_mfma_i32_16x16x64_i8 v[114:117], v[106:109], v[206:209], v[114:117]
	v_mfma_i32_16x16x64_i8 v[90:93], v[98:101], v[214:217], v[90:93]
	v_mfma_i32_16x16x64_i8 v[66:69], v[106:109], v[214:217], v[66:69]
	s_setprio 0
	s_barrier
	s_add_i32 s42, s67, s57
	v_lshl_add_u64 v[184:185], s[46:47], 0, v[164:165]
	s_mov_b32 m0, s42
	ds_read_b128 v[176:179], v192 offset:16384
	ds_read_b128 v[180:183], v192 offset:17408
	ds_read_b128 v[194:197], v192 offset:18432
	ds_read_b128 v[198:201], v192 offset:19456
	ds_read_b128 v[202:205], v192 offset:20480
	ds_read_b128 v[206:209], v192 offset:21504
	ds_read_b128 v[210:213], v192 offset:22528
	ds_read_b128 v[214:217], v192 offset:23552
	global_load_lds_dwordx4 v[184:185], off
	s_add_i32 m0, s42, 0x2000
	s_add_u32 s42, s46, 0x40000
	v_lshl_add_u64 v[218:219], s[46:47], 0, v[166:167]
	s_addc_u32 s43, s47, 0
	s_add_i32 s72, s68, s57
	global_load_lds_dwordx4 v[218:219], off
	v_lshl_add_u64 v[220:221], s[42:43], 0, v[164:165]
	s_mov_b32 m0, s72
	v_mov_b32_e32 v169, v171
	global_load_lds_dwordx4 v[220:221], off
	v_lshl_add_u64 v[220:221], s[42:43], 0, v[166:167]
	s_add_i32 m0, s72, 0x2000
	v_lshl_add_u64 v[222:223], s[48:49], 0, v[168:169]
	global_load_lds_dwordx4 v[220:221], off
	s_mov_b32 m0, s11
	v_lshl_add_u64 v[220:221], s[48:49], 0, v[170:171]
	global_load_lds_dwordx4 v170, s[48:49]
	s_mov_b32 m0, s58
	s_nop 0
	global_load_lds_dwordx4 v168, s[48:49]
	s_waitcnt vmcnt(8)
	s_waitcnt lgkmcnt(0)
	s_barrier
	s_setprio 1
	s_waitcnt lgkmcnt(0)
	v_mfma_i32_16x16x64_i8 v[62:65], v[70:73], v[176:179], 0
	v_mfma_i32_16x16x64_i8 v[54:57], v[78:81], v[176:179], 0
	v_mfma_i32_16x16x64_i8 v[46:49], v[70:73], v[194:197], 0
	v_mfma_i32_16x16x64_i8 v[38:41], v[78:81], v[194:197], 0
	v_mfma_i32_16x16x64_i8 v[30:33], v[70:73], v[202:205], 0
	v_mfma_i32_16x16x64_i8 v[22:25], v[78:81], v[202:205], 0
	v_mfma_i32_16x16x64_i8 v[14:17], v[70:73], v[210:213], 0
	v_mfma_i32_16x16x64_i8 v[6:9], v[78:81], v[210:213], 0
	v_mfma_i32_16x16x64_i8 v[62:65], v[74:77], v[180:183], v[62:65]
	v_mfma_i32_16x16x64_i8 v[54:57], v[82:85], v[180:183], v[54:57]
	v_mfma_i32_16x16x64_i8 v[46:49], v[74:77], v[198:201], v[46:49]
	v_mfma_i32_16x16x64_i8 v[38:41], v[82:85], v[198:201], v[38:41]
	v_mfma_i32_16x16x64_i8 v[30:33], v[74:77], v[206:209], v[30:33]
	v_mfma_i32_16x16x64_i8 v[22:25], v[82:85], v[206:209], v[22:25]
	v_mfma_i32_16x16x64_i8 v[14:17], v[74:77], v[214:217], v[14:17]
	v_mfma_i32_16x16x64_i8 v[6:9], v[82:85], v[214:217], v[6:9]
	v_mfma_i32_16x16x64_i8 v[58:61], v[94:97], v[176:179], 0
	v_mfma_i32_16x16x64_i8 v[50:53], v[102:105], v[176:179], 0
	v_mfma_i32_16x16x64_i8 v[42:45], v[94:97], v[194:197], 0
	v_mfma_i32_16x16x64_i8 v[34:37], v[102:105], v[194:197], 0
	v_mfma_i32_16x16x64_i8 v[26:29], v[94:97], v[202:205], 0
	v_mfma_i32_16x16x64_i8 v[18:21], v[102:105], v[202:205], 0
	v_mfma_i32_16x16x64_i8 v[10:13], v[94:97], v[210:213], 0
	v_mfma_i32_16x16x64_i8 v[2:5], v[102:105], v[210:213], 0
	v_mfma_i32_16x16x64_i8 v[58:61], v[98:101], v[180:183], v[58:61]
	v_mfma_i32_16x16x64_i8 v[50:53], v[106:109], v[180:183], v[50:53]
	v_mfma_i32_16x16x64_i8 v[42:45], v[98:101], v[198:201], v[42:45]
	v_mfma_i32_16x16x64_i8 v[34:37], v[106:109], v[198:201], v[34:37]
	v_mfma_i32_16x16x64_i8 v[26:29], v[98:101], v[206:209], v[26:29]
	v_mfma_i32_16x16x64_i8 v[18:21], v[106:109], v[206:209], v[18:21]
	v_mfma_i32_16x16x64_i8 v[10:13], v[98:101], v[214:217], v[10:13]
	v_mfma_i32_16x16x64_i8 v[2:5], v[106:109], v[214:217], v[2:5]
	s_setprio 0
	s_barrier
	s_add_i32 s42, 0, 0x18000
	v_add_u32_e32 v0, s42, v189
	s_add_i32 s72, 0, 0x1c000
	ds_read_b128 v[70:73], v0
	ds_read_b128 v[74:77], v0 offset:1024
	ds_read_b128 v[78:81], v0 offset:2048
	ds_read_b128 v[82:85], v0 offset:3072
	v_add_u32_e32 v0, s72, v189
	ds_read_b128 v[94:97], v0
	ds_read_b128 v[98:101], v0 offset:1024
	ds_read_b128 v[102:105], v0 offset:2048
	ds_read_b128 v[106:109], v0 offset:3072
	s_mov_b32 m0, s59
	ds_read_b128 v[176:179], v192 offset:32768
	ds_read_b128 v[180:183], v192 offset:33792
	ds_read_b128 v[194:197], v192 offset:34816
	ds_read_b128 v[198:201], v192 offset:35840
	ds_read_b128 v[202:205], v192 offset:36864
	ds_read_b128 v[206:209], v192 offset:37888
	ds_read_b128 v[210:213], v192 offset:38912
	ds_read_b128 v[214:217], v192 offset:39936
	global_load_lds_dwordx4 v187, s[48:49]
	s_mov_b32 m0, s60
	s_nop 0
	global_load_lds_dwordx4 v186, s[48:49]
	s_waitcnt vmcnt(8)
	s_waitcnt lgkmcnt(0)
	s_barrier
	s_setprio 1
	s_waitcnt lgkmcnt(0)
	v_mfma_i32_16x16x64_i8 v[158:161], v[70:73], v[176:179], v[158:161]
	v_mfma_i32_16x16x64_i8 v[150:153], v[78:81], v[176:179], v[150:153]
	v_mfma_i32_16x16x64_i8 v[142:145], v[70:73], v[194:197], v[142:145]
	v_mfma_i32_16x16x64_i8 v[134:137], v[78:81], v[194:197], v[134:137]
	v_mfma_i32_16x16x64_i8 v[126:129], v[70:73], v[202:205], v[126:129]
	v_mfma_i32_16x16x64_i8 v[118:121], v[78:81], v[202:205], v[118:121]
	v_mfma_i32_16x16x64_i8 v[110:113], v[70:73], v[210:213], v[110:113]
	v_mfma_i32_16x16x64_i8 v[86:89], v[78:81], v[210:213], v[86:89]
	v_mfma_i32_16x16x64_i8 v[158:161], v[74:77], v[180:183], v[158:161]
	v_mfma_i32_16x16x64_i8 v[150:153], v[82:85], v[180:183], v[150:153]
	v_mfma_i32_16x16x64_i8 v[142:145], v[74:77], v[198:201], v[142:145]
	v_mfma_i32_16x16x64_i8 v[134:137], v[82:85], v[198:201], v[134:137]
	v_mfma_i32_16x16x64_i8 v[126:129], v[74:77], v[206:209], v[126:129]
	v_mfma_i32_16x16x64_i8 v[118:121], v[82:85], v[206:209], v[118:121]
	v_mfma_i32_16x16x64_i8 v[110:113], v[74:77], v[214:217], v[110:113]
	v_mfma_i32_16x16x64_i8 v[86:89], v[82:85], v[214:217], v[86:89]
	v_mfma_i32_16x16x64_i8 v[154:157], v[94:97], v[176:179], v[154:157]
	v_mfma_i32_16x16x64_i8 v[146:149], v[102:105], v[176:179], v[146:149]
	v_mfma_i32_16x16x64_i8 v[138:141], v[94:97], v[194:197], v[138:141]
	v_mfma_i32_16x16x64_i8 v[130:133], v[102:105], v[194:197], v[130:133]
	v_mfma_i32_16x16x64_i8 v[122:125], v[94:97], v[202:205], v[122:125]
	v_mfma_i32_16x16x64_i8 v[114:117], v[102:105], v[202:205], v[114:117]
	v_mfma_i32_16x16x64_i8 v[90:93], v[94:97], v[210:213], v[90:93]
	v_mfma_i32_16x16x64_i8 v[66:69], v[102:105], v[210:213], v[66:69]
	v_mfma_i32_16x16x64_i8 v[154:157], v[98:101], v[180:183], v[154:157]
	v_mfma_i32_16x16x64_i8 v[146:149], v[106:109], v[180:183], v[146:149]
	v_mfma_i32_16x16x64_i8 v[138:141], v[98:101], v[198:201], v[138:141]
	v_mfma_i32_16x16x64_i8 v[130:133], v[106:109], v[198:201], v[130:133]
	v_mfma_i32_16x16x64_i8 v[122:125], v[98:101], v[206:209], v[122:125]
	v_mfma_i32_16x16x64_i8 v[114:117], v[106:109], v[206:209], v[114:117]
	v_mfma_i32_16x16x64_i8 v[90:93], v[98:101], v[214:217], v[90:93]
	v_mfma_i32_16x16x64_i8 v[66:69], v[106:109], v[214:217], v[66:69]
	s_setprio 0
	s_barrier
	s_add_i32 s42, s42, s57
	v_lshl_add_u64 v[184:185], v[184:185], 0, s[22:23]
	s_mov_b32 m0, s42
	ds_read_b128 v[176:179], v192 offset:49152
	ds_read_b128 v[180:183], v192 offset:50176
	ds_read_b128 v[194:197], v192 offset:51200
	ds_read_b128 v[198:201], v192 offset:52224
	ds_read_b128 v[202:205], v192 offset:53248
	ds_read_b128 v[206:209], v192 offset:54272
	ds_read_b128 v[210:213], v192 offset:55296
	ds_read_b128 v[214:217], v192 offset:56320
	global_load_lds_dwordx4 v[184:185], off
	s_add_i32 m0, s42, 0x2000
	s_add_u32 s42, s46, 0x40080
	v_lshl_add_u64 v[184:185], v[218:219], 0, s[22:23]
	s_addc_u32 s43, s47, 0
	s_add_i32 s46, s72, s57
	global_load_lds_dwordx4 v[184:185], off
	v_lshl_add_u64 v[184:185], s[42:43], 0, v[164:165]
	s_mov_b32 m0, s46
	s_nop 0
	global_load_lds_dwordx4 v[184:185], off
	v_lshl_add_u64 v[184:185], s[42:43], 0, v[166:167]
	s_add_i32 m0, s46, 0x2000
	s_nop 0
	global_load_lds_dwordx4 v[184:185], off
	v_lshl_add_u64 v[184:185], v[220:221], 0, s[22:23]
	s_mov_b32 m0, s63
	s_nop 0
	global_load_lds_dwordx4 v[184:185], off
	v_lshl_add_u64 v[184:185], v[222:223], 0, s[22:23]
	s_mov_b32 m0, s64
	s_nop 0
	global_load_lds_dwordx4 v[184:185], off
	s_waitcnt vmcnt(8)
	s_waitcnt lgkmcnt(0)
	s_barrier
	s_setprio 1
	s_waitcnt lgkmcnt(0)
	v_mfma_i32_16x16x64_i8 v[62:65], v[70:73], v[176:179], v[62:65]
	v_mfma_i32_16x16x64_i8 v[54:57], v[78:81], v[176:179], v[54:57]
	v_mfma_i32_16x16x64_i8 v[46:49], v[70:73], v[194:197], v[46:49]
	v_mfma_i32_16x16x64_i8 v[38:41], v[78:81], v[194:197], v[38:41]
	v_mfma_i32_16x16x64_i8 v[30:33], v[70:73], v[202:205], v[30:33]
	v_mfma_i32_16x16x64_i8 v[22:25], v[78:81], v[202:205], v[22:25]
	v_mfma_i32_16x16x64_i8 v[14:17], v[70:73], v[210:213], v[14:17]
	v_mfma_i32_16x16x64_i8 v[6:9], v[78:81], v[210:213], v[6:9]
	v_mfma_i32_16x16x64_i8 v[62:65], v[74:77], v[180:183], v[62:65]
	v_mfma_i32_16x16x64_i8 v[54:57], v[82:85], v[180:183], v[54:57]
	v_mfma_i32_16x16x64_i8 v[46:49], v[74:77], v[198:201], v[46:49]
	v_mfma_i32_16x16x64_i8 v[38:41], v[82:85], v[198:201], v[38:41]
	v_mfma_i32_16x16x64_i8 v[30:33], v[74:77], v[206:209], v[30:33]
	v_mfma_i32_16x16x64_i8 v[22:25], v[82:85], v[206:209], v[22:25]
	v_mfma_i32_16x16x64_i8 v[14:17], v[74:77], v[214:217], v[14:17]
	v_mfma_i32_16x16x64_i8 v[6:9], v[82:85], v[214:217], v[6:9]
	v_mfma_i32_16x16x64_i8 v[58:61], v[94:97], v[176:179], v[58:61]
	v_mfma_i32_16x16x64_i8 v[50:53], v[102:105], v[176:179], v[50:53]
	v_mfma_i32_16x16x64_i8 v[42:45], v[94:97], v[194:197], v[42:45]
	v_mfma_i32_16x16x64_i8 v[34:37], v[102:105], v[194:197], v[34:37]
	v_mfma_i32_16x16x64_i8 v[26:29], v[94:97], v[202:205], v[26:29]
	v_mfma_i32_16x16x64_i8 v[18:21], v[102:105], v[202:205], v[18:21]
	v_mfma_i32_16x16x64_i8 v[10:13], v[94:97], v[210:213], v[10:13]
	v_mfma_i32_16x16x64_i8 v[2:5], v[102:105], v[210:213], v[2:5]
	v_mfma_i32_16x16x64_i8 v[58:61], v[98:101], v[180:183], v[58:61]
	v_mfma_i32_16x16x64_i8 v[50:53], v[106:109], v[180:183], v[50:53]
	v_mfma_i32_16x16x64_i8 v[42:45], v[98:101], v[198:201], v[42:45]
	v_mfma_i32_16x16x64_i8 v[34:37], v[106:109], v[198:201], v[34:37]
	v_mfma_i32_16x16x64_i8 v[26:29], v[98:101], v[206:209], v[26:29]
	v_mfma_i32_16x16x64_i8 v[18:21], v[106:109], v[206:209], v[18:21]
	v_mfma_i32_16x16x64_i8 v[10:13], v[98:101], v[214:217], v[10:13]
	v_mfma_i32_16x16x64_i8 v[2:5], v[106:109], v[214:217], v[2:5]
	s_setprio 0
	s_barrier
	s_add_i32 s39, s39, 2
	s_cmp_gt_u32 s39, 13
	s_mov_b64 s[42:43], s[44:45]
	s_cbranch_scc0 .LBB0_1214
	s_branch .Lkexit_1214
	s_nop 0
	s_nop 0
	s_nop 0
	s_nop 0
	s_nop 0
	s_nop 0
	s_nop 0
	s_nop 0
	s_nop 0
	s_nop 0
	s_nop 0
	s_nop 0
	s_nop 0
	s_nop 0
	s_nop 0
	s_nop 0
	s_nop 0
	s_nop 0
	s_nop 0
	s_nop 0
	s_nop 0
	s_nop 0
	s_nop 0
	s_nop 0
	s_nop 0
.LBB0_1214:
	ds_read_b128 v[70:73], v190
	ds_read_b128 v[74:77], v190 offset:1024
	ds_read_b128 v[78:81], v190 offset:2048
	ds_read_b128 v[82:85], v190 offset:3072
	ds_read_b128 v[94:97], v191
	ds_read_b128 v[98:101], v191 offset:1024
	ds_read_b128 v[102:105], v191 offset:2048
	ds_read_b128 v[106:109], v191 offset:3072
	s_add_u32 s44, s42, 0x100
	s_addc_u32 s45, s43, 0
	s_add_u32 s48, s35, s42
	s_addc_u32 s49, s37, s43
	s_cmp_eq_u32 s39, 12
	s_cselect_b64 vcc, -1, 0
	s_and_b64 s[46:47], vcc, exec
	s_cselect_b32 s73, 0, s44
	s_cselect_b32 s72, 0, s45
	s_cselect_b32 s46, s0, s48
	s_cselect_b32 s47, s1, s49
	s_add_u32 s48, s14, s73
	s_addc_u32 s49, s15, s72
	s_add_i32 m0, s11, 0xc000
	s_add_u32 s42, s24, s42
	s_addc_u32 s43, s25, s43
	ds_read_b128 v[176:179], v192
	ds_read_b128 v[180:183], v192 offset:1024
	ds_read_b128 v[194:197], v192 offset:2048
	ds_read_b128 v[198:201], v192 offset:3072
	ds_read_b128 v[202:205], v192 offset:4096
	ds_read_b128 v[206:209], v192 offset:5120
	ds_read_b128 v[210:213], v192 offset:6144
	ds_read_b128 v[214:217], v192 offset:7168
	global_load_lds_dwordx4 v187, s[42:43]
	s_add_i32 m0, s11, 0xe000
	v_mov_b32_e32 v0, v172
	global_load_lds_dwordx4 v186, s[42:43]
	v_mov_b32_e32 v169, v173
	v_lshlrev_b32_e32 v184, 11, v0
	v_lshlrev_b32_e32 v185, 11, v169
	v_bfe_u32 v0, v0, 16, 16
	v_bfe_u32 v169, v169, 16, 16
	v_and_b32_e32 v184, 0x7fff800, v184
	v_and_b32_e32 v185, 0x7fff800, v185
	v_lshl_add_u32 v0, v0, 11, v175
	v_lshl_add_u32 v169, v169, 11, v175
	v_add_u32_e32 v184, v184, v175
	v_add_u32_e32 v185, v185, v175
	v_cndmask_b32_e32 v168, v168, v0, vcc
	v_cndmask_b32_e32 v186, v186, v169, vcc
	v_cndmask_b32_e32 v170, v170, v184, vcc
	v_cndmask_b32_e32 v187, v187, v185, vcc
	s_waitcnt vmcnt(8)
	s_waitcnt lgkmcnt(0)
	s_barrier
	s_setprio 1
	s_waitcnt lgkmcnt(0)
	v_mfma_i32_16x16x64_i8 v[158:161], v[70:73], v[176:179], v[158:161]
	v_mfma_i32_16x16x64_i8 v[150:153], v[78:81], v[176:179], v[150:153]
	v_mfma_i32_16x16x64_i8 v[142:145], v[70:73], v[194:197], v[142:145]
	v_mfma_i32_16x16x64_i8 v[134:137], v[78:81], v[194:197], v[134:137]
	v_mfma_i32_16x16x64_i8 v[126:129], v[70:73], v[202:205], v[126:129]
	v_mfma_i32_16x16x64_i8 v[118:121], v[78:81], v[202:205], v[118:121]
	v_mfma_i32_16x16x64_i8 v[110:113], v[70:73], v[210:213], v[110:113]
	v_mfma_i32_16x16x64_i8 v[86:89], v[78:81], v[210:213], v[86:89]
	v_mfma_i32_16x16x64_i8 v[158:161], v[74:77], v[180:183], v[158:161]
	v_mfma_i32_16x16x64_i8 v[150:153], v[82:85], v[180:183], v[150:153]
	v_mfma_i32_16x16x64_i8 v[142:145], v[74:77], v[198:201], v[142:145]
	v_mfma_i32_16x16x64_i8 v[134:137], v[82:85], v[198:201], v[134:137]
	v_mfma_i32_16x16x64_i8 v[126:129], v[74:77], v[206:209], v[126:129]
	v_mfma_i32_16x16x64_i8 v[118:121], v[82:85], v[206:209], v[118:121]
	v_mfma_i32_16x16x64_i8 v[110:113], v[74:77], v[214:217], v[110:113]
	v_mfma_i32_16x16x64_i8 v[86:89], v[82:85], v[214:217], v[86:89]
	v_mfma_i32_16x16x64_i8 v[154:157], v[94:97], v[176:179], v[154:157]
	v_mfma_i32_16x16x64_i8 v[146:149], v[102:105], v[176:179], v[146:149]
	v_mfma_i32_16x16x64_i8 v[138:141], v[94:97], v[194:197], v[138:141]
	v_mfma_i32_16x16x64_i8 v[130:133], v[102:105], v[194:197], v[130:133]
	v_mfma_i32_16x16x64_i8 v[122:125], v[94:97], v[202:205], v[122:125]
	v_mfma_i32_16x16x64_i8 v[114:117], v[102:105], v[202:205], v[114:117]
	v_mfma_i32_16x16x64_i8 v[90:93], v[94:97], v[210:213], v[90:93]
	v_mfma_i32_16x16x64_i8 v[66:69], v[102:105], v[210:213], v[66:69]
	v_mfma_i32_16x16x64_i8 v[154:157], v[98:101], v[180:183], v[154:157]
	v_mfma_i32_16x16x64_i8 v[146:149], v[106:109], v[180:183], v[146:149]
	v_mfma_i32_16x16x64_i8 v[138:141], v[98:101], v[198:201], v[138:141]
	v_mfma_i32_16x16x64_i8 v[130:133], v[106:109], v[198:201], v[130:133]
	v_mfma_i32_16x16x64_i8 v[122:125], v[98:101], v[206:209], v[122:125]
	v_mfma_i32_16x16x64_i8 v[114:117], v[106:109], v[206:209], v[114:117]
	v_mfma_i32_16x16x64_i8 v[90:93], v[98:101], v[214:217], v[90:93]
	v_mfma_i32_16x16x64_i8 v[66:69], v[106:109], v[214:217], v[66:69]
	s_setprio 0
	s_barrier
	s_add_i32 s42, s67, s57
	v_lshl_add_u64 v[184:185], s[46:47], 0, v[164:165]
	s_mov_b32 m0, s42
	ds_read_b128 v[176:179], v192 offset:16384
	ds_read_b128 v[180:183], v192 offset:17408
	ds_read_b128 v[194:197], v192 offset:18432
	ds_read_b128 v[198:201], v192 offset:19456
	ds_read_b128 v[202:205], v192 offset:20480
	ds_read_b128 v[206:209], v192 offset:21504
	ds_read_b128 v[210:213], v192 offset:22528
	ds_read_b128 v[214:217], v192 offset:23552
	global_load_lds_dwordx4 v[184:185], off
	s_add_i32 m0, s42, 0x2000
	s_add_u32 s42, s46, 0x40000
	v_lshl_add_u64 v[218:219], s[46:47], 0, v[166:167]
	s_addc_u32 s43, s47, 0
	s_add_i32 s72, s68, s57
	global_load_lds_dwordx4 v[218:219], off
	v_lshl_add_u64 v[220:221], s[42:43], 0, v[164:165]
	s_mov_b32 m0, s72
	v_mov_b32_e32 v169, v171
	global_load_lds_dwordx4 v[220:221], off
	v_lshl_add_u64 v[220:221], s[42:43], 0, v[166:167]
	s_add_i32 m0, s72, 0x2000
	v_lshl_add_u64 v[222:223], s[48:49], 0, v[168:169]
	global_load_lds_dwordx4 v[220:221], off
	s_mov_b32 m0, s11
	v_lshl_add_u64 v[220:221], s[48:49], 0, v[170:171]
	global_load_lds_dwordx4 v170, s[48:49]
	s_mov_b32 m0, s58
	s_nop 0
	global_load_lds_dwordx4 v168, s[48:49]
	s_waitcnt vmcnt(8)
	s_waitcnt lgkmcnt(0)
	s_barrier
	s_setprio 1
	s_waitcnt lgkmcnt(0)
	v_mfma_i32_16x16x64_i8 v[62:65], v[70:73], v[176:179], v[62:65]
	v_mfma_i32_16x16x64_i8 v[54:57], v[78:81], v[176:179], v[54:57]
	v_mfma_i32_16x16x64_i8 v[46:49], v[70:73], v[194:197], v[46:49]
	v_mfma_i32_16x16x64_i8 v[38:41], v[78:81], v[194:197], v[38:41]
	v_mfma_i32_16x16x64_i8 v[30:33], v[70:73], v[202:205], v[30:33]
	v_mfma_i32_16x16x64_i8 v[22:25], v[78:81], v[202:205], v[22:25]
	v_mfma_i32_16x16x64_i8 v[14:17], v[70:73], v[210:213], v[14:17]
	v_mfma_i32_16x16x64_i8 v[6:9], v[78:81], v[210:213], v[6:9]
	v_mfma_i32_16x16x64_i8 v[62:65], v[74:77], v[180:183], v[62:65]
	v_mfma_i32_16x16x64_i8 v[54:57], v[82:85], v[180:183], v[54:57]
	v_mfma_i32_16x16x64_i8 v[46:49], v[74:77], v[198:201], v[46:49]
	v_mfma_i32_16x16x64_i8 v[38:41], v[82:85], v[198:201], v[38:41]
	v_mfma_i32_16x16x64_i8 v[30:33], v[74:77], v[206:209], v[30:33]
	v_mfma_i32_16x16x64_i8 v[22:25], v[82:85], v[206:209], v[22:25]
	v_mfma_i32_16x16x64_i8 v[14:17], v[74:77], v[214:217], v[14:17]
	v_mfma_i32_16x16x64_i8 v[6:9], v[82:85], v[214:217], v[6:9]
	v_mfma_i32_16x16x64_i8 v[58:61], v[94:97], v[176:179], v[58:61]
	v_mfma_i32_16x16x64_i8 v[50:53], v[102:105], v[176:179], v[50:53]
	v_mfma_i32_16x16x64_i8 v[42:45], v[94:97], v[194:197], v[42:45]
	v_mfma_i32_16x16x64_i8 v[34:37], v[102:105], v[194:197], v[34:37]
	v_mfma_i32_16x16x64_i8 v[26:29], v[94:97], v[202:205], v[26:29]
	v_mfma_i32_16x16x64_i8 v[18:21], v[102:105], v[202:205], v[18:21]
	v_mfma_i32_16x16x64_i8 v[10:13], v[94:97], v[210:213], v[10:13]
	v_mfma_i32_16x16x64_i8 v[2:5], v[102:105], v[210:213], v[2:5]
	v_mfma_i32_16x16x64_i8 v[58:61], v[98:101], v[180:183], v[58:61]
	v_mfma_i32_16x16x64_i8 v[50:53], v[106:109], v[180:183], v[50:53]
	v_mfma_i32_16x16x64_i8 v[42:45], v[98:101], v[198:201], v[42:45]
	v_mfma_i32_16x16x64_i8 v[34:37], v[106:109], v[198:201], v[34:37]
	v_mfma_i32_16x16x64_i8 v[26:29], v[98:101], v[206:209], v[26:29]
	v_mfma_i32_16x16x64_i8 v[18:21], v[106:109], v[206:209], v[18:21]
	v_mfma_i32_16x16x64_i8 v[10:13], v[98:101], v[214:217], v[10:13]
	v_mfma_i32_16x16x64_i8 v[2:5], v[106:109], v[214:217], v[2:5]
	s_setprio 0
	s_barrier
	s_add_i32 s42, 0, 0x18000
	v_add_u32_e32 v0, s42, v189
	s_add_i32 s72, 0, 0x1c000
	ds_read_b128 v[70:73], v0
	ds_read_b128 v[74:77], v0 offset:1024
	ds_read_b128 v[78:81], v0 offset:2048
	ds_read_b128 v[82:85], v0 offset:3072
	v_add_u32_e32 v0, s72, v189
	ds_read_b128 v[94:97], v0
	ds_read_b128 v[98:101], v0 offset:1024
	ds_read_b128 v[102:105], v0 offset:2048
	ds_read_b128 v[106:109], v0 offset:3072
	s_mov_b32 m0, s59
	ds_read_b128 v[176:179], v192 offset:32768
	ds_read_b128 v[180:183], v192 offset:33792
	ds_read_b128 v[194:197], v192 offset:34816
	ds_read_b128 v[198:201], v192 offset:35840
	ds_read_b128 v[202:205], v192 offset:36864
	ds_read_b128 v[206:209], v192 offset:37888
	ds_read_b128 v[210:213], v192 offset:38912
	ds_read_b128 v[214:217], v192 offset:39936
	global_load_lds_dwordx4 v187, s[48:49]
	s_mov_b32 m0, s60
	s_nop 0
	global_load_lds_dwordx4 v186, s[48:49]
	s_waitcnt vmcnt(8)
	s_waitcnt lgkmcnt(0)
	s_barrier
	s_setprio 1
	s_waitcnt lgkmcnt(0)
	v_mfma_i32_16x16x64_i8 v[158:161], v[70:73], v[176:179], v[158:161]
	v_mfma_i32_16x16x64_i8 v[150:153], v[78:81], v[176:179], v[150:153]
	v_mfma_i32_16x16x64_i8 v[142:145], v[70:73], v[194:197], v[142:145]
	v_mfma_i32_16x16x64_i8 v[134:137], v[78:81], v[194:197], v[134:137]
	v_mfma_i32_16x16x64_i8 v[126:129], v[70:73], v[202:205], v[126:129]
	v_mfma_i32_16x16x64_i8 v[118:121], v[78:81], v[202:205], v[118:121]
	v_mfma_i32_16x16x64_i8 v[110:113], v[70:73], v[210:213], v[110:113]
	v_mfma_i32_16x16x64_i8 v[86:89], v[78:81], v[210:213], v[86:89]
	v_mfma_i32_16x16x64_i8 v[158:161], v[74:77], v[180:183], v[158:161]
	v_mfma_i32_16x16x64_i8 v[150:153], v[82:85], v[180:183], v[150:153]
	v_mfma_i32_16x16x64_i8 v[142:145], v[74:77], v[198:201], v[142:145]
	v_mfma_i32_16x16x64_i8 v[134:137], v[82:85], v[198:201], v[134:137]
	v_mfma_i32_16x16x64_i8 v[126:129], v[74:77], v[206:209], v[126:129]
	v_mfma_i32_16x16x64_i8 v[118:121], v[82:85], v[206:209], v[118:121]
	v_mfma_i32_16x16x64_i8 v[110:113], v[74:77], v[214:217], v[110:113]
	v_mfma_i32_16x16x64_i8 v[86:89], v[82:85], v[214:217], v[86:89]
	v_mfma_i32_16x16x64_i8 v[154:157], v[94:97], v[176:179], v[154:157]
	v_mfma_i32_16x16x64_i8 v[146:149], v[102:105], v[176:179], v[146:149]
	v_mfma_i32_16x16x64_i8 v[138:141], v[94:97], v[194:197], v[138:141]
	v_mfma_i32_16x16x64_i8 v[130:133], v[102:105], v[194:197], v[130:133]
	v_mfma_i32_16x16x64_i8 v[122:125], v[94:97], v[202:205], v[122:125]
	v_mfma_i32_16x16x64_i8 v[114:117], v[102:105], v[202:205], v[114:117]
	v_mfma_i32_16x16x64_i8 v[90:93], v[94:97], v[210:213], v[90:93]
	v_mfma_i32_16x16x64_i8 v[66:69], v[102:105], v[210:213], v[66:69]
	v_mfma_i32_16x16x64_i8 v[154:157], v[98:101], v[180:183], v[154:157]
	v_mfma_i32_16x16x64_i8 v[146:149], v[106:109], v[180:183], v[146:149]
	v_mfma_i32_16x16x64_i8 v[138:141], v[98:101], v[198:201], v[138:141]
	v_mfma_i32_16x16x64_i8 v[130:133], v[106:109], v[198:201], v[130:133]
	v_mfma_i32_16x16x64_i8 v[122:125], v[98:101], v[206:209], v[122:125]
	v_mfma_i32_16x16x64_i8 v[114:117], v[106:109], v[206:209], v[114:117]
	v_mfma_i32_16x16x64_i8 v[90:93], v[98:101], v[214:217], v[90:93]
	v_mfma_i32_16x16x64_i8 v[66:69], v[106:109], v[214:217], v[66:69]
	s_setprio 0
	s_barrier
	s_add_i32 s42, s42, s57
	v_lshl_add_u64 v[184:185], v[184:185], 0, s[22:23]
	s_mov_b32 m0, s42
	ds_read_b128 v[176:179], v192 offset:49152
	ds_read_b128 v[180:183], v192 offset:50176
	ds_read_b128 v[194:197], v192 offset:51200
	ds_read_b128 v[198:201], v192 offset:52224
	ds_read_b128 v[202:205], v192 offset:53248
	ds_read_b128 v[206:209], v192 offset:54272
	ds_read_b128 v[210:213], v192 offset:55296
	ds_read_b128 v[214:217], v192 offset:56320
	global_load_lds_dwordx4 v[184:185], off
	s_add_i32 m0, s42, 0x2000
	s_add_u32 s42, s46, 0x40080
	v_lshl_add_u64 v[184:185], v[218:219], 0, s[22:23]
	s_addc_u32 s43, s47, 0
	s_add_i32 s46, s72, s57
	global_load_lds_dwordx4 v[184:185], off
	v_lshl_add_u64 v[184:185], s[42:43], 0, v[164:165]
	s_mov_b32 m0, s46
	s_nop 0
	global_load_lds_dwordx4 v[184:185], off
	v_lshl_add_u64 v[184:185], s[42:43], 0, v[166:167]
	s_add_i32 m0, s46, 0x2000
	s_nop 0
	global_load_lds_dwordx4 v[184:185], off
	v_lshl_add_u64 v[184:185], v[220:221], 0, s[22:23]
	s_mov_b32 m0, s63
	s_nop 0
	global_load_lds_dwordx4 v[184:185], off
	v_lshl_add_u64 v[184:185], v[222:223], 0, s[22:23]
	s_mov_b32 m0, s64
	s_nop 0
	global_load_lds_dwordx4 v[184:185], off
	s_waitcnt vmcnt(8)
	s_waitcnt lgkmcnt(0)
	s_barrier
	s_setprio 1
	s_waitcnt lgkmcnt(0)
	v_mfma_i32_16x16x64_i8 v[62:65], v[70:73], v[176:179], v[62:65]
	v_mfma_i32_16x16x64_i8 v[54:57], v[78:81], v[176:179], v[54:57]
	v_mfma_i32_16x16x64_i8 v[46:49], v[70:73], v[194:197], v[46:49]
	v_mfma_i32_16x16x64_i8 v[38:41], v[78:81], v[194:197], v[38:41]
	v_mfma_i32_16x16x64_i8 v[30:33], v[70:73], v[202:205], v[30:33]
	v_mfma_i32_16x16x64_i8 v[22:25], v[78:81], v[202:205], v[22:25]
	v_mfma_i32_16x16x64_i8 v[14:17], v[70:73], v[210:213], v[14:17]
	v_mfma_i32_16x16x64_i8 v[6:9], v[78:81], v[210:213], v[6:9]
	v_mfma_i32_16x16x64_i8 v[62:65], v[74:77], v[180:183], v[62:65]
	v_mfma_i32_16x16x64_i8 v[54:57], v[82:85], v[180:183], v[54:57]
	v_mfma_i32_16x16x64_i8 v[46:49], v[74:77], v[198:201], v[46:49]
	v_mfma_i32_16x16x64_i8 v[38:41], v[82:85], v[198:201], v[38:41]
	v_mfma_i32_16x16x64_i8 v[30:33], v[74:77], v[206:209], v[30:33]
	v_mfma_i32_16x16x64_i8 v[22:25], v[82:85], v[206:209], v[22:25]
	v_mfma_i32_16x16x64_i8 v[14:17], v[74:77], v[214:217], v[14:17]
	v_mfma_i32_16x16x64_i8 v[6:9], v[82:85], v[214:217], v[6:9]
	v_mfma_i32_16x16x64_i8 v[58:61], v[94:97], v[176:179], v[58:61]
	v_mfma_i32_16x16x64_i8 v[50:53], v[102:105], v[176:179], v[50:53]
	v_mfma_i32_16x16x64_i8 v[42:45], v[94:97], v[194:197], v[42:45]
	v_mfma_i32_16x16x64_i8 v[34:37], v[102:105], v[194:197], v[34:37]
	v_mfma_i32_16x16x64_i8 v[26:29], v[94:97], v[202:205], v[26:29]
	v_mfma_i32_16x16x64_i8 v[18:21], v[102:105], v[202:205], v[18:21]
	v_mfma_i32_16x16x64_i8 v[10:13], v[94:97], v[210:213], v[10:13]
	v_mfma_i32_16x16x64_i8 v[2:5], v[102:105], v[210:213], v[2:5]
	v_mfma_i32_16x16x64_i8 v[58:61], v[98:101], v[180:183], v[58:61]
	v_mfma_i32_16x16x64_i8 v[50:53], v[106:109], v[180:183], v[50:53]
	v_mfma_i32_16x16x64_i8 v[42:45], v[98:101], v[198:201], v[42:45]
	v_mfma_i32_16x16x64_i8 v[34:37], v[106:109], v[198:201], v[34:37]
	v_mfma_i32_16x16x64_i8 v[26:29], v[98:101], v[206:209], v[26:29]
	v_mfma_i32_16x16x64_i8 v[18:21], v[106:109], v[206:209], v[18:21]
	v_mfma_i32_16x16x64_i8 v[10:13], v[98:101], v[214:217], v[10:13]
	v_mfma_i32_16x16x64_i8 v[2:5], v[106:109], v[214:217], v[2:5]
	s_setprio 0
	s_barrier
	s_add_i32 s39, s39, 2
	s_cmp_gt_u32 s39, 13
	s_mov_b64 s[42:43], s[44:45]
	s_cbranch_scc0 .LBB0_1214

.LBB0_1239:
	s_waitcnt vmcnt(0)
	s_barrier
	s_mov_b64 s[0:1], exec
	v_readlane_b32 s4, v252, 11
	v_readlane_b32 s5, v252, 12
	s_and_b64 s[4:5], s[0:1], s[4:5]
	s_mov_b64 exec, s[4:5]
	s_cbranch_execz .LBB0_1291
	s_add_i32 s4, 0, 0x26f20
	v_mov_b32_e32 v0, s4
	s_waitcnt vmcnt(0) expcnt(0) lgkmcnt(0)
	ds_read_b32 v3, v0
	s_add_i32 s4, 0, 0x26f24
	v_mov_b32_e32 v0, s4
	ds_read_b32 v1, v0
	s_waitcnt lgkmcnt(1)
	v_cmp_ne_u32_e32 vcc, 0, v3
	s_cbranch_vccnz .LBB0_1255
	v_readlane_b32 s4, v252, 4
	v_readlane_b32 s5, v252, 5
	s_load_dwordx2 s[10:11], s[4:5], 0x4
	v_readlane_b32 s42, v252, 2
	v_readlane_b32 s43, v252, 3
	s_add_u32 s4, s42, 0x4200
	s_addc_u32 s5, s43, 0
	s_add_u32 s6, s42, 0x4400
	s_addc_u32 s7, s43, 0
	v_readlane_b32 s14, v252, 6
	s_waitcnt lgkmcnt(0)
	s_mul_i32 s51, s10, s14
	s_add_u32 s10, s42, 0x4500
	s_mul_i32 s51, s51, s11
	s_addc_u32 s11, s43, 0
	v_readlane_b32 s15, v252, 7
	s_add_u32 s14, s42, 0x4600
	s_addc_u32 s15, s43, 0
	s_add_u32 s16, s42, 0x4700
	s_addc_u32 s17, s43, 0
	s_add_u32 s18, s42, 0x4800
	s_addc_u32 s19, s43, 0
	s_add_u32 s20, s42, 0x4900
	s_addc_u32 s21, s43, 0
	s_add_u32 s22, s42, 0x4a00
	s_addc_u32 s23, s43, 0
	s_add_u32 s24, s42, 0x4b00
	s_addc_u32 s25, s43, 0
	s_add_u32 s26, s42, 0x4c00
	s_addc_u32 s27, s43, 0
	s_add_u32 s28, s42, 0x4d00
	s_addc_u32 s29, s43, 0
	s_add_u32 s30, s42, 0x4e00
	s_addc_u32 s31, s43, 0
	s_add_u32 s34, s42, 0x4f00
	s_addc_u32 s35, s43, 0
	s_add_u32 s36, s42, 0x5000
	s_addc_u32 s37, s43, 0
	s_add_u32 s38, s42, 0x5100
	s_addc_u32 s39, s43, 0
	s_add_u32 s40, s42, 0x5200
	s_addc_u32 s41, s43, 0
	s_add_u32 s42, s42, 0x5300
	s_addc_u32 s43, s43, 0
	s_mov_b32 s52, 1
	v_mov_b32_e32 v17, 0
	s_branch .LBB0_1243
	s_nop 0
	s_nop 0
	s_nop 0
	s_nop 0
	s_nop 0
	s_nop 0
	s_nop 0
	s_nop 0
	s_nop 0
	s_nop 0
	s_nop 0
	s_nop 0
	s_nop 0
	s_nop 0
	s_nop 0
	s_nop 0
	s_nop 0
	s_nop 0
	s_nop 0
	s_nop 0
	s_nop 0
	s_nop 0
	s_nop 0
	s_nop 0
	s_nop 0
	s_nop 0
	s_nop 0
	s_nop 0
	s_nop 0
	s_nop 0
	s_nop 0
	s_nop 0
	s_nop 0
	s_nop 0
	s_nop 0
	s_nop 0
	s_nop 0
	s_nop 0
	s_nop 0
	s_nop 0

.LBB0_1366:
	s_lshl_b64 s[36:37], s[28:29], 19
	s_add_u32 s36, s2, s36
	s_addc_u32 s37, s3, s37
	s_and_b64 s[0:1], exec, s[0:1]
	s_cselect_b32 s27, s37, s43
	s_cselect_b32 s29, s36, s42
	s_add_u32 s0, s42, 0x40080
	s_addc_u32 s1, s43, 0
	s_add_u32 s31, s40, 0x100
	s_addc_u32 s39, s41, 0
	s_mov_b32 s61, -2
	ds_read_b128 v[66:69], v229
	ds_read_b128 v[70:73], v229 offset:1024
	ds_read_b128 v[82:85], v229 offset:2048
	ds_read_b128 v[86:89], v229 offset:3072
	ds_read_b128 v[90:93], v230
	ds_read_b128 v[94:97], v230 offset:1024
	ds_read_b128 v[98:101], v230 offset:2048
	ds_read_b128 v[102:105], v230 offset:3072
	s_add_u32 s40, s0, 0xfffc0080
	s_addc_u32 s41, s1, -1
	s_cmp_eq_u32 s61, 12
	s_cselect_b32 s43, s27, s41
	s_cselect_b32 s42, s29, s40
	s_cselect_b32 s41, s35, s39
	s_cselect_b32 s40, s34, s31
	v_lshl_add_u64 v[208:209], s[0:1], 0, v[170:171]
	s_add_i32 m0, s15, 0xc000
	ds_read_b128 v[176:179], v231
	ds_read_b128 v[180:183], v231 offset:1024
	ds_read_b128 v[184:187], v231 offset:2048
	ds_read_b128 v[188:191], v231 offset:3072
	ds_read_b128 v[192:195], v231 offset:4096
	ds_read_b128 v[196:199], v231 offset:5120
	ds_read_b128 v[200:203], v231 offset:6144
	ds_read_b128 v[204:207], v231 offset:7168
	global_load_lds_dwordx4 v[208:209], off
	v_lshl_add_u64 v[208:209], s[0:1], 0, v[172:173]
	s_add_i32 m0, s15, 0xe000
	s_nop 0
	global_load_lds_dwordx4 v[208:209], off
	s_waitcnt vmcnt(32)
	s_waitcnt lgkmcnt(0)
	s_barrier
	s_setprio 1
	s_waitcnt lgkmcnt(0)
	v_mfma_i32_16x16x64_i8 v[158:161], v[66:69], v[176:179], 0
	v_mfma_i32_16x16x64_i8 v[154:157], v[82:85], v[176:179], 0
	v_mfma_i32_16x16x64_i8 v[142:145], v[66:69], v[184:187], 0
	v_mfma_i32_16x16x64_i8 v[138:141], v[82:85], v[184:187], 0
	v_mfma_i32_16x16x64_i8 v[126:129], v[66:69], v[192:195], 0
	v_mfma_i32_16x16x64_i8 v[122:125], v[82:85], v[192:195], 0
	v_mfma_i32_16x16x64_i8 v[110:113], v[66:69], v[200:203], 0
	v_mfma_i32_16x16x64_i8 v[106:109], v[82:85], v[200:203], 0
	v_mfma_i32_16x16x64_i8 v[158:161], v[70:73], v[180:183], v[158:161]
	v_mfma_i32_16x16x64_i8 v[154:157], v[86:89], v[180:183], v[154:157]
	v_mfma_i32_16x16x64_i8 v[142:145], v[70:73], v[188:191], v[142:145]
	v_mfma_i32_16x16x64_i8 v[138:141], v[86:89], v[188:191], v[138:141]
	v_mfma_i32_16x16x64_i8 v[126:129], v[70:73], v[196:199], v[126:129]
	v_mfma_i32_16x16x64_i8 v[122:125], v[86:89], v[196:199], v[122:125]
	v_mfma_i32_16x16x64_i8 v[110:113], v[70:73], v[204:207], v[110:113]
	v_mfma_i32_16x16x64_i8 v[106:109], v[86:89], v[204:207], v[106:109]
	v_mfma_i32_16x16x64_i8 v[150:153], v[90:93], v[176:179], 0
	v_mfma_i32_16x16x64_i8 v[146:149], v[98:101], v[176:179], 0
	v_mfma_i32_16x16x64_i8 v[134:137], v[90:93], v[184:187], 0
	v_mfma_i32_16x16x64_i8 v[130:133], v[98:101], v[184:187], 0
	v_mfma_i32_16x16x64_i8 v[118:121], v[90:93], v[192:195], 0
	v_mfma_i32_16x16x64_i8 v[114:117], v[98:101], v[192:195], 0
	v_mfma_i32_16x16x64_i8 v[78:81], v[90:93], v[200:203], 0
	v_mfma_i32_16x16x64_i8 v[74:77], v[98:101], v[200:203], 0
	v_mfma_i32_16x16x64_i8 v[150:153], v[94:97], v[180:183], v[150:153]
	v_mfma_i32_16x16x64_i8 v[146:149], v[102:105], v[180:183], v[146:149]
	v_mfma_i32_16x16x64_i8 v[134:137], v[94:97], v[188:191], v[134:137]
	v_mfma_i32_16x16x64_i8 v[130:133], v[102:105], v[188:191], v[130:133]
	v_mfma_i32_16x16x64_i8 v[118:121], v[94:97], v[196:199], v[118:121]
	v_mfma_i32_16x16x64_i8 v[114:117], v[102:105], v[196:199], v[114:117]
	v_mfma_i32_16x16x64_i8 v[78:81], v[94:97], v[204:207], v[78:81]
	v_mfma_i32_16x16x64_i8 v[74:77], v[102:105], v[204:207], v[74:77]
	s_setprio 0
	s_barrier
	s_add_i32 s62, s57, s47
	v_lshl_add_u64 v[208:209], s[40:41], 0, v[164:165]
	s_mov_b32 m0, s62
	ds_read_b128 v[176:179], v231 offset:16384
	ds_read_b128 v[180:183], v231 offset:17408
	ds_read_b128 v[184:187], v231 offset:18432
	ds_read_b128 v[188:191], v231 offset:19456
	ds_read_b128 v[192:195], v231 offset:20480
	ds_read_b128 v[196:199], v231 offset:21504
	ds_read_b128 v[200:203], v231 offset:22528
	ds_read_b128 v[204:207], v231 offset:23552
	global_load_lds_dwordx4 v[208:209], off
	s_add_i32 m0, s62, 0x2000
	s_add_u32 s62, s40, 0x40000
	v_lshl_add_u64 v[210:211], s[40:41], 0, v[168:169]
	s_addc_u32 s63, s41, 0
	s_add_i32 s64, s58, s47
	global_load_lds_dwordx4 v[210:211], off
	v_lshl_add_u64 v[212:213], s[62:63], 0, v[164:165]
	s_mov_b32 m0, s64
	v_lshl_add_u64 v[214:215], s[42:43], 0, v[166:167]
	global_load_lds_dwordx4 v[212:213], off
	v_lshl_add_u64 v[212:213], s[62:63], 0, v[168:169]
	s_add_i32 m0, s64, 0x2000
	s_nop 0
	global_load_lds_dwordx4 v[212:213], off
	v_lshl_add_u64 v[212:213], s[42:43], 0, v[162:163]
	s_mov_b32 m0, s15
	s_nop 0
	global_load_lds_dwordx4 v[212:213], off
	s_mov_b32 m0, s48
	s_nop 0
	global_load_lds_dwordx4 v[214:215], off
	s_waitcnt vmcnt(8)
	s_waitcnt lgkmcnt(0)
	s_barrier
	s_setprio 1
	s_waitcnt lgkmcnt(0)
	v_mfma_i32_16x16x64_i8 v[62:65], v[66:69], v[176:179], 0
	v_mfma_i32_16x16x64_i8 v[58:61], v[82:85], v[176:179], 0
	v_mfma_i32_16x16x64_i8 v[46:49], v[66:69], v[184:187], 0
	v_mfma_i32_16x16x64_i8 v[42:45], v[82:85], v[184:187], 0
	v_mfma_i32_16x16x64_i8 v[30:33], v[66:69], v[192:195], 0
	v_mfma_i32_16x16x64_i8 v[26:29], v[82:85], v[192:195], 0
	v_mfma_i32_16x16x64_i8 v[14:17], v[66:69], v[200:203], 0
	v_mfma_i32_16x16x64_i8 v[10:13], v[82:85], v[200:203], 0
	v_mfma_i32_16x16x64_i8 v[62:65], v[70:73], v[180:183], v[62:65]
	v_mfma_i32_16x16x64_i8 v[58:61], v[86:89], v[180:183], v[58:61]
	v_mfma_i32_16x16x64_i8 v[46:49], v[70:73], v[188:191], v[46:49]
	v_mfma_i32_16x16x64_i8 v[42:45], v[86:89], v[188:191], v[42:45]
	v_mfma_i32_16x16x64_i8 v[30:33], v[70:73], v[196:199], v[30:33]
	v_mfma_i32_16x16x64_i8 v[26:29], v[86:89], v[196:199], v[26:29]
	v_mfma_i32_16x16x64_i8 v[14:17], v[70:73], v[204:207], v[14:17]
	v_mfma_i32_16x16x64_i8 v[10:13], v[86:89], v[204:207], v[10:13]
	v_mfma_i32_16x16x64_i8 v[54:57], v[90:93], v[176:179], 0
	v_mfma_i32_16x16x64_i8 v[50:53], v[98:101], v[176:179], 0
	v_mfma_i32_16x16x64_i8 v[38:41], v[90:93], v[184:187], 0
	v_mfma_i32_16x16x64_i8 v[34:37], v[98:101], v[184:187], 0
	v_mfma_i32_16x16x64_i8 v[22:25], v[90:93], v[192:195], 0
	v_mfma_i32_16x16x64_i8 v[18:21], v[98:101], v[192:195], 0
	v_mfma_i32_16x16x64_i8 v[6:9], v[90:93], v[200:203], 0
	v_mfma_i32_16x16x64_i8 v[2:5], v[98:101], v[200:203], 0
	v_mfma_i32_16x16x64_i8 v[54:57], v[94:97], v[180:183], v[54:57]
	v_mfma_i32_16x16x64_i8 v[50:53], v[102:105], v[180:183], v[50:53]
	v_mfma_i32_16x16x64_i8 v[38:41], v[94:97], v[188:191], v[38:41]
	v_mfma_i32_16x16x64_i8 v[34:37], v[102:105], v[188:191], v[34:37]
	v_mfma_i32_16x16x64_i8 v[22:25], v[94:97], v[196:199], v[22:25]
	v_mfma_i32_16x16x64_i8 v[18:21], v[102:105], v[196:199], v[18:21]
	v_mfma_i32_16x16x64_i8 v[6:9], v[94:97], v[204:207], v[6:9]
	v_mfma_i32_16x16x64_i8 v[2:5], v[102:105], v[204:207], v[2:5]
	s_setprio 0
	s_barrier
	s_add_i32 s62, 0, 0x18000
	v_add_u32_e32 v0, s62, v227
	s_add_i32 s63, 0, 0x1c000
	ds_read_b128 v[66:69], v0
	ds_read_b128 v[70:73], v0 offset:1024
	ds_read_b128 v[82:85], v0 offset:2048
	ds_read_b128 v[86:89], v0 offset:3072
	v_add_u32_e32 v0, s63, v227
	ds_read_b128 v[90:93], v0
	ds_read_b128 v[94:97], v0 offset:1024
	ds_read_b128 v[98:101], v0 offset:2048
	ds_read_b128 v[102:105], v0 offset:3072
	s_add_u32 s42, s42, 0x40000
	s_addc_u32 s43, s43, 0
	s_mov_b32 m0, s49
	v_lshl_add_u64 v[216:217], s[42:43], 0, v[162:163]
	ds_read_b128 v[176:179], v231 offset:32768
	ds_read_b128 v[180:183], v231 offset:33792
	ds_read_b128 v[184:187], v231 offset:34816
	ds_read_b128 v[188:191], v231 offset:35840
	ds_read_b128 v[192:195], v231 offset:36864
	ds_read_b128 v[196:199], v231 offset:37888
	ds_read_b128 v[200:203], v231 offset:38912
	ds_read_b128 v[204:207], v231 offset:39936
	global_load_lds_dwordx4 v[216:217], off
	v_lshl_add_u64 v[216:217], s[42:43], 0, v[166:167]
	s_mov_b32 m0, s51
	s_nop 0
	global_load_lds_dwordx4 v[216:217], off
	s_waitcnt vmcnt(8)
	s_waitcnt lgkmcnt(0)
	s_barrier
	s_setprio 1
	s_waitcnt lgkmcnt(0)
	v_mfma_i32_16x16x64_i8 v[158:161], v[66:69], v[176:179], v[158:161]
	v_mfma_i32_16x16x64_i8 v[154:157], v[82:85], v[176:179], v[154:157]
	v_mfma_i32_16x16x64_i8 v[142:145], v[66:69], v[184:187], v[142:145]
	v_mfma_i32_16x16x64_i8 v[138:141], v[82:85], v[184:187], v[138:141]
	v_mfma_i32_16x16x64_i8 v[126:129], v[66:69], v[192:195], v[126:129]
	v_mfma_i32_16x16x64_i8 v[122:125], v[82:85], v[192:195], v[122:125]
	v_mfma_i32_16x16x64_i8 v[110:113], v[66:69], v[200:203], v[110:113]
	v_mfma_i32_16x16x64_i8 v[106:109], v[82:85], v[200:203], v[106:109]
	v_mfma_i32_16x16x64_i8 v[158:161], v[70:73], v[180:183], v[158:161]
	v_mfma_i32_16x16x64_i8 v[154:157], v[86:89], v[180:183], v[154:157]
	v_mfma_i32_16x16x64_i8 v[142:145], v[70:73], v[188:191], v[142:145]
	v_mfma_i32_16x16x64_i8 v[138:141], v[86:89], v[188:191], v[138:141]
	v_mfma_i32_16x16x64_i8 v[126:129], v[70:73], v[196:199], v[126:129]
	v_mfma_i32_16x16x64_i8 v[122:125], v[86:89], v[196:199], v[122:125]
	v_mfma_i32_16x16x64_i8 v[110:113], v[70:73], v[204:207], v[110:113]
	v_mfma_i32_16x16x64_i8 v[106:109], v[86:89], v[204:207], v[106:109]
	v_mfma_i32_16x16x64_i8 v[150:153], v[90:93], v[176:179], v[150:153]
	v_mfma_i32_16x16x64_i8 v[146:149], v[98:101], v[176:179], v[146:149]
	v_mfma_i32_16x16x64_i8 v[134:137], v[90:93], v[184:187], v[134:137]
	v_mfma_i32_16x16x64_i8 v[130:133], v[98:101], v[184:187], v[130:133]
	v_mfma_i32_16x16x64_i8 v[118:121], v[90:93], v[192:195], v[118:121]
	v_mfma_i32_16x16x64_i8 v[114:117], v[98:101], v[192:195], v[114:117]
	v_mfma_i32_16x16x64_i8 v[78:81], v[90:93], v[200:203], v[78:81]
	v_mfma_i32_16x16x64_i8 v[74:77], v[98:101], v[200:203], v[74:77]
	v_mfma_i32_16x16x64_i8 v[150:153], v[94:97], v[180:183], v[150:153]
	v_mfma_i32_16x16x64_i8 v[146:149], v[102:105], v[180:183], v[146:149]
	v_mfma_i32_16x16x64_i8 v[134:137], v[94:97], v[188:191], v[134:137]
	v_mfma_i32_16x16x64_i8 v[130:133], v[102:105], v[188:191], v[130:133]
	v_mfma_i32_16x16x64_i8 v[118:121], v[94:97], v[196:199], v[118:121]
	v_mfma_i32_16x16x64_i8 v[114:117], v[102:105], v[196:199], v[114:117]
	v_mfma_i32_16x16x64_i8 v[78:81], v[94:97], v[204:207], v[78:81]
	v_mfma_i32_16x16x64_i8 v[74:77], v[102:105], v[204:207], v[74:77]
	s_setprio 0
	s_barrier
	s_add_i32 s42, s62, s47
	v_lshl_add_u64 v[208:209], v[208:209], 0, s[22:23]
	s_mov_b32 m0, s42
	ds_read_b128 v[176:179], v231 offset:49152
	ds_read_b128 v[180:183], v231 offset:50176
	ds_read_b128 v[184:187], v231 offset:51200
	ds_read_b128 v[188:191], v231 offset:52224
	ds_read_b128 v[192:195], v231 offset:53248
	ds_read_b128 v[196:199], v231 offset:54272
	ds_read_b128 v[200:203], v231 offset:55296
	ds_read_b128 v[204:207], v231 offset:56320
	global_load_lds_dwordx4 v[208:209], off
	s_add_i32 m0, s42, 0x2000
	s_add_u32 s40, s40, 0x40080
	v_lshl_add_u64 v[208:209], v[210:211], 0, s[22:23]
	s_addc_u32 s41, s41, 0
	s_add_i32 s42, s63, s47
	global_load_lds_dwordx4 v[208:209], off
	v_lshl_add_u64 v[208:209], s[40:41], 0, v[164:165]
	s_mov_b32 m0, s42
	s_nop 0
	global_load_lds_dwordx4 v[208:209], off
	v_lshl_add_u64 v[208:209], s[40:41], 0, v[168:169]
	s_add_i32 m0, s42, 0x2000
	s_nop 0
	global_load_lds_dwordx4 v[208:209], off
	v_lshl_add_u64 v[208:209], v[212:213], 0, s[22:23]
	s_mov_b32 m0, s53
	s_nop 0
	global_load_lds_dwordx4 v[208:209], off
	v_lshl_add_u64 v[208:209], v[214:215], 0, s[22:23]
	s_mov_b32 m0, s54
	s_nop 0
	global_load_lds_dwordx4 v[208:209], off
	s_waitcnt vmcnt(8)
	s_waitcnt lgkmcnt(0)
	s_barrier
	s_setprio 1
	s_waitcnt lgkmcnt(0)
	v_mfma_i32_16x16x64_i8 v[62:65], v[66:69], v[176:179], v[62:65]
	v_mfma_i32_16x16x64_i8 v[58:61], v[82:85], v[176:179], v[58:61]
	v_mfma_i32_16x16x64_i8 v[46:49], v[66:69], v[184:187], v[46:49]
	v_mfma_i32_16x16x64_i8 v[42:45], v[82:85], v[184:187], v[42:45]
	v_mfma_i32_16x16x64_i8 v[30:33], v[66:69], v[192:195], v[30:33]
	v_mfma_i32_16x16x64_i8 v[26:29], v[82:85], v[192:195], v[26:29]
	v_mfma_i32_16x16x64_i8 v[14:17], v[66:69], v[200:203], v[14:17]
	v_mfma_i32_16x16x64_i8 v[10:13], v[82:85], v[200:203], v[10:13]
	v_mfma_i32_16x16x64_i8 v[62:65], v[70:73], v[180:183], v[62:65]
	v_mfma_i32_16x16x64_i8 v[58:61], v[86:89], v[180:183], v[58:61]
	v_mfma_i32_16x16x64_i8 v[46:49], v[70:73], v[188:191], v[46:49]
	v_mfma_i32_16x16x64_i8 v[42:45], v[86:89], v[188:191], v[42:45]
	v_mfma_i32_16x16x64_i8 v[30:33], v[70:73], v[196:199], v[30:33]
	v_mfma_i32_16x16x64_i8 v[26:29], v[86:89], v[196:199], v[26:29]
	v_mfma_i32_16x16x64_i8 v[14:17], v[70:73], v[204:207], v[14:17]
	v_mfma_i32_16x16x64_i8 v[10:13], v[86:89], v[204:207], v[10:13]
	v_mfma_i32_16x16x64_i8 v[54:57], v[90:93], v[176:179], v[54:57]
	v_mfma_i32_16x16x64_i8 v[50:53], v[98:101], v[176:179], v[50:53]
	v_mfma_i32_16x16x64_i8 v[38:41], v[90:93], v[184:187], v[38:41]
	v_mfma_i32_16x16x64_i8 v[34:37], v[98:101], v[184:187], v[34:37]
	v_mfma_i32_16x16x64_i8 v[22:25], v[90:93], v[192:195], v[22:25]
	v_mfma_i32_16x16x64_i8 v[18:21], v[98:101], v[192:195], v[18:21]
	v_mfma_i32_16x16x64_i8 v[6:9], v[90:93], v[200:203], v[6:9]
	v_mfma_i32_16x16x64_i8 v[2:5], v[98:101], v[200:203], v[2:5]
	v_mfma_i32_16x16x64_i8 v[54:57], v[94:97], v[180:183], v[54:57]
	v_mfma_i32_16x16x64_i8 v[50:53], v[102:105], v[180:183], v[50:53]
	v_mfma_i32_16x16x64_i8 v[38:41], v[94:97], v[188:191], v[38:41]
	v_mfma_i32_16x16x64_i8 v[34:37], v[102:105], v[188:191], v[34:37]
	v_mfma_i32_16x16x64_i8 v[22:25], v[94:97], v[196:199], v[22:25]
	v_mfma_i32_16x16x64_i8 v[18:21], v[102:105], v[196:199], v[18:21]
	v_mfma_i32_16x16x64_i8 v[6:9], v[94:97], v[204:207], v[6:9]
	v_mfma_i32_16x16x64_i8 v[2:5], v[102:105], v[204:207], v[2:5]
	s_setprio 0
	s_barrier
	s_add_i32 s61, s61, 2
	s_add_u32 s0, s0, 0x100
	s_addc_u32 s1, s1, 0
	s_add_u32 s31, s31, 0x100
	s_addc_u32 s39, s39, 0
	s_cmp_gt_u32 s61, 13
	s_cbranch_scc0 .LBB0_1367
	s_branch .Lkexit_1367
	s_nop 0
	s_nop 0
	s_nop 0
	s_nop 0
	s_nop 0
	s_nop 0
	s_nop 0
	s_nop 0
	s_nop 0
	s_nop 0
	s_nop 0
	s_nop 0
	s_nop 0
	s_nop 0
	s_nop 0
	s_nop 0
	s_nop 0
	s_nop 0
	s_nop 0
	s_nop 0
	s_nop 0
.LBB0_1367:
	ds_read_b128 v[66:69], v229
	ds_read_b128 v[70:73], v229 offset:1024
	ds_read_b128 v[82:85], v229 offset:2048
	ds_read_b128 v[86:89], v229 offset:3072
	ds_read_b128 v[90:93], v230
	ds_read_b128 v[94:97], v230 offset:1024
	ds_read_b128 v[98:101], v230 offset:2048
	ds_read_b128 v[102:105], v230 offset:3072
	s_add_u32 s40, s0, 0xfffc0080
	s_addc_u32 s41, s1, -1
	s_cmp_eq_u32 s61, 12
	s_cselect_b32 s43, s27, s41
	s_cselect_b32 s42, s29, s40
	s_cselect_b32 s41, s35, s39
	s_cselect_b32 s40, s34, s31
	v_lshl_add_u64 v[208:209], s[0:1], 0, v[170:171]
	s_add_i32 m0, s15, 0xc000
	ds_read_b128 v[176:179], v231
	ds_read_b128 v[180:183], v231 offset:1024
	ds_read_b128 v[184:187], v231 offset:2048
	ds_read_b128 v[188:191], v231 offset:3072
	ds_read_b128 v[192:195], v231 offset:4096
	ds_read_b128 v[196:199], v231 offset:5120
	ds_read_b128 v[200:203], v231 offset:6144
	ds_read_b128 v[204:207], v231 offset:7168
	global_load_lds_dwordx4 v[208:209], off
	v_lshl_add_u64 v[208:209], s[0:1], 0, v[172:173]
	s_add_i32 m0, s15, 0xe000
	s_nop 0
	global_load_lds_dwordx4 v[208:209], off
	s_waitcnt vmcnt(8)
	s_waitcnt lgkmcnt(0)
	s_barrier
	s_setprio 1
	s_waitcnt lgkmcnt(0)
	v_mfma_i32_16x16x64_i8 v[158:161], v[66:69], v[176:179], v[158:161]
	v_mfma_i32_16x16x64_i8 v[154:157], v[82:85], v[176:179], v[154:157]
	v_mfma_i32_16x16x64_i8 v[142:145], v[66:69], v[184:187], v[142:145]
	v_mfma_i32_16x16x64_i8 v[138:141], v[82:85], v[184:187], v[138:141]
	v_mfma_i32_16x16x64_i8 v[126:129], v[66:69], v[192:195], v[126:129]
	v_mfma_i32_16x16x64_i8 v[122:125], v[82:85], v[192:195], v[122:125]
	v_mfma_i32_16x16x64_i8 v[110:113], v[66:69], v[200:203], v[110:113]
	v_mfma_i32_16x16x64_i8 v[106:109], v[82:85], v[200:203], v[106:109]
	v_mfma_i32_16x16x64_i8 v[158:161], v[70:73], v[180:183], v[158:161]
	v_mfma_i32_16x16x64_i8 v[154:157], v[86:89], v[180:183], v[154:157]
	v_mfma_i32_16x16x64_i8 v[142:145], v[70:73], v[188:191], v[142:145]
	v_mfma_i32_16x16x64_i8 v[138:141], v[86:89], v[188:191], v[138:141]
	v_mfma_i32_16x16x64_i8 v[126:129], v[70:73], v[196:199], v[126:129]
	v_mfma_i32_16x16x64_i8 v[122:125], v[86:89], v[196:199], v[122:125]
	v_mfma_i32_16x16x64_i8 v[110:113], v[70:73], v[204:207], v[110:113]
	v_mfma_i32_16x16x64_i8 v[106:109], v[86:89], v[204:207], v[106:109]
	v_mfma_i32_16x16x64_i8 v[150:153], v[90:93], v[176:179], v[150:153]
	v_mfma_i32_16x16x64_i8 v[146:149], v[98:101], v[176:179], v[146:149]
	v_mfma_i32_16x16x64_i8 v[134:137], v[90:93], v[184:187], v[134:137]
	v_mfma_i32_16x16x64_i8 v[130:133], v[98:101], v[184:187], v[130:133]
	v_mfma_i32_16x16x64_i8 v[118:121], v[90:93], v[192:195], v[118:121]
	v_mfma_i32_16x16x64_i8 v[114:117], v[98:101], v[192:195], v[114:117]
	v_mfma_i32_16x16x64_i8 v[78:81], v[90:93], v[200:203], v[78:81]
	v_mfma_i32_16x16x64_i8 v[74:77], v[98:101], v[200:203], v[74:77]
	v_mfma_i32_16x16x64_i8 v[150:153], v[94:97], v[180:183], v[150:153]
	v_mfma_i32_16x16x64_i8 v[146:149], v[102:105], v[180:183], v[146:149]
	v_mfma_i32_16x16x64_i8 v[134:137], v[94:97], v[188:191], v[134:137]
	v_mfma_i32_16x16x64_i8 v[130:133], v[102:105], v[188:191], v[130:133]
	v_mfma_i32_16x16x64_i8 v[118:121], v[94:97], v[196:199], v[118:121]
	v_mfma_i32_16x16x64_i8 v[114:117], v[102:105], v[196:199], v[114:117]
	v_mfma_i32_16x16x64_i8 v[78:81], v[94:97], v[204:207], v[78:81]
	v_mfma_i32_16x16x64_i8 v[74:77], v[102:105], v[204:207], v[74:77]
	s_setprio 0
	s_barrier
	s_add_i32 s62, s57, s47
	v_lshl_add_u64 v[208:209], s[40:41], 0, v[164:165]
	s_mov_b32 m0, s62
	ds_read_b128 v[176:179], v231 offset:16384
	ds_read_b128 v[180:183], v231 offset:17408
	ds_read_b128 v[184:187], v231 offset:18432
	ds_read_b128 v[188:191], v231 offset:19456
	ds_read_b128 v[192:195], v231 offset:20480
	ds_read_b128 v[196:199], v231 offset:21504
	ds_read_b128 v[200:203], v231 offset:22528
	ds_read_b128 v[204:207], v231 offset:23552
	global_load_lds_dwordx4 v[208:209], off
	s_add_i32 m0, s62, 0x2000
	s_add_u32 s62, s40, 0x40000
	v_lshl_add_u64 v[210:211], s[40:41], 0, v[168:169]
	s_addc_u32 s63, s41, 0
	s_add_i32 s64, s58, s47
	global_load_lds_dwordx4 v[210:211], off
	v_lshl_add_u64 v[212:213], s[62:63], 0, v[164:165]
	s_mov_b32 m0, s64
	v_lshl_add_u64 v[214:215], s[42:43], 0, v[166:167]
	global_load_lds_dwordx4 v[212:213], off
	v_lshl_add_u64 v[212:213], s[62:63], 0, v[168:169]
	s_add_i32 m0, s64, 0x2000
	s_nop 0
	global_load_lds_dwordx4 v[212:213], off
	v_lshl_add_u64 v[212:213], s[42:43], 0, v[162:163]
	s_mov_b32 m0, s15
	s_nop 0
	global_load_lds_dwordx4 v[212:213], off
	s_mov_b32 m0, s48
	s_nop 0
	global_load_lds_dwordx4 v[214:215], off
	s_waitcnt vmcnt(8)
	s_waitcnt lgkmcnt(0)
	s_barrier
	s_setprio 1
	s_waitcnt lgkmcnt(0)
	v_mfma_i32_16x16x64_i8 v[62:65], v[66:69], v[176:179], v[62:65]
	v_mfma_i32_16x16x64_i8 v[58:61], v[82:85], v[176:179], v[58:61]
	v_mfma_i32_16x16x64_i8 v[46:49], v[66:69], v[184:187], v[46:49]
	v_mfma_i32_16x16x64_i8 v[42:45], v[82:85], v[184:187], v[42:45]
	v_mfma_i32_16x16x64_i8 v[30:33], v[66:69], v[192:195], v[30:33]
	v_mfma_i32_16x16x64_i8 v[26:29], v[82:85], v[192:195], v[26:29]
	v_mfma_i32_16x16x64_i8 v[14:17], v[66:69], v[200:203], v[14:17]
	v_mfma_i32_16x16x64_i8 v[10:13], v[82:85], v[200:203], v[10:13]
	v_mfma_i32_16x16x64_i8 v[62:65], v[70:73], v[180:183], v[62:65]
	v_mfma_i32_16x16x64_i8 v[58:61], v[86:89], v[180:183], v[58:61]
	v_mfma_i32_16x16x64_i8 v[46:49], v[70:73], v[188:191], v[46:49]
	v_mfma_i32_16x16x64_i8 v[42:45], v[86:89], v[188:191], v[42:45]
	v_mfma_i32_16x16x64_i8 v[30:33], v[70:73], v[196:199], v[30:33]
	v_mfma_i32_16x16x64_i8 v[26:29], v[86:89], v[196:199], v[26:29]
	v_mfma_i32_16x16x64_i8 v[14:17], v[70:73], v[204:207], v[14:17]
	v_mfma_i32_16x16x64_i8 v[10:13], v[86:89], v[204:207], v[10:13]
	v_mfma_i32_16x16x64_i8 v[54:57], v[90:93], v[176:179], v[54:57]
	v_mfma_i32_16x16x64_i8 v[50:53], v[98:101], v[176:179], v[50:53]
	v_mfma_i32_16x16x64_i8 v[38:41], v[90:93], v[184:187], v[38:41]
	v_mfma_i32_16x16x64_i8 v[34:37], v[98:101], v[184:187], v[34:37]
	v_mfma_i32_16x16x64_i8 v[22:25], v[90:93], v[192:195], v[22:25]
	v_mfma_i32_16x16x64_i8 v[18:21], v[98:101], v[192:195], v[18:21]
	v_mfma_i32_16x16x64_i8 v[6:9], v[90:93], v[200:203], v[6:9]
	v_mfma_i32_16x16x64_i8 v[2:5], v[98:101], v[200:203], v[2:5]
	v_mfma_i32_16x16x64_i8 v[54:57], v[94:97], v[180:183], v[54:57]
	v_mfma_i32_16x16x64_i8 v[50:53], v[102:105], v[180:183], v[50:53]
	v_mfma_i32_16x16x64_i8 v[38:41], v[94:97], v[188:191], v[38:41]
	v_mfma_i32_16x16x64_i8 v[34:37], v[102:105], v[188:191], v[34:37]
	v_mfma_i32_16x16x64_i8 v[22:25], v[94:97], v[196:199], v[22:25]
	v_mfma_i32_16x16x64_i8 v[18:21], v[102:105], v[196:199], v[18:21]
	v_mfma_i32_16x16x64_i8 v[6:9], v[94:97], v[204:207], v[6:9]
	v_mfma_i32_16x16x64_i8 v[2:5], v[102:105], v[204:207], v[2:5]
	s_setprio 0
	s_barrier
	s_add_i32 s62, 0, 0x18000
	v_add_u32_e32 v0, s62, v227
	s_add_i32 s63, 0, 0x1c000
	ds_read_b128 v[66:69], v0
	ds_read_b128 v[70:73], v0 offset:1024
	ds_read_b128 v[82:85], v0 offset:2048
	ds_read_b128 v[86:89], v0 offset:3072
	v_add_u32_e32 v0, s63, v227
	ds_read_b128 v[90:93], v0
	ds_read_b128 v[94:97], v0 offset:1024
	ds_read_b128 v[98:101], v0 offset:2048
	ds_read_b128 v[102:105], v0 offset:3072
	s_add_u32 s42, s42, 0x40000
	s_addc_u32 s43, s43, 0
	s_mov_b32 m0, s49
	v_lshl_add_u64 v[216:217], s[42:43], 0, v[162:163]
	ds_read_b128 v[176:179], v231 offset:32768
	ds_read_b128 v[180:183], v231 offset:33792
	ds_read_b128 v[184:187], v231 offset:34816
	ds_read_b128 v[188:191], v231 offset:35840
	ds_read_b128 v[192:195], v231 offset:36864
	ds_read_b128 v[196:199], v231 offset:37888
	ds_read_b128 v[200:203], v231 offset:38912
	ds_read_b128 v[204:207], v231 offset:39936
	global_load_lds_dwordx4 v[216:217], off
	v_lshl_add_u64 v[216:217], s[42:43], 0, v[166:167]
	s_mov_b32 m0, s51
	s_nop 0
	global_load_lds_dwordx4 v[216:217], off
	s_waitcnt vmcnt(8)
	s_waitcnt lgkmcnt(0)
	s_barrier
	s_setprio 1
	s_waitcnt lgkmcnt(0)
	v_mfma_i32_16x16x64_i8 v[158:161], v[66:69], v[176:179], v[158:161]
	v_mfma_i32_16x16x64_i8 v[154:157], v[82:85], v[176:179], v[154:157]
	v_mfma_i32_16x16x64_i8 v[142:145], v[66:69], v[184:187], v[142:145]
	v_mfma_i32_16x16x64_i8 v[138:141], v[82:85], v[184:187], v[138:141]
	v_mfma_i32_16x16x64_i8 v[126:129], v[66:69], v[192:195], v[126:129]
	v_mfma_i32_16x16x64_i8 v[122:125], v[82:85], v[192:195], v[122:125]
	v_mfma_i32_16x16x64_i8 v[110:113], v[66:69], v[200:203], v[110:113]
	v_mfma_i32_16x16x64_i8 v[106:109], v[82:85], v[200:203], v[106:109]
	v_mfma_i32_16x16x64_i8 v[158:161], v[70:73], v[180:183], v[158:161]
	v_mfma_i32_16x16x64_i8 v[154:157], v[86:89], v[180:183], v[154:157]
	v_mfma_i32_16x16x64_i8 v[142:145], v[70:73], v[188:191], v[142:145]
	v_mfma_i32_16x16x64_i8 v[138:141], v[86:89], v[188:191], v[138:141]
	v_mfma_i32_16x16x64_i8 v[126:129], v[70:73], v[196:199], v[126:129]
	v_mfma_i32_16x16x64_i8 v[122:125], v[86:89], v[196:199], v[122:125]
	v_mfma_i32_16x16x64_i8 v[110:113], v[70:73], v[204:207], v[110:113]
	v_mfma_i32_16x16x64_i8 v[106:109], v[86:89], v[204:207], v[106:109]
	v_mfma_i32_16x16x64_i8 v[150:153], v[90:93], v[176:179], v[150:153]
	v_mfma_i32_16x16x64_i8 v[146:149], v[98:101], v[176:179], v[146:149]
	v_mfma_i32_16x16x64_i8 v[134:137], v[90:93], v[184:187], v[134:137]
	v_mfma_i32_16x16x64_i8 v[130:133], v[98:101], v[184:187], v[130:133]
	v_mfma_i32_16x16x64_i8 v[118:121], v[90:93], v[192:195], v[118:121]
	v_mfma_i32_16x16x64_i8 v[114:117], v[98:101], v[192:195], v[114:117]
	v_mfma_i32_16x16x64_i8 v[78:81], v[90:93], v[200:203], v[78:81]
	v_mfma_i32_16x16x64_i8 v[74:77], v[98:101], v[200:203], v[74:77]
	v_mfma_i32_16x16x64_i8 v[150:153], v[94:97], v[180:183], v[150:153]
	v_mfma_i32_16x16x64_i8 v[146:149], v[102:105], v[180:183], v[146:149]
	v_mfma_i32_16x16x64_i8 v[134:137], v[94:97], v[188:191], v[134:137]
	v_mfma_i32_16x16x64_i8 v[130:133], v[102:105], v[188:191], v[130:133]
	v_mfma_i32_16x16x64_i8 v[118:121], v[94:97], v[196:199], v[118:121]
	v_mfma_i32_16x16x64_i8 v[114:117], v[102:105], v[196:199], v[114:117]
	v_mfma_i32_16x16x64_i8 v[78:81], v[94:97], v[204:207], v[78:81]
	v_mfma_i32_16x16x64_i8 v[74:77], v[102:105], v[204:207], v[74:77]
	s_setprio 0
	s_barrier
	s_add_i32 s42, s62, s47
	v_lshl_add_u64 v[208:209], v[208:209], 0, s[22:23]
	s_mov_b32 m0, s42
	ds_read_b128 v[176:179], v231 offset:49152
	ds_read_b128 v[180:183], v231 offset:50176
	ds_read_b128 v[184:187], v231 offset:51200
	ds_read_b128 v[188:191], v231 offset:52224
	ds_read_b128 v[192:195], v231 offset:53248
	ds_read_b128 v[196:199], v231 offset:54272
	ds_read_b128 v[200:203], v231 offset:55296
	ds_read_b128 v[204:207], v231 offset:56320
	global_load_lds_dwordx4 v[208:209], off
	s_add_i32 m0, s42, 0x2000
	s_add_u32 s40, s40, 0x40080
	v_lshl_add_u64 v[208:209], v[210:211], 0, s[22:23]
	s_addc_u32 s41, s41, 0
	s_add_i32 s42, s63, s47
	global_load_lds_dwordx4 v[208:209], off
	v_lshl_add_u64 v[208:209], s[40:41], 0, v[164:165]
	s_mov_b32 m0, s42
	s_nop 0
	global_load_lds_dwordx4 v[208:209], off
	v_lshl_add_u64 v[208:209], s[40:41], 0, v[168:169]
	s_add_i32 m0, s42, 0x2000
	s_nop 0
	global_load_lds_dwordx4 v[208:209], off
	v_lshl_add_u64 v[208:209], v[212:213], 0, s[22:23]
	s_mov_b32 m0, s53
	s_nop 0
	global_load_lds_dwordx4 v[208:209], off
	v_lshl_add_u64 v[208:209], v[214:215], 0, s[22:23]
	s_mov_b32 m0, s54
	s_nop 0
	global_load_lds_dwordx4 v[208:209], off
	s_waitcnt vmcnt(8)
	s_waitcnt lgkmcnt(0)
	s_barrier
	s_setprio 1
	s_waitcnt lgkmcnt(0)
	v_mfma_i32_16x16x64_i8 v[62:65], v[66:69], v[176:179], v[62:65]
	v_mfma_i32_16x16x64_i8 v[58:61], v[82:85], v[176:179], v[58:61]
	v_mfma_i32_16x16x64_i8 v[46:49], v[66:69], v[184:187], v[46:49]
	v_mfma_i32_16x16x64_i8 v[42:45], v[82:85], v[184:187], v[42:45]
	v_mfma_i32_16x16x64_i8 v[30:33], v[66:69], v[192:195], v[30:33]
	v_mfma_i32_16x16x64_i8 v[26:29], v[82:85], v[192:195], v[26:29]
	v_mfma_i32_16x16x64_i8 v[14:17], v[66:69], v[200:203], v[14:17]
	v_mfma_i32_16x16x64_i8 v[10:13], v[82:85], v[200:203], v[10:13]
	v_mfma_i32_16x16x64_i8 v[62:65], v[70:73], v[180:183], v[62:65]
	v_mfma_i32_16x16x64_i8 v[58:61], v[86:89], v[180:183], v[58:61]
	v_mfma_i32_16x16x64_i8 v[46:49], v[70:73], v[188:191], v[46:49]
	v_mfma_i32_16x16x64_i8 v[42:45], v[86:89], v[188:191], v[42:45]
	v_mfma_i32_16x16x64_i8 v[30:33], v[70:73], v[196:199], v[30:33]
	v_mfma_i32_16x16x64_i8 v[26:29], v[86:89], v[196:199], v[26:29]
	v_mfma_i32_16x16x64_i8 v[14:17], v[70:73], v[204:207], v[14:17]
	v_mfma_i32_16x16x64_i8 v[10:13], v[86:89], v[204:207], v[10:13]
	v_mfma_i32_16x16x64_i8 v[54:57], v[90:93], v[176:179], v[54:57]
	v_mfma_i32_16x16x64_i8 v[50:53], v[98:101], v[176:179], v[50:53]
	v_mfma_i32_16x16x64_i8 v[38:41], v[90:93], v[184:187], v[38:41]
	v_mfma_i32_16x16x64_i8 v[34:37], v[98:101], v[184:187], v[34:37]
	v_mfma_i32_16x16x64_i8 v[22:25], v[90:93], v[192:195], v[22:25]
	v_mfma_i32_16x16x64_i8 v[18:21], v[98:101], v[192:195], v[18:21]
	v_mfma_i32_16x16x64_i8 v[6:9], v[90:93], v[200:203], v[6:9]
	v_mfma_i32_16x16x64_i8 v[2:5], v[98:101], v[200:203], v[2:5]
	v_mfma_i32_16x16x64_i8 v[54:57], v[94:97], v[180:183], v[54:57]
	v_mfma_i32_16x16x64_i8 v[50:53], v[102:105], v[180:183], v[50:53]
	v_mfma_i32_16x16x64_i8 v[38:41], v[94:97], v[188:191], v[38:41]
	v_mfma_i32_16x16x64_i8 v[34:37], v[102:105], v[188:191], v[34:37]
	v_mfma_i32_16x16x64_i8 v[22:25], v[94:97], v[196:199], v[22:25]
	v_mfma_i32_16x16x64_i8 v[18:21], v[102:105], v[196:199], v[18:21]
	v_mfma_i32_16x16x64_i8 v[6:9], v[94:97], v[204:207], v[6:9]
	v_mfma_i32_16x16x64_i8 v[2:5], v[102:105], v[204:207], v[2:5]
	s_setprio 0
	s_barrier
	s_add_i32 s61, s61, 2
	s_add_u32 s0, s0, 0x100
	s_addc_u32 s1, s1, 0
	s_add_u32 s31, s31, 0x100
	s_addc_u32 s39, s39, 0
	s_cmp_gt_u32 s61, 13
	s_cbranch_scc0 .LBB0_1367

.LBB0_1406:
	s_waitcnt vmcnt(0)
	s_barrier
	s_mov_b64 s[0:1], exec
	v_readlane_b32 s2, v252, 11
	v_readlane_b32 s3, v252, 12
	s_and_b64 s[2:3], s[0:1], s[2:3]
	s_mov_b64 exec, s[2:3]
	s_cbranch_execz .LBB0_1458
	s_add_i32 s2, 0, 0x26f20
	v_mov_b32_e32 v0, s2
	s_waitcnt vmcnt(0) expcnt(0) lgkmcnt(0)
	ds_read_b32 v3, v0
	s_add_i32 s2, 0, 0x26f24
	v_mov_b32_e32 v0, s2
	ds_read_b32 v1, v0
	s_waitcnt lgkmcnt(1)
	v_cmp_ne_u32_e32 vcc, 0, v3
	s_cbranch_vccnz .LBB0_1422
	v_readlane_b32 s2, v252, 4
	v_readlane_b32 s3, v252, 5
	s_load_dwordx2 s[6:7], s[2:3], 0x4
	v_readlane_b32 s40, v252, 2
	v_readlane_b32 s41, v252, 3
	s_add_u32 s2, s40, 0x4200
	s_addc_u32 s3, s41, 0
	s_add_u32 s4, s40, 0x4400
	s_addc_u32 s5, s41, 0
	v_readlane_b32 s10, v252, 6
	s_waitcnt lgkmcnt(0)
	s_mul_i32 s33, s6, s10
	s_add_u32 s6, s40, 0x4500
	s_mul_i32 s33, s33, s7
	s_addc_u32 s7, s41, 0
	v_readlane_b32 s11, v252, 7
	s_add_u32 s10, s40, 0x4600
	s_addc_u32 s11, s41, 0
	s_add_u32 s14, s40, 0x4700
	s_addc_u32 s15, s41, 0
	s_add_u32 s16, s40, 0x4800
	s_addc_u32 s17, s41, 0
	s_add_u32 s18, s40, 0x4900
	s_addc_u32 s19, s41, 0
	s_add_u32 s20, s40, 0x4a00
	s_addc_u32 s21, s41, 0
	s_add_u32 s22, s40, 0x4b00
	s_addc_u32 s23, s41, 0
	s_add_u32 s24, s40, 0x4c00
	s_addc_u32 s25, s41, 0
	s_add_u32 s26, s40, 0x4d00
	s_addc_u32 s27, s41, 0
	s_add_u32 s28, s40, 0x4e00
	s_addc_u32 s29, s41, 0
	s_add_u32 s30, s40, 0x4f00
	s_addc_u32 s31, s41, 0
	s_add_u32 s34, s40, 0x5000
	s_addc_u32 s35, s41, 0
	s_add_u32 s36, s40, 0x5100
	s_addc_u32 s37, s41, 0
	s_add_u32 s38, s40, 0x5200
	s_addc_u32 s39, s41, 0
	s_add_u32 s40, s40, 0x5300
	s_addc_u32 s41, s41, 0
	s_mov_b32 s48, 1
	v_mov_b32_e32 v17, 0
	s_branch .LBB0_1410
	s_nop 0
	s_nop 0
	s_nop 0
	s_nop 0
	s_nop 0
	s_nop 0
	s_nop 0
	s_nop 0
	s_nop 0
	s_nop 0
	s_nop 0
	s_nop 0
	s_nop 0
	s_nop 0
	s_nop 0
	s_nop 0
	s_nop 0
	s_nop 0
	s_nop 0
	s_nop 0
	s_nop 0
	s_nop 0
	s_nop 0
	s_nop 0
	s_nop 0
	s_nop 0
	s_nop 0
	s_nop 0
	s_nop 0
	s_nop 0
	s_nop 0
	s_nop 0
	s_nop 0
	s_nop 0
	s_nop 0
	s_nop 0
	s_nop 0
	s_nop 0
	s_nop 0
	s_nop 0
	s_nop 0
	s_nop 0
	s_nop 0
	s_nop 0
	s_nop 0
	s_nop 0
	s_nop 0
	s_nop 0
	s_nop 0
	s_nop 0
	s_nop 0
	s_nop 0
	s_nop 0
	s_nop 0
	s_nop 0
	s_nop 0
	s_nop 0
	s_nop 0
	s_nop 0
	s_nop 0
	s_nop 0
	s_nop 0
	s_nop 0
	s_nop 0
	s_nop 0
	s_nop 0
	s_nop 0
	s_nop 0
	s_nop 0
	s_nop 0
	s_nop 0
	s_nop 0
